# combined edits + first K-fragment LDS reads issued before the conversion issue block at loop top + flat memory ops of LN/combine phases converted to global
# speedup vs baseline: 1.0041x; 1.0041x over previous
; DEVI int vtid() { return tidx() & 255; }
; DEVI int vbid() { return bidx() * 2 + vhb(); }
; DEVI int vgrid() { return (int)gridDim.x * 2; }
; DEVI void row_stats(const f32x4 (&v)[4], float& mu, float& rstd) {
;     float s = 0.f;
; #pragma unroll
;     for (int i = 0; i < 4; ++i) s += (v[i][0] + v[i][1]) + (v[i][2] + v[i][3]);
;     mu = wave_sum(s) * (1.f / 1024.f);
;     float q = 0.f;
; #pragma unroll
;     for (int i = 0; i < 4; ++i)
; #pragma unroll
;         for (int j = 0; j < 4; ++j) { const float d = v[i][j] - mu; q += d * d; }
;     rstd = rsqrtf(wave_sum(q) * (1.f / 1024.f) + LN_EPS);
; DEVI void phase_ln_first(const Params& p) {
;     const int lane = vtid() & 63, gw = vbid() * 4 + (vtid() >> 6), nw = vgrid() * 4;
;     const float* xin = p.x; bf16_t* hb = p.h; asm volatile("" : "+s"(xin), "+s"(hb));
;     f32x4 sh4[4], sc4[4]; int bcur = -1;
; #pragma unroll
;     for (int i = 0; i < 4; ++i) { sh4[i] = (f32x4){0.f, 0.f, 0.f, 0.f}; sc4[i] = sh4[i]; }
;     f32x4 v[4], vn[4];
; #pragma unroll
;     for (int i = 0; i < 4; ++i) v[i] = *(const f32x4*)(xin + (size_t)(gw < T_ ? gw : 0) * 1024 + lane * 4 + 256 * i);
;     for (int t = gw; t < T_; t += nw) {
;         const int b = t >> 12; const int tn = t + nw < T_ ? t + nw : t;
; #pragma unroll
;         for (int i = 0; i < 4; ++i) vn[i] = *(const f32x4*)(xin + (size_t)tn * 1024 + lane * 4 + 256 * i);
.LBB0_168:
	s_or_b64 exec, exec, s[4:5]
	s_mov_b64 s[6:7], s[0:1]
	s_waitcnt lgkmcnt(0)
	s_barrier
	v_mov_b32_e32 v1, v0
	s_mov_b32 s2, s84
	v_mov_b32_e32 v3, v0
	v_mov_b32_e32 v2, v0
	s_load_dwordx2 s[4:5], s[6:7], 0x0
	s_load_dwordx2 s[14:15], s[6:7], 0x160
	v_readfirstlane_b32 s8, v3
	s_lshr_b32 s8, s8, 6
	s_and_b32 s8, s8, 0x3fffffc
	s_lshl_b32 s2, s2, 3
	s_add_i32 s8, s8, s2
	s_lshl_b32 s86, s33, 3
	s_cmpk_gt_u32 s8, 0x7fff
	s_movk_i32 s2, 0x7fff
	s_waitcnt lgkmcnt(0)
	s_cbranch_scc1 .LBB0_174
	v_lshrrev_b32_e32 v2, 6, v2
	v_lshlrev_b32_e32 v3, 2, v1
	v_and_or_b32 v68, v2, 3, s8
	v_and_b32_e32 v50, 0xfc, v3
	v_mov_b32_e32 v67, 0
	v_lshlrev_b32_e32 v66, 12, v68
	v_lshl_add_u64 v[2:3], s[4:5], 0, v[66:67]
	v_lshlrev_b32_e32 v66, 2, v50
	v_lshl_add_u64 v[10:11], v[2:3], 0, v[66:67]
	global_load_dwordx4 v[14:17], v[10:11], off
	global_load_dwordx4 v[6:9], v[10:11], off offset:1024
	global_load_dwordx4 v[2:5], v[10:11], off offset:2048
	global_load_dwordx4 v[46:49], v[10:11], off offset:3072
	v_mov_b32_e32 v69, v67
	v_and_b32_e32 v33, 63, v1
	v_mov_b32_e32 v12, v67
	v_mov_b32_e32 v13, v67
	v_lshlrev_b64 v[52:53], 11, v[68:69]
	s_ashr_i32 s87, s86, 31
	v_mov_b32_e32 v10, v67
	v_mov_b32_e32 v11, v67
	v_mov_b64_e32 v[36:37], v[12:13]
	v_mov_b64_e32 v[40:41], v[12:13]
	v_mov_b64_e32 v[44:45], v[12:13]
	v_lshl_or_b32 v52, v33, 3, v52
	v_mov_b32_e32 v76, -1
	s_mov_b64 s[8:9], 0
	s_mov_b32 s16, 0x8000
	s_mov_b64 s[10:11], 0x1000
	v_mov_b32_e32 v1, 0x3727c5ac
	s_mov_b32 s17, 0x800000
	s_lshl_b64 s[12:13], s[86:87], 11
	v_mov_b32_e32 v18, v67
	v_mov_b32_e32 v19, v67
	v_mov_b32_e32 v20, v67
	v_mov_b32_e32 v21, v67
	v_mov_b32_e32 v22, v67
	v_mov_b32_e32 v23, v67
	v_mov_b32_e32 v24, v67
	v_mov_b32_e32 v25, v67
	v_mov_b32_e32 v26, v67
	v_mov_b32_e32 v27, v67
	v_mov_b32_e32 v28, v67
	v_mov_b32_e32 v29, v67
	v_mov_b32_e32 v30, v67
	v_mov_b32_e32 v31, v67
	v_mov_b32_e32 v32, v67
	v_mov_b64_e32 v[34:35], v[10:11]
	v_mov_b64_e32 v[38:39], v[10:11]
	v_mov_b64_e32 v[42:43], v[10:11]
	v_lshl_add_u64 v[70:71], s[4:5], 0, v[66:67]
	v_lshl_add_u64 v[72:73], s[14:15], 0, v[52:53]
	v_lshlrev_b32_e32 v66, 2, v50
	v_mov_b32_e32 v33, v67
	s_waitcnt vmcnt(0) lgkmcnt(0)
	v_mov_b32_e32 v74, v15
	v_mov_b32_e32 v75, v16
	v_mov_b32_e32 v15, v17
	v_mov_b32_e32 v16, v7
	v_mov_b32_e32 v17, v8
	v_mov_b32_e32 v7, v9
	s_branch .LBB0_171
.LBB0_170:
	s_or_b64 exec, exec, s[14:15]
	v_pk_add_f32 v[8:9], v[74:75], v[14:15]
	v_pk_add_f32 v[78:79], v[16:17], v[6:7]
	v_add_f32_e32 v8, v8, v9
	v_pk_add_f32 v[78:79], v[78:79], v[78:79] op_sel_hi:[0,1]
	v_add_f32_e32 v9, 0, v8
	v_add_f32_e32 v81, v2, v3
	v_add_f32_e32 v83, v4, v5
	v_mov_b32_e32 v80, v46
	v_mov_b32_e32 v82, v47
	v_mov_b32_e32 v78, v48
	v_mov_b32_e32 v8, v49
	v_pk_add_f32 v[80:81], v[80:81], v[82:83]
	v_pk_add_f32 v[8:9], v[78:79], v[8:9]
	s_and_b64 s[4:5], exec, s[4:5]
	v_pk_add_f32 v[8:9], v[80:81], v[8:9]
	s_or_b64 s[8:9], s[4:5], s[8:9]
	v_add_f32_e32 v8, v8, v9
	s_nop 1
	v_add_f32_dpp v8, v8, v8 quad_perm:[1,0,3,2] row_mask:0xf bank_mask:0xf bound_ctrl:1
	s_nop 1
	v_add_f32_dpp v8, v8, v8 quad_perm:[2,3,0,1] row_mask:0xf bank_mask:0xf bound_ctrl:1
	s_nop 1
	v_add_f32_dpp v8, v8, v8 row_half_mirror row_mask:0xf bank_mask:0xf bound_ctrl:1
	s_nop 1
	v_add_f32_dpp v8, v8, v8 row_mirror row_mask:0xf bank_mask:0xf bound_ctrl:1
	s_nop 0
	v_readlane_b32 s18, v8, 16
	v_readlane_b32 s19, v8, 48
	v_readlane_b32 s14, v8, 0
	v_readlane_b32 s15, v8, 32
	v_mov_b32_e32 v8, s18
	v_mov_b32_e32 v9, s19
	v_pk_add_f32 v[8:9], s[14:15], v[8:9]
	s_nop 0
	v_add_f32_e32 v9, v8, v9
	v_fmac_f32_e32 v74, 0xba800000, v9
	v_fmac_f32_e32 v14, 0xba800000, v9
	v_mul_f32_e32 v69, v74, v74
	v_fmac_f32_e32 v69, v14, v14
	v_fmac_f32_e32 v75, 0xba800000, v9
	v_fmac_f32_e32 v69, v75, v75
	v_fmac_f32_e32 v15, 0xba800000, v9
	v_fmac_f32_e32 v69, v15, v15
	v_fmac_f32_e32 v6, 0xba800000, v9
	v_fmac_f32_e32 v69, v6, v6
	v_fmac_f32_e32 v16, 0xba800000, v9
	v_fmac_f32_e32 v69, v16, v16
	v_fmac_f32_e32 v17, 0xba800000, v9
	v_fmac_f32_e32 v69, v17, v17
	v_fmac_f32_e32 v7, 0xba800000, v9
	v_mul_f32_e32 v8, 0x3a800000, v9
	v_fmac_f32_e32 v69, v7, v7
	v_fmac_f32_e32 v2, 0xba800000, v9
	v_fmac_f32_e32 v69, v2, v2
	v_fmac_f32_e32 v3, 0xba800000, v9
	v_pk_add_f32 v[4:5], v[4:5], v[8:9] op_sel_hi:[1,0] neg_lo:[0,1] neg_hi:[0,1]
	v_fmac_f32_e32 v69, v3, v3
	v_pk_mul_f32 v[78:79], v[4:5], v[4:5]
	s_nop 0
	v_add_f32_e32 v9, v78, v69
	v_add_f32_e32 v9, v79, v9
	v_pk_add_f32 v[46:47], v[46:47], v[8:9] op_sel_hi:[1,0] neg_lo:[0,1] neg_hi:[0,1]
	s_nop 0
	v_pk_mul_f32 v[78:79], v[46:47], v[46:47]
	s_nop 0
	v_add_f32_e32 v9, v78, v9
	v_add_f32_e32 v69, v79, v9
	v_pk_add_f32 v[8:9], v[48:49], v[8:9] op_sel_hi:[1,0] neg_lo:[0,1] neg_hi:[0,1]
	s_nop 0
	v_pk_mul_f32 v[48:49], v[8:9], v[8:9]
	s_nop 0
	v_add_f32_e32 v48, v48, v69
	v_add_f32_e32 v48, v49, v48
	s_waitcnt vmcnt(0)
; DEVI int vtid() { return tidx() & 255; }
; DEVI int vbid() { return bidx() * 2 + vhb(); }
; DEVI int vgrid() { return (int)gridDim.x * 2; }
; DEVI unsigned cvt_pk_bf16(float lo, float hi) { unsigned r; asm volatile("v_cvt_pk_bf16_f32 %0, %1, %2" : "=v"(r) : "v"(lo), "v"(hi)); return r; }
; DEVI void write_h_reg(const f32x4 (&v)[4], const f32x4 (&sh)[4], const f32x4 (&sc)[4], bf16_t* hrow, int lane) {
;     float mu, rstd; row_stats(v, mu, rstd);
; #pragma unroll
;     for (int i = 0; i < 4; ++i) { float o[4];
; #pragma unroll
;         for (int j = 0; j < 4; ++j) o[j] = (v[i][j] - mu) * rstd * (1.f + sc[i][j]) + sh[i][j];
;         u32x2 w; w.x = cvt_pk_bf16(o[0], o[1]); w.y = cvt_pk_bf16(o[2], o[3]);
;         *(u32x2*)(hrow + lane * 4 + 256 * i) = w; }
; }
; DEVI void phase_ln_first(const Params& p) {
;     const int lane = vtid() & 63, gw = vbid() * 4 + (vtid() >> 6), nw = vgrid() * 4;
;     const float* xin = p.x; bf16_t* hb = p.h; asm volatile("" : "+s"(xin), "+s"(hb));
;     f32x4 sh4[4], sc4[4]; int bcur = -1;
; #pragma unroll
;     for (int i = 0; i < 4; ++i) { sh4[i] = (f32x4){0.f, 0.f, 0.f, 0.f}; sc4[i] = sh4[i]; }
;     f32x4 v[4], vn[4];
; #pragma unroll
;     for (int i = 0; i < 4; ++i) v[i] = *(const f32x4*)(xin + (size_t)(gw < T_ ? gw : 0) * 1024 + lane * 4 + 256 * i);
;     for (int t = gw; t < T_; t += nw) {
;         const int b = t >> 12; const int tn = t + nw < T_ ? t + nw : t;
; #pragma unroll
;         for (int i = 0; i < 4; ++i) vn[i] = *(const f32x4*)(xin + (size_t)tn * 1024 + lane * 4 + 256 * i);
;         if (b != bcur) { bcur = b; const float* ad = p.ada + (size_t)(0 * 8 + b) * 6144;
; #pragma unroll
;             for (int i = 0; i < 4; ++i) { sh4[i] = *(const f32x4*)(ad + lane * 4 + 256 * i); sc4[i] = *(const f32x4*)(ad + 1024 + lane * 4 + 256 * i); } }
;         write_h_reg(v, sh4, sc4, hb + (size_t)t * 1024, lane);
; #pragma unroll
;         for (int i = 0; i < 4; ++i) v[i] = vn[i];
	v_add_f32_e32 v69, 1.0, v11
	v_add_f32_dpp v48, v48, v48 quad_perm:[1,0,3,2] row_mask:0xf bank_mask:0xf bound_ctrl:1
	s_nop 1
	v_add_f32_dpp v48, v48, v48 quad_perm:[2,3,0,1] row_mask:0xf bank_mask:0xf bound_ctrl:1
	s_nop 1
	v_add_f32_dpp v48, v48, v48 row_half_mirror row_mask:0xf bank_mask:0xf bound_ctrl:1
	s_nop 1
	v_add_f32_dpp v48, v48, v48 row_mirror row_mask:0xf bank_mask:0xf bound_ctrl:1
	s_nop 0
	v_readlane_b32 s18, v48, 16
	v_readlane_b32 s19, v48, 48
	v_readlane_b32 s14, v48, 0
	v_readlane_b32 s15, v48, 32
	v_mov_b32_e32 v48, s18
	v_mov_b32_e32 v49, s19
	v_pk_add_f32 v[48:49], s[14:15], v[48:49]
	s_nop 0
	v_add_f32_e32 v48, v48, v49
	v_fmamk_f32 v48, v48, 0x3a800000, v1
	v_mul_f32_e32 v49, 0x4b800000, v48
	v_cmp_gt_f32_e32 vcc, s17, v48
	s_nop 1
	v_cndmask_b32_e32 v48, v48, v49, vcc
	v_rsq_f32_e32 v48, v48
	s_nop 0
	v_mul_f32_e32 v49, 0x45800000, v48
	v_cndmask_b32_e32 v48, v48, v49, vcc
	v_mul_f32_e32 v14, v14, v48
	v_add_f32_e32 v49, 1.0, v10
	v_fma_f32 v14, v49, v14, v18
	v_mul_f32_e32 v49, v74, v48
	v_fma_f32 v49, v69, v49, v19
	v_mul_f32_e32 v69, v75, v48
	v_add_f32_e32 v74, 1.0, v12
	v_fma_f32 v69, v74, v69, v20
	v_mul_f32_e32 v15, v15, v48
	v_add_f32_e32 v74, 1.0, v13
	v_fma_f32 v15, v74, v15, v21
	v_cvt_pk_bf16_f32 v14, v14, v49
	v_cvt_pk_bf16_f32 v15, v69, v15
	global_store_dwordx2 v[72:73], v[14:15], off
	v_mul_f32_e32 v6, v6, v48
	v_add_f32_e32 v14, 1.0, v34
	v_fma_f32 v6, v14, v6, v22
	v_mul_f32_e32 v14, v16, v48
	v_add_f32_e32 v15, 1.0, v35
	v_fma_f32 v14, v15, v14, v23
	v_mul_f32_e32 v15, v17, v48
	v_add_f32_e32 v16, 1.0, v36
	v_fma_f32 v15, v16, v15, v24
	v_mul_f32_e32 v7, v7, v48
	v_add_f32_e32 v16, 1.0, v37
	v_fma_f32 v7, v16, v7, v25
	v_cvt_pk_bf16_f32 v6, v6, v14
	v_cvt_pk_bf16_f32 v7, v15, v7
	global_store_dwordx2 v[72:73], v[6:7], off offset:512
	v_mul_f32_e32 v2, v2, v48
	v_add_f32_e32 v6, 1.0, v38
	v_fma_f32 v2, v6, v2, v26
	v_mul_f32_e32 v3, v3, v48
	v_add_f32_e32 v6, 1.0, v39
	v_fma_f32 v3, v6, v3, v27
	v_mul_f32_e32 v4, v4, v48
	v_add_f32_e32 v6, 1.0, v40
	v_fma_f32 v4, v6, v4, v28
	v_mul_f32_e32 v5, v5, v48
	v_add_f32_e32 v6, 1.0, v41
	v_fma_f32 v5, v6, v5, v29
	v_cvt_pk_bf16_f32 v2, v2, v3
	v_cvt_pk_bf16_f32 v3, v4, v5
	global_store_dwordx2 v[72:73], v[2:3], off offset:1024
	v_mul_f32_e32 v2, v46, v48
	v_add_f32_e32 v3, 1.0, v42
	v_fma_f32 v2, v3, v2, v30
	v_mul_f32_e32 v3, v47, v48
	v_add_f32_e32 v4, 1.0, v43
	v_fma_f32 v3, v4, v3, v31
	v_mul_f32_e32 v4, v8, v48
	v_add_f32_e32 v5, 1.0, v44
	v_fma_f32 v4, v5, v4, v32
	v_mul_f32_e32 v5, v9, v48
	v_add_f32_e32 v6, 1.0, v45
	v_fma_f32 v5, v6, v5, v33
	v_cvt_pk_bf16_f32 v2, v2, v3
	v_cvt_pk_bf16_f32 v3, v4, v5
	global_store_dwordx2 v[72:73], v[2:3], off offset:1536
	v_lshl_add_u64 v[72:73], v[72:73], 0, s[12:13]
	s_waitcnt lgkmcnt(0)
	v_mov_b32_e32 v14, v62
	v_mov_b32_e32 v74, v63
	v_mov_b32_e32 v75, v64
	v_mov_b32_e32 v15, v65
	v_mov_b32_e32 v6, v58
	v_mov_b32_e32 v16, v59
	v_mov_b32_e32 v17, v60
	v_mov_b32_e32 v7, v61
	v_mov_b32_e32 v2, v54
	v_mov_b32_e32 v3, v55
	v_mov_b32_e32 v4, v56
	v_mov_b32_e32 v5, v57
	v_mov_b32_e32 v46, v50
	v_mov_b32_e32 v47, v51
	v_mov_b32_e32 v48, v52
	v_mov_b32_e32 v49, v53
	s_andn2_b64 exec, exec, s[8:9]
	s_cbranch_execz .LBB0_173
.LBB0_171:
	v_mov_b32_e32 v69, v68
	v_add_u32_e32 v68, s86, v69
	v_cmp_gt_i32_e32 vcc, s16, v68
	v_cmp_lt_i32_e64 s[4:5], s2, v68
	s_nop 0
	v_cndmask_b32_e32 v8, v69, v68, vcc
	v_ashrrev_i32_e32 v9, 31, v8
	v_lshlrev_b64 v[8:9], 12, v[8:9]
	v_lshl_add_u64 v[8:9], v[70:71], 0, v[8:9]
	global_load_dwordx4 v[62:65], v[8:9], off
	global_load_dwordx4 v[58:61], v[8:9], off offset:1024
	global_load_dwordx4 v[54:57], v[8:9], off offset:2048
	global_load_dwordx4 v[50:53], v[8:9], off offset:3072
	v_ashrrev_i32_e32 v8, 12, v69
	v_cmp_ne_u32_e32 vcc, v8, v76
	s_and_saveexec_b64 s[14:15], vcc
	s_cbranch_execz .LBB0_170
	s_load_dwordx2 s[18:19], s[6:7], 0x108
	v_mul_hi_i32_i24_e32 v11, 0x6000, v8
	v_mul_i32_i24_e32 v10, 0x6000, v8
	s_waitcnt lgkmcnt(0)
	v_lshl_add_u64 v[10:11], s[18:19], 0, v[10:11]
	v_lshl_add_u64 v[76:77], v[10:11], 0, v[66:67]
	v_add_co_u32_e32 v80, vcc, 0x1000, v76
	v_lshl_add_u64 v[78:79], v[76:77], 0, s[10:11]
	s_nop 0
	v_addc_co_u32_e32 v81, vcc, 0, v77, vcc
	global_load_dwordx4 v[18:21], v[76:77], off
	global_load_dwordx4 v[22:25], v[76:77], off offset:1024
	global_load_dwordx4 v[34:37], v[78:79], off offset:1024
	global_load_dwordx4 v[38:41], v[78:79], off offset:2048
	global_load_dwordx4 v[26:29], v[76:77], off offset:2048
	global_load_dwordx4 v[30:33], v[76:77], off offset:3072
	global_load_dwordx4 v[10:13], v[80:81], off
	global_load_dwordx4 v[42:45], v[78:79], off offset:3072
	v_mov_b32_e32 v76, v8
	s_branch .LBB0_170

; DEVI CvSlice cv_slice(const Params& p, int l, int s, int lane) {
;     CvSlice c;
;     if (s < NS_W13) {
;         const int e = s >> 9, r = s & 511, hb = r & 7, mat = (r >> 3) & 1, ks = r >> 4;
;         const float* W = mat ? (e < NE ? p.w3 + ((size_t)l * NE + e) * 1024 * 256 : p.ws3 + (size_t)l * 1024 * 256)
;                              : (e < NE ? p.w1 + ((size_t)l * NE + e) * 1024 * 256 : p.ws1 + (size_t)l * 1024 * 256);
;         const int hc0 = hb * 32;
;         c.src = W + hc0 + (lane & 7) * 4; c.ld = 256; c.dst = p.w13t + (size_t)e * 512 * 1024; c.K = 1024;
;         c.r0 = (hc0 >> 7) * 256 + ((hc0 >> 5) & 3) * 32 + mat * 16; c.k0 = ks * 32; c.perm = 0;
;     } else {
;         s -= NS_W13;
;         const int e = s >> 8, r = s & 255, nb = r & 31, ks = r >> 5;
;         const float* W2 = e < NE ? p.w2 + ((size_t)l * NE + e) * 256 * 1024 : p.ws2 + (size_t)l * 256 * 1024;
;         c.src = W2 + nb * 32 + (lane & 7) * 4; c.ld = 1024; c.dst = p.w2t + (size_t)e * 1024 * 256; c.K = 256; c.r0 = (nb >> 3) * 256 + ((nb & 7) >> 1) * 32 + (nb & 1) * 8; c.k0 = ks * 32; c.perm = 1;
;     }
; DEVI void attn_unit8(const Params& p, char* smem, int unit, int l, int& cvs  , CvRun& crun) {
;     ...
;         const char* Kb = K_lds + s0 * 24576; const int vb = vb0 + s0 * 16384;
;         CvRegs cvr; cv_issue(p, l, cvs, lane, cvr, crun); cvs += (int)gridDim.x * 8;
;         qkt(pB0, pB1, Kb + 12288, qr, r32, hi, cinit);
.LBB0_666:
	s_mul_i32 s98, s89, 0x6000
	s_add_i32 s98, s98, 0
	v_add_u32_e32 v86, s98, v129
	ds_read_b128 v[82:85], v86 offset:12288
	ds_read_b128 v[124:127], v86 offset:18432
	s_cmp_lt_i32 s54, 0x30300
	s_mov_b32 s61, s2
	s_cselect_b64 s[14:15], -1, 0
	s_cmp_gt_i32 s54, 0x302ff
	s_mov_b32 s2, s6
	s_cbranch_scc1 .LBB0_696
	s_cmp_lt_i32 s56, 1
	s_mov_b64 s[16:17], -1
	s_cbranch_scc0 .LBB0_693
	s_cmp_gt_i32 s54, 0x201ff
	s_cselect_b64 s[16:17], -1, 0
	s_mov_b64 s[6:7], -1
	s_and_b64 vcc, exec, s[16:17]
	s_cbranch_vccz .LBB0_670
	s_add_i32 s6, s54, 0xfffdfe00
	s_lshr_b32 s8, s6, 8
	s_and_b32 s10, s54, 0xe0
	s_cmp_lt_u32 s6, 0x10000
	s_cselect_b64 s[6:7], -1, 0
	s_and_b32 s11, s70, 0x3fc0000
	s_and_b64 s[6:7], s[6:7], exec
	s_cselect_b32 s6, 0xc0, s78
	s_cselect_b32 s11, s11, 0
	s_add_u32 s6, s24, s6
	s_addc_u32 s7, s25, 0
	s_load_dwordx2 s[6:7], s[6:7], 0x0
	s_lshl_b32 s11, s11, 2
	s_load_dwordx2 s[20:21], s[24:25], 0x158
	s_waitcnt lgkmcnt(0)
	s_add_u32 s6, s6, s11
	s_addc_u32 s7, s7, 0
	s_and_b32 s11, s71, 0x3e0
	s_lshl_b32 s11, s11, 2
	s_add_u32 s18, s6, s11
	s_addc_u32 s19, s7, 0
	s_lshl_b64 s[6:7], s[8:9], 19
	s_add_u32 s20, s20, s6
	s_addc_u32 s21, s21, s7
	s_and_b32 s6, s71, 0x300
	s_and_b32 s7, s84, 0x60
	s_or_b32 s6, s6, s7
	s_and_b32 s7, s85, 8
	s_or_b32 s8, s6, s7
	s_mov_b64 s[6:7], 0

; DEVI f32x4 ld_nt(const float* p) { return __builtin_nontemporal_load((const f32x4*)p); }
; DEVI void cv_next(const Params& p, int l, int s, int lane, int stride, CvRun& run) {
;     ...
;     run.c = cv_slice(p, l, s, lane); run.left = 0;
;     if ((stride & 511) == 0) {
;         if (s < NS_W13) { const int e = s >> 9, es = stride >> 9; if (e < NE) { run.left = (NE - 1 - e) / es; run.sstep = (long)es * 1024 * 256; run.dstep = (long)es * 512 * 1024; } }
;         else { const int e = (s - NS_W13) >> 8, es = stride >> 8; if (e < NE) { run.left = (NE - 1 - e) / es; run.sstep = (long)es * 256 * 1024; run.dstep = (long)es * 1024 * 256; } } }
; }
; DEVI void cv_issue(const Params& p, int l, int s, int lane, CvRegs& R, CvRun& run) {
;     R.live = s < NS_SLICES ? 1 : 0;
;     if (R.live) { cv_next(p, l, s, lane, (int)gridDim.x * 8, run); R.c = run.c; const int kq = lane >> 3;
;         const float* sp = R.c.src + (size_t)(R.c.k0 + 2 * kq) * R.c.ld;
;         R.a0 = ld_nt(sp); R.b0 = ld_nt(sp + R.c.ld); R.a1 = ld_nt(sp + (size_t)16 * R.c.ld); R.b1 = ld_nt(sp + (size_t)17 * R.c.ld); }
.LBB0_692:
	v_lshlrev_b32_e32 v174, 2, v114
	v_lshl_add_u64 v[250:251], s[18:19], 0, v[174:175]
	s_mov_b64 s[16:17], 0
	v_mov_b64_e32 v[182:183], s[20:21]
.LBB0_693:
	s_and_b64 vcc, exec, s[16:17]
	s_cbranch_vccz .LBB0_695
	s_lshl_b64 s[6:7], s[26:27], 1
	v_lshl_add_u64 v[250:251], s[28:29], 2, v[170:171]
	v_lshl_add_u64 v[182:183], v[172:173], 0, s[6:7]
	s_add_i32 s11, s56, -1
	s_mov_b32 s8, s60
	s_mov_b32 s94, s59
	s_mov_b32 s10, s58
	s_mov_b32 s6, s57
	s_mov_b32 s95, s55
	s_mov_b64 s[50:51], s[28:29]
	s_mov_b64 s[22:23], s[26:27]
.LBB0_695:
	v_add_u32_e32 v252, s10, v128
	s_ashr_i32 s7, s6, 31
	v_mad_i64_i32 v[252:253], s[16:17], v252, s6, 0
	v_lshl_add_u64 v[252:253], v[252:253], 2, v[250:251]
	s_lshl_b64 s[16:17], s[6:7], 2
	v_lshl_add_u64 v[254:255], v[252:253], 0, s[16:17]
	global_load_dwordx4 v[154:157], v[252:253], off nt
	global_load_dwordx4 v[158:161], v[254:255], off nt
	v_mad_i64_i32 v[252:253], s[18:19], s6, 60, v[254:255]
	v_lshl_add_u64 v[254:255], v[252:253], 0, s[16:17]
	global_load_dwordx4 v[162:165], v[252:253], off nt
	global_load_dwordx4 v[166:169], v[254:255], off nt
	s_mov_b64 s[26:27], s[22:23]
	s_mov_b64 s[28:29], s[50:51]
	s_mov_b32 s56, s11
	s_mov_b32 s55, s95
	v_mov_b64_e32 v[170:171], v[250:251]
	s_mov_b32 s57, s6
	s_mov_b32 s58, s10
	v_mov_b64_e32 v[172:173], v[182:183]
	s_mov_b32 s59, s94
	s_mov_b32 s60, s8
; DEVI void pv_both(f32x16& o0, f32x16& o1, int vb, bf16x8 pa0, bf16x8 pa1, bf16x8 pa2, bf16x8 pa3) {
;     const s16x4 a0 = tr_read<v_rd_off(0, 0, 0)>(vb), b0 = tr_read<v_rd_off(0, 0, 1)>(vb), a1 = tr_read<v_rd_off(0, 1, 0)>(vb), b1 = tr_read<v_rd_off(0, 1, 1)>(vb);
;     const s16x4 a2 = tr_read<v_rd_off(0, 2, 0)>(vb), b2 = tr_read<v_rd_off(0, 2, 1)>(vb), a3 = tr_read<v_rd_off(0, 3, 0)>(vb), b3 = tr_read<v_rd_off(0, 3, 1)>(vb);
;     const s16x4 c0 = tr_read<v_rd_off(1, 0, 0)>(vb), d0 = tr_read<v_rd_off(1, 0, 1)>(vb), c1 = tr_read<v_rd_off(1, 1, 0)>(vb), d1 = tr_read<v_rd_off(1, 1, 1)>(vb);
;     const s16x4 c2 = tr_read<v_rd_off(1, 2, 0)>(vb), d2 = tr_read<v_rd_off(1, 2, 1)>(vb), c3 = tr_read<v_rd_off(1, 3, 0)>(vb), d3 = tr_read<v_rd_off(1, 3, 1)>(vb);
;     asm volatile("s_waitcnt lgkmcnt(8)" ::: "memory"); SBAR();
;     ...
;     o0 = __builtin_amdgcn_mfma_f32_32x32x16_bf16(pa0, PK(a0, b0), o0, 0, 0, 0);
;     o0 = __builtin_amdgcn_mfma_f32_32x32x16_bf16(pa1, PK(a1, b1), o0, 0, 0, 0);
;     o0 = __builtin_amdgcn_mfma_f32_32x32x16_bf16(pa2, PK(a2, b2), o0, 0, 0, 0);
;     o0 = __builtin_amdgcn_mfma_f32_32x32x16_bf16(pa3, PK(a3, b3), o0, 0, 0, 0);
;     asm volatile("s_waitcnt lgkmcnt(0)" ::: "memory"); SBAR();
;     o1 = __builtin_amdgcn_mfma_f32_32x32x16_bf16(pa0, PK(c0, d0), o1, 0, 0, 0);
;     o1 = __builtin_amdgcn_mfma_f32_32x32x16_bf16(pa1, PK(c1, d1), o1, 0, 0, 0);
;     o1 = __builtin_amdgcn_mfma_f32_32x32x16_bf16(pa2, PK(c2, d2), o1, 0, 0, 0);
;     o1 = __builtin_amdgcn_mfma_f32_32x32x16_bf16(pa3, PK(c3, d3), o1, 0, 0, 0);
;     ...
; }
; template <bool FIRST> DEVI bool partialSM(f32x16& p0, f32x16& p1, float& m_reg, float& alpha) {
;     float pmax = p0[0];
; #pragma unroll
;     for (int r = 1; r < 16; ++r) pmax = fmaxf(pmax, p0[r]);
; #pragma unroll
;     for (int r = 0; r < 16; ++r) pmax = fmaxf(pmax, p1[r]);
;     { auto rr = __builtin_amdgcn_permlane32_swap(__float_as_uint(pmax), __float_as_uint(pmax), false, false);
;       pmax = fmaxf(__uint_as_float(rr[0]), __uint_as_float(rr[1])); }
;     if (FIRST) { m_reg = pmax; alpha = 1.f;
; #pragma unroll
;         for (int r = 0; r < 16; ++r) { p0[r] = __builtin_amdgcn_exp2f(p0[r] - pmax); p1[r] = p1[r] - pmax; }
;         return false;
;     } else if (__builtin_expect(__all(pmax <= ATT_THR), 1)) { alpha = 1.f;
; #pragma unroll
;         for (int r = 0; r < 16; ++r) p0[r] = __builtin_amdgcn_exp2f(p0[r]);
.LBB0_696:
	v_add_u32_e32 v174, s98, v204
	v_exp_f32_e32 v66, v66
	v_exp_f32_e32 v67, v67
	s_waitcnt lgkmcnt(1)
	v_mfma_f32_32x32x16_bf16 v[98:113], v[82:85], v[150:153], v[34:49]
	v_add_u32_e32 v82, s98, v184
	v_add_u32_e32 v83, s98, v185
	ds_read_b128 v[208:211], v82 offset:12288
	ds_read_b128 v[212:215], v82 offset:18432
	ds_read_b128 v[216:219], v83 offset:12288
	ds_read_b128 v[220:223], v83 offset:18432
	v_exp_f32_e32 v68, v68
	v_exp_f32_e32 v69, v69
	v_exp_f32_e32 v70, v70
	v_exp_f32_e32 v71, v71
	s_waitcnt lgkmcnt(4)
	v_mfma_f32_32x32x16_bf16 v[82:97], v[124:127], v[150:153], v[34:49]
	ds_read_b128 v[124:127], v174 offset:12288
	ds_read_b128 v[224:227], v174 offset:18432
	v_exp_f32_e32 v72, v72
	v_exp_f32_e32 v73, v73
	v_exp_f32_e32 v74, v74
	v_exp_f32_e32 v75, v75
	v_exp_f32_e32 v76, v76
	v_exp_f32_e32 v77, v77
	s_waitcnt lgkmcnt(5)
	v_mfma_f32_32x32x16_bf16 v[98:113], v[208:211], v[138:141], v[98:113]
	v_add_u32_e32 v174, s98, v205
	v_exp_f32_e32 v78, v78
	v_exp_f32_e32 v79, v79
	ds_read_b128 v[228:231], v174 offset:12288
	ds_read_b128 v[232:235], v174 offset:18432
	v_exp_f32_e32 v80, v80
	v_exp_f32_e32 v81, v81
	v_add_u32_e32 v174, s98, v206
	s_waitcnt lgkmcnt(6)
	v_mfma_f32_32x32x16_bf16 v[82:97], v[212:215], v[138:141], v[82:97]
	v_add_f32_e64 v212, v50, v66
	v_add_f32_e64 v213, v51, v67
	v_add_f32_e64 v214, v52, v68
	v_add_f32_e64 v215, v53, v69
	v_lshl_add_u32 v202, s89, 14, v115
	v_pk_add_f32 v[212:213], v[214:215], v[212:213]
	v_pk_add_f32 v[214:215], v[54:55], v[70:71]
	ds_read_b128 v[208:211], v174 offset:12288
	ds_read_b128 v[236:239], v174 offset:18432
	v_pk_add_f32 v[212:213], v[214:215], v[212:213]
	s_waitcnt lgkmcnt(7)
	v_mfma_f32_32x32x16_bf16 v[98:113], v[216:219], v[134:137], v[98:113]
	v_add_f32_e64 v214, v56, v72
	v_add_f32_e64 v215, v57, v73
	v_cvt_pk_bf16_f32 v50, v50, v51
	v_cvt_pk_bf16_f32 v51, v52, v53
	v_cvt_pk_bf16_f32 v52, v54, v55
	v_cvt_pk_bf16_f32 v53, v56, v57
	v_cvt_pk_bf16_f32 v54, v58, v59
	v_add_f32_e64 v212, v214, v212
	v_add_f32_e64 v213, v215, v213
	s_waitcnt lgkmcnt(6)
	v_mfma_f32_32x32x16_bf16 v[82:97], v[220:223], v[134:137], v[82:97]
	v_add_f32_e64 v214, v58, v74
	v_add_f32_e64 v215, v59, v75
	v_cvt_pk_bf16_f32 v55, v60, v61
	v_cvt_pk_bf16_f32 v56, v62, v63
	v_cvt_pk_bf16_f32 v57, v64, v65
	v_cvt_pk_bf16_f32 v58, v66, v67
	v_cvt_pk_bf16_f32 v59, v68, v69
	v_add_f32_e64 v212, v214, v212
	v_add_f32_e64 v213, v215, v213
	s_waitcnt lgkmcnt(5)
	v_mfma_f32_32x32x16_bf16 v[98:113], v[124:127], v[130:133], v[98:113]
	v_add_f32_e64 v214, v60, v76
	v_add_f32_e64 v215, v61, v77
	v_add_f32_e64 v126, v62, v78
	v_add_f32_e64 v127, v63, v79
	v_add_f32_e64 v124, v214, v212
	v_add_f32_e64 v125, v215, v213
	v_cvt_pk_bf16_f32 v60, v70, v71
	v_cvt_pk_bf16_f32 v61, v72, v73
	v_cvt_pk_bf16_f32 v62, v74, v75
	v_cvt_pk_bf16_f32 v63, v76, v77
	s_waitcnt lgkmcnt(4)
	v_mfma_f32_32x32x16_bf16 v[82:97], v[224:227], v[130:133], v[82:97]
	v_add_f32_e64 v124, v126, v124
	v_add_f32_e64 v125, v127, v125
	v_add_f32_e64 v126, v64, v80
	v_add_f32_e64 v127, v65, v81
	v_cvt_pk_bf16_f32 v64, v78, v79
	v_cvt_pk_bf16_f32 v65, v80, v81
	ds_read_b64_tr_b16 v[66:67], v202 offset:0
	ds_read_b64_tr_b16 v[68:69], v202 offset:0x400
	ds_read_b64_tr_b16 v[70:71], v202 offset:0x800
	s_waitcnt lgkmcnt(6)
	v_mfma_f32_32x32x16_bf16 v[98:113], v[228:231], v[146:149], v[98:113]
	ds_read_b64_tr_b16 v[72:73], v202 offset:0xc00
	ds_read_b64_tr_b16 v[74:75], v202 offset:0x1000
	ds_read_b64_tr_b16 v[76:77], v202 offset:0x1400
	ds_read_b64_tr_b16 v[78:79], v202 offset:0x1800
	ds_read_b64_tr_b16 v[80:81], v202 offset:0x1c00
	v_add_f32_e64 v124, v126, v124
	v_add_f32_e64 v125, v127, v125
	s_waitcnt lgkmcnt(10)
	v_mfma_f32_32x32x16_bf16 v[82:97], v[232:235], v[146:149], v[82:97]
	v_pk_add_f32 v[124:125], v[124:125], v[124:125] op_sel:[0,1] op_sel_hi:[1,0]
	s_nop 0
	v_mov_b32_e32 v125, v124
	s_nop 1
	v_permlane32_swap_b32_e32 v124, v125
	s_waitcnt lgkmcnt(9)
	v_mfma_f32_32x32x16_bf16 v[98:113], v[208:211], v[142:145], v[98:113]
	ds_read_b64_tr_b16 v[208:209], v202 offset:0x200
	ds_read_b64_tr_b16 v[210:211], v202 offset:0x600
	ds_read_b64_tr_b16 v[212:213], v202 offset:0xa00
	ds_read_b64_tr_b16 v[214:215], v202 offset:0xe00
	ds_read_b64_tr_b16 v[216:217], v202 offset:0x1200
	ds_read_b64_tr_b16 v[218:219], v202 offset:0x1600
	ds_read_b64_tr_b16 v[220:221], v202 offset:0x1a00
	s_waitcnt lgkmcnt(15)
	v_mfma_f32_32x32x16_bf16 v[82:97], v[236:239], v[142:145], v[82:97]
	ds_read_b64_tr_b16 v[222:223], v202 offset:0x1e00
	s_waitcnt lgkmcnt(14)
	v_mfma_f32_32x32x16_bf16 v[18:33], v[50:53], v[66:69], v[18:33]
	s_waitcnt lgkmcnt(12)
	v_mfma_f32_32x32x16_bf16 v[18:33], v[54:57], v[70:73], v[18:33]
	s_waitcnt lgkmcnt(10)
	v_mfma_f32_32x32x16_bf16 v[18:33], v[58:61], v[74:77], v[18:33]
	s_waitcnt lgkmcnt(8)
	v_mfma_f32_32x32x16_bf16 v[18:33], v[62:65], v[78:81], v[18:33]
	s_waitcnt lgkmcnt(6)
	v_mfma_f32_32x32x16_bf16 v[2:17], v[50:53], v[208:211], v[2:17]
	s_nop 4
	v_max_f32_e32 v249, v99, v99
	v_max_f32_e32 v250, v98, v98
	v_max_f32_e32 v249, v250, v249
	v_max3_f32 v249, v249, v100, v101
	v_max3_f32 v249, v249, v102, v103
	v_max3_f32 v251, v249, v104, v105
	v_max3_f32 v251, v251, v106, v107
	s_waitcnt lgkmcnt(4)
	v_exp_f32_e32 v50, v98
	v_exp_f32_e32 v51, v99
	v_exp_f32_e32 v52, v100
	v_exp_f32_e32 v53, v101
	v_mov_b64_e32 v[66:67], v[82:83]
	v_mov_b64_e32 v[68:69], v[84:85]
	v_mfma_f32_32x32x16_bf16 v[2:17], v[54:57], v[212:215], v[2:17]
	v_max3_f32 v251, v251, v108, v109
	v_max3_f32 v251, v251, v110, v111
	v_max3_f32 v251, v251, v112, v113
	v_max3_f32 v251, v251, v82, v83
	v_max3_f32 v251, v251, v84, v85
	v_max3_f32 v251, v251, v86, v87
	v_max3_f32 v251, v251, v88, v89
	s_waitcnt lgkmcnt(2)
	v_exp_f32_e32 v54, v102
	v_exp_f32_e32 v55, v103
	v_exp_f32_e32 v56, v104
	v_exp_f32_e32 v57, v105
	v_mov_b64_e32 v[70:71], v[86:87]
	v_mov_b64_e32 v[72:73], v[88:89]
	v_mfma_f32_32x32x16_bf16 v[2:17], v[58:61], v[216:219], v[2:17]
	v_max3_f32 v251, v251, v90, v91
	v_max3_f32 v251, v251, v92, v93
	v_max3_f32 v251, v251, v94, v95
	v_max3_f32 v251, v251, v96, v97
	v_mov_b32_e32 v252, v251
	s_nop 1
	v_permlane32_swap_b32_e32 v251, v252
	s_waitcnt lgkmcnt(0)
	v_exp_f32_e32 v58, v106
	v_exp_f32_e32 v59, v107
	v_exp_f32_e32 v60, v108
	v_exp_f32_e32 v61, v109
	v_mov_b64_e32 v[74:75], v[90:91]
	v_mov_b64_e32 v[76:77], v[92:93]
	v_mfma_f32_32x32x16_bf16 v[2:17], v[62:65], v[220:223], v[2:17]
	v_exp_f32_e32 v62, v110
	v_exp_f32_e32 v63, v111
	v_exp_f32_e32 v64, v112
	v_exp_f32_e32 v65, v113
	v_mov_b64_e32 v[78:79], v[94:95]
	v_mov_b64_e32 v[80:81], v[96:97]
	v_max_f32_e32 v252, v252, v252
	v_max_f32_e32 v251, v251, v251
	v_max_f32_e32 v126, v251, v252
	v_cmp_ge_f32_e32 vcc, s79, v126
	s_cmp_lg_u64 vcc, exec
	s_cselect_b64 s[6:7], -1, 0
	s_cbranch_scc1 .LBB0_705
	v_mov_b32_e32 v208, 1.0
	v_mov_b32_e32 v209, v203
	s_branch .LBB0_699

; DEVI int vtid() { return tidx() & 255; }
; DEVI int vbid() { return bidx() * 2 + vhb(); }
; DEVI int vgrid() { return (int)gridDim.x * 2; }
; DEVI float bflo(unsigned w) { return __uint_as_float(w << 16); }
; DEVI float bfhi(unsigned w) { return __uint_as_float(w & 0xffff0000u); }
; DEVI void row_stats(const f32x4 (&v)[4], float& mu, float& rstd) {
;     float s = 0.f;
; #pragma unroll
;     for (int i = 0; i < 4; ++i) s += (v[i][0] + v[i][1]) + (v[i][2] + v[i][3]);
;     mu = wave_sum(s) * (1.f / 1024.f);
;     float q = 0.f;
; #pragma unroll
;     for (int i = 0; i < 4; ++i)
; #pragma unroll
;         for (int j = 0; j < 4; ++j) { const float d = v[i][j] - mu; q += d * d; }
;     rstd = rsqrtf(wave_sum(q) * (1.f / 1024.f) + LN_EPS);
; DEVI void phase_ln_mid(const Params& p, int l) {
;     const int lane = vtid() & 63, gw = vbid() * 4 + (vtid() >> 6), nw = vgrid() * 4;
;     bf16_t* xab = p.xa; bf16_t* hb = p.h; asm volatile("" : "+s"(xab), "+s"(hb));
;     f32x4 lg4[4], lb4[4], sh4[4], sc4[4]; int bcur = -1;
; #pragma unroll
;     for (int i = 0; i < 4; ++i) { const int c = lane * 4 + 256 * i; lg4[i] = *(const f32x4*)(p.ln1_g + l * 1024 + c); lb4[i] = *(const f32x4*)(p.ln1_b + l * 1024 + c); sh4[i] = lg4[i]; sc4[i] = lg4[i]; }
;     u32x2 rw[4], rn[4];
; #pragma unroll
;     for (int i = 0; i < 4; ++i) rw[i] = *(const u32x2*)(xab + (size_t)(gw < T_ ? gw : 0) * 1024 + lane * 4 + 256 * i);
;     for (int t = gw; t < T_; t += nw) {
;         const int b = t >> 12; f32x4 v[4]; const int tn = t + nw < T_ ? t + nw : t;
; #pragma unroll
;         for (int i = 0; i < 4; ++i) { v[i] = (f32x4){bflo(rw[i].x), bfhi(rw[i].x), bflo(rw[i].y), bfhi(rw[i].y)}; rn[i] = *(const u32x2*)(xab + (size_t)tn * 1024 + lane * 4 + 256 * i); }
.LBB0_1080:
	s_or_b64 exec, exec, s[4:5]
	s_mov_b64 s[8:9], s[0:1]
	v_mov_b32_e32 v34, v0
	s_mov_b32 s2, s84
	s_waitcnt lgkmcnt(0)
	v_mov_b32_e32 v2, v0
	v_mov_b32_e32 v18, v0
	s_barrier
	s_load_dwordx4 s[4:7], s[8:9], 0x160
	v_readfirstlane_b32 s10, v2
	s_lshr_b32 s10, s10, 6
	s_and_b32 s12, s10, 0x3fffffc
	s_lshl_b32 s2, s2, 3
	s_waitcnt lgkmcnt(0)
	s_mov_b64 s[10:11], s[4:5]
	s_add_i32 s4, s12, s2
	s_cmpk_gt_u32 s4, 0x7fff
	s_movk_i32 s2, 0x7fff
	s_cbranch_scc1 .LBB0_1086
	s_load_dwordx4 s[12:15], s[8:9], 0x90
	v_lshrrev_b32_e32 v18, 6, v18
	v_lshlrev_b32_e32 v2, 2, v34
	v_and_or_b32 v68, v18, 3, s4
	v_and_b32_e32 v36, 0xfc, v2
	v_mov_b32_e32 v67, 0
	v_lshlrev_b32_e32 v66, 11, v68
	v_lshlrev_b32_e32 v35, 2, v36
	v_lshl_add_u64 v[18:19], s[6:7], 0, v[66:67]
	v_lshlrev_b32_e32 v66, 1, v36
	s_waitcnt lgkmcnt(0)
	global_load_dwordx4 v[2:5], v35, s[12:13]
	global_load_dwordx4 v[6:9], v35, s[12:13] offset:1024
	global_load_dwordx4 v[10:13], v35, s[12:13] offset:2048
	global_load_dwordx4 v[14:17], v35, s[12:13] offset:3072
	v_lshl_add_u64 v[38:39], v[18:19], 0, v[66:67]
	global_load_dwordx4 v[18:21], v35, s[14:15]
	global_load_dwordx4 v[22:25], v35, s[14:15] offset:1024
	global_load_dwordx4 v[26:29], v35, s[14:15] offset:2048
	global_load_dwordx4 v[30:33], v35, s[14:15] offset:3072
	global_load_dwordx2 v[82:83], v[38:39], off offset:1536
	global_load_dwordx2 v[84:85], v[38:39], off offset:1024
	global_load_dwordx2 v[86:87], v[38:39], off offset:512
	global_load_dwordx2 v[88:89], v[38:39], off
	v_mov_b32_e32 v69, v67
	v_and_b32_e32 v34, 63, v34
	v_lshlrev_b64 v[70:71], 11, v[68:69]
	s_ashr_i32 s87, s86, 31
	v_lshl_or_b32 v70, v34, 3, v70
	v_lshl_add_u64 v[72:73], s[6:7], 0, v[66:67]
	v_lshlrev_b32_e32 v66, 2, v36
	v_mov_b32_e32 v91, -1
	s_mov_b64 s[12:13], 0
	s_mov_b32 s22, 0x8000
	s_mov_b64 s[14:15], 0x3000
	s_mov_b64 s[16:17], 0x4000
	v_mov_b32_e32 v90, 0x3727c5ac
	s_mov_b32 s23, 0x800000
	s_lshl_b64 s[18:19], s[86:87], 11
	s_waitcnt vmcnt(0)
	v_mov_b64_e32 v[36:37], v[4:5]
	v_mov_b64_e32 v[44:45], v[8:9]
	v_mov_b64_e32 v[48:49], v[12:13]
	v_mov_b64_e32 v[56:57], v[16:17]
	v_mov_b64_e32 v[34:35], v[2:3]
	v_mov_b64_e32 v[42:43], v[6:7]
	v_mov_b64_e32 v[46:47], v[10:11]
	v_mov_b64_e32 v[54:55], v[14:15]
	v_mov_b32_e32 v38, v2
	v_mov_b32_e32 v39, v3
	v_mov_b32_e32 v40, v4
	v_mov_b32_e32 v41, v5
	v_mov_b32_e32 v50, v6
	v_mov_b32_e32 v51, v7
	v_mov_b32_e32 v52, v8
	v_mov_b32_e32 v53, v9
	v_mov_b32_e32 v58, v10
	v_mov_b32_e32 v59, v11
	v_mov_b32_e32 v60, v12
	v_mov_b32_e32 v61, v13
	v_mov_b32_e32 v62, v14
	v_mov_b32_e32 v63, v15
	v_mov_b32_e32 v64, v16
	v_mov_b32_e32 v65, v17
	s_branch .LBB0_1083
.LBB0_1082:
	s_or_b64 exec, exec, s[20:21]
	s_waitcnt lgkmcnt(0)
	v_lshlrev_b32_e32 v93, 16, v89
	v_lshlrev_b32_e32 v92, 16, v88
	v_and_b32_e32 v89, 0xffff0000, v89
	v_and_b32_e32 v88, 0xffff0000, v88
	v_lshlrev_b32_e32 v95, 16, v87
	v_lshlrev_b32_e32 v94, 16, v86
	v_and_b32_e32 v87, 0xffff0000, v87
	v_and_b32_e32 v86, 0xffff0000, v86
	v_lshlrev_b32_e32 v96, 16, v84
	v_and_b32_e32 v97, 0xffff0000, v84
	v_and_b32_e32 v84, 0xffff0000, v85
	v_lshlrev_b32_e32 v85, 16, v85
	v_pk_add_f32 v[100:101], v[92:93], v[88:89]
	v_pk_add_f32 v[102:103], v[94:95], v[86:87]
	v_and_b32_e32 v98, 0xffff0000, v82
	v_lshlrev_b32_e32 v99, 16, v82
	v_and_b32_e32 v82, 0xffff0000, v83
	v_lshlrev_b32_e32 v83, 16, v83
	v_add_f32_e32 v69, v100, v101
	v_pk_add_f32 v[102:103], v[102:103], v[102:103] op_sel_hi:[0,1]
	v_pk_add_f32 v[106:107], v[84:85], v[84:85] op_sel_hi:[0,1]
	v_add_f32_e32 v101, 0, v69
	v_add_f32_e32 v105, v96, v97
	v_mov_b32_e32 v104, v99
	v_mov_b32_e32 v106, v98
	v_mov_b32_e32 v102, v83
	v_mov_b32_e32 v100, v82
	v_pk_add_f32 v[104:105], v[104:105], v[106:107]
	v_pk_add_f32 v[100:101], v[102:103], v[100:101]
	s_nop 0
	v_pk_add_f32 v[100:101], v[104:105], v[100:101]
	s_nop 0
	v_add_f32_e32 v69, v100, v101
	s_nop 1
	v_add_f32_dpp v69, v69, v69 quad_perm:[1,0,3,2] row_mask:0xf bank_mask:0xf bound_ctrl:1
	s_nop 1
	v_add_f32_dpp v69, v69, v69 quad_perm:[2,3,0,1] row_mask:0xf bank_mask:0xf bound_ctrl:1
	s_nop 1
	v_add_f32_dpp v69, v69, v69 row_half_mirror row_mask:0xf bank_mask:0xf bound_ctrl:1
	s_nop 1
	v_add_f32_dpp v69, v69, v69 row_mirror row_mask:0xf bank_mask:0xf bound_ctrl:1
	s_nop 0
	v_readlane_b32 s20, v69, 16
	v_readlane_b32 s21, v69, 48
	v_readlane_b32 s4, v69, 0
	v_readlane_b32 s5, v69, 32
	v_mov_b32_e32 v100, s20
	v_mov_b32_e32 v101, s21
	v_pk_add_f32 v[100:101], s[4:5], v[100:101]
	s_nop 0
	v_add_f32_e32 v69, v100, v101
	v_fmac_f32_e32 v88, 0xba800000, v69
	v_fmac_f32_e32 v92, 0xba800000, v69
	v_mul_f32_e32 v101, v88, v88
	v_fmac_f32_e32 v101, v92, v92
	v_fmac_f32_e32 v93, 0xba800000, v69
	v_fmac_f32_e32 v101, v93, v93
	v_fmac_f32_e32 v89, 0xba800000, v69
	v_fmac_f32_e32 v101, v89, v89
	v_fmac_f32_e32 v94, 0xba800000, v69
	v_fmac_f32_e32 v101, v94, v94
	v_fmac_f32_e32 v86, 0xba800000, v69
	v_fmac_f32_e32 v101, v86, v86
	v_fmac_f32_e32 v95, 0xba800000, v69
	v_fmac_f32_e32 v101, v95, v95
	v_fmac_f32_e32 v87, 0xba800000, v69
	v_fmac_f32_e32 v101, v87, v87
	v_fmac_f32_e32 v96, 0xba800000, v69
	v_fmac_f32_e32 v101, v96, v96
	v_fmac_f32_e32 v97, 0xba800000, v69
	v_mul_f32_e32 v100, 0x3a800000, v69
	v_fmac_f32_e32 v101, v97, v97
	v_pk_add_f32 v[102:103], v[84:85], v[100:101] op_sel_hi:[1,0] neg_lo:[0,1] neg_hi:[0,1]
	v_fmac_f32_e32 v84, 0xba800000, v69
	v_pk_mul_f32 v[102:103], v[102:103], v[102:103]
	v_fmac_f32_e32 v85, 0xba800000, v69
	v_add_f32_e32 v101, v103, v101
	v_add_f32_e32 v101, v102, v101
	v_pk_add_f32 v[102:103], v[98:99], v[100:101] op_sel_hi:[1,0] neg_lo:[0,1] neg_hi:[0,1]
	v_fmac_f32_e32 v98, 0xba800000, v69
	v_pk_mul_f32 v[102:103], v[102:103], v[102:103]
; DEVI void row_stats(const f32x4 (&v)[4], float& mu, float& rstd) {
;     float s = 0.f;
; #pragma unroll
;     for (int i = 0; i < 4; ++i) s += (v[i][0] + v[i][1]) + (v[i][2] + v[i][3]);
;     mu = wave_sum(s) * (1.f / 1024.f);
;     float q = 0.f;
; #pragma unroll
;     for (int i = 0; i < 4; ++i)
; #pragma unroll
;         for (int j = 0; j < 4; ++j) { const float d = v[i][j] - mu; q += d * d; }
;     rstd = rsqrtf(wave_sum(q) * (1.f / 1024.f) + LN_EPS);
; }
;     float mu, rstd; row_stats(v, mu, rstd);
; #pragma unroll
;     for (int i = 0; i < 4; ++i) { const int c = LAY ? lane * 16 + 4 * i : lane * 4 + 256 * i;
;         const f32x4 s4 = *(const f32x4*)(sc + c), h4 = *(const f32x4*)(sh + c);
;         float o[4];
; #pragma unroll
;         for (int j = 0; j < 4; ++j) o[j] = (v[i][j] - mu) * rstd * (1.f + s4[j]) + h4[j];
;         u32x2 w; w.x = cvt_pk_bf16(o[0], o[1]); w.y = cvt_pk_bf16(o[2], o[3]);
;         *(u32x2*)(hrow + c) = w; }
; }
; DEVI void write_h_reg(const f32x4 (&v)[4], const f32x4 (&sh)[4], const f32x4 (&sc)[4], bf16_t* hrow, int lane) {
;     float mu, rstd; row_stats(v, mu, rstd);
; #pragma unroll
;     for (int i = 0; i < 4; ++i) { float o[4];
; #pragma unroll
;         for (int j = 0; j < 4; ++j) o[j] = (v[i][j] - mu) * rstd * (1.f + sc[i][j]) + sh[i][j];
;         u32x2 w; w.x = cvt_pk_bf16(o[0], o[1]); w.y = cvt_pk_bf16(o[2], o[3]);
;         *(u32x2*)(hrow + lane * 4 + 256 * i) = w; }
; }
; DEVI void phase_ln_mid(const Params& p, int l) {
;     ...
;     for (int t = gw; t < T_; t += nw) {
;         const int b = t >> 12; f32x4 v[4]; const int tn = t + nw < T_ ? t + nw : t;
; #pragma unroll
;         for (int i = 0; i < 4; ++i) { v[i] = (f32x4){bflo(rw[i].x), bfhi(rw[i].x), bflo(rw[i].y), bfhi(rw[i].y)}; rn[i] = *(const u32x2*)(xab + (size_t)tn * 1024 + lane * 4 + 256 * i); }
;         if (b != bcur) { bcur = b; const float* ad = p.ada + ((size_t)l * 8 + b) * 6144;
; #pragma unroll
;             for (int i = 0; i < 4; ++i) { sh4[i] = *(const f32x4*)(ad + 3072 + lane * 4 + 256 * i); sc4[i] = *(const f32x4*)(ad + 4096 + lane * 4 + 256 * i); } }
;         float mu, rstd; row_stats(v, mu, rstd);
; #pragma unroll
;         for (int i = 0; i < 4; ++i) { const int c = lane * 4 + 256 * i; v[i] = (v[i] - mu) * rstd * lg4[i] + lb4[i]; st_bf4(xab + (size_t)t * 1024 + c, v[i]); }
;         write_h_reg(v, sh4, sc4, hb + (size_t)t * 1024, lane);
	v_fmac_f32_e32 v99, 0xba800000, v69
	v_add_f32_e32 v101, v103, v101
	v_add_f32_e32 v102, v102, v101
	v_pk_add_f32 v[100:101], v[82:83], v[100:101] op_sel_hi:[1,0] neg_lo:[0,1] neg_hi:[0,1]
	v_mov_b32_e32 v103, v88
	v_pk_mul_f32 v[100:101], v[100:101], v[100:101]
	v_mov_b32_e32 v88, v93
	v_add_f32_e32 v101, v101, v102
	v_add_f32_e32 v100, v100, v101
	v_mov_b32_e32 v102, v92
	v_fmac_f32_e32 v82, 0xba800000, v69
	v_add_f32_dpp v100, v100, v100 quad_perm:[1,0,3,2] row_mask:0xf bank_mask:0xf bound_ctrl:1
	v_fmac_f32_e32 v83, 0xba800000, v69
	s_nop 0
	v_add_f32_dpp v100, v100, v100 quad_perm:[2,3,0,1] row_mask:0xf bank_mask:0xf bound_ctrl:1
	s_nop 1
	v_add_f32_dpp v100, v100, v100 row_half_mirror row_mask:0xf bank_mask:0xf bound_ctrl:1
	s_nop 1
	v_add_f32_dpp v100, v100, v100 row_mirror row_mask:0xf bank_mask:0xf bound_ctrl:1
	s_nop 0
	v_readlane_b32 s20, v100, 16
	v_readlane_b32 s21, v100, 48
	v_readlane_b32 s4, v100, 0
	v_readlane_b32 s5, v100, 32
	v_mov_b32_e32 v100, s20
	v_mov_b32_e32 v101, s21
	v_pk_add_f32 v[100:101], s[4:5], v[100:101]
	s_nop 0
	v_add_f32_e32 v100, v100, v101
	v_fmamk_f32 v100, v100, 0x3a800000, v90
	v_mul_f32_e32 v101, 0x4b800000, v100
	v_cmp_gt_f32_e32 vcc, s23, v100
	s_nop 1
	v_cndmask_b32_e32 v100, v100, v101, vcc
	v_rsq_f32_e32 v100, v100
	s_nop 0
	v_mul_f32_e32 v101, 0x45800000, v100
	v_cndmask_b32_e32 v100, v100, v101, vcc
	v_pk_mul_f32 v[102:103], v[102:103], v[100:101] op_sel_hi:[1,0]
	v_pk_mul_f32 v[88:89], v[88:89], v[100:101] op_sel_hi:[1,0]
	v_pk_fma_f32 v[92:93], v[2:3], v[102:103], v[18:19]
	v_pk_fma_f32 v[88:89], v[4:5], v[88:89], v[20:21]
	v_lshl_add_u64 v[102:103], s[6:7], 0, v[70:71]
	v_cvt_pk_bf16_f32 v104, v92, v93
	v_cvt_pk_bf16_f32 v105, v88, v89
	global_store_dwordx2 v[102:103], v[104:105], off
	v_mov_b32_e32 v104, v94
	v_mov_b32_e32 v105, v86
	v_mov_b32_e32 v86, v95
	v_pk_mul_f32 v[104:105], v[104:105], v[100:101] op_sel_hi:[1,0]
	v_pk_mul_f32 v[86:87], v[86:87], v[100:101] op_sel_hi:[1,0]
	v_pk_fma_f32 v[94:95], v[6:7], v[104:105], v[22:23]
	v_pk_fma_f32 v[86:87], v[8:9], v[86:87], v[24:25]
	v_cvt_pk_bf16_f32 v104, v94, v95
	v_pk_mul_f32 v[96:97], v[96:97], v[100:101] op_sel_hi:[1,0]
	v_cvt_pk_bf16_f32 v105, v86, v87
	global_store_dwordx2 v[102:103], v[104:105], off offset:512
	v_mov_b32_e32 v104, v85
	v_mov_b32_e32 v105, v84
	v_pk_mul_f32 v[84:85], v[104:105], v[100:101] op_sel_hi:[1,0]
	v_pk_fma_f32 v[96:97], v[10:11], v[96:97], v[26:27]
	v_pk_fma_f32 v[84:85], v[12:13], v[84:85], v[28:29]
	v_cvt_pk_bf16_f32 v104, v96, v97
	v_mov_b32_e32 v106, v94
	v_cvt_pk_bf16_f32 v105, v84, v85
	global_store_dwordx2 v[102:103], v[104:105], off offset:1024
	v_mov_b32_e32 v104, v99
	v_mov_b32_e32 v105, v98
	v_pk_mul_f32 v[98:99], v[104:105], v[100:101] op_sel_hi:[1,0]
	v_mov_b32_e32 v104, v83
	v_mov_b32_e32 v105, v82
	v_pk_mul_f32 v[82:83], v[104:105], v[100:101] op_sel_hi:[1,0]
	v_pk_mov_b32 v[100:101], v[92:93], v[88:89] op_sel:[1,0]
	v_mov_b32_e32 v104, v92
	v_mov_b32_e32 v105, v89
	v_pk_add_f32 v[100:101], v[100:101], v[104:105]
	v_pk_mov_b32 v[104:105], v[94:95], v[86:87] op_sel:[1,0]
	v_mov_b32_e32 v107, v87
	v_pk_add_f32 v[104:105], v[104:105], v[106:107]
	v_pk_fma_f32 v[82:83], v[16:17], v[82:83], v[32:33]
	v_pk_fma_f32 v[98:99], v[14:15], v[98:99], v[30:31]
	v_add_f32_e32 v69, v100, v101
	v_pk_add_f32 v[104:105], v[104:105], v[104:105] op_sel_hi:[0,1]
	v_add_f32_e32 v101, 0, v69
	v_add_f32_e32 v107, v96, v97
	v_add_f32_e32 v109, v84, v85
	v_mov_b32_e32 v106, v98
	v_mov_b32_e32 v108, v99
	v_mov_b32_e32 v104, v82
	v_mov_b32_e32 v100, v83
	v_pk_add_f32 v[106:107], v[106:107], v[108:109]
	v_pk_add_f32 v[100:101], v[104:105], v[100:101]
	s_nop 0
	v_pk_add_f32 v[100:101], v[106:107], v[100:101]
	s_nop 0
	v_add_f32_e32 v69, v100, v101
	s_nop 1
	v_add_f32_dpp v69, v69, v69 quad_perm:[1,0,3,2] row_mask:0xf bank_mask:0xf bound_ctrl:1
	s_nop 1
	v_add_f32_dpp v69, v69, v69 quad_perm:[2,3,0,1] row_mask:0xf bank_mask:0xf bound_ctrl:1
	s_nop 1
	v_add_f32_dpp v69, v69, v69 row_half_mirror row_mask:0xf bank_mask:0xf bound_ctrl:1
	s_nop 1
	v_add_f32_dpp v69, v69, v69 row_mirror row_mask:0xf bank_mask:0xf bound_ctrl:1
	s_nop 0
	v_readlane_b32 s20, v69, 16
	v_readlane_b32 s21, v69, 48
	v_readlane_b32 s4, v69, 0
	v_readlane_b32 s5, v69, 32
	v_mov_b32_e32 v100, s20
	v_mov_b32_e32 v101, s21
	v_pk_add_f32 v[100:101], s[4:5], v[100:101]
	s_nop 0
	v_add_f32_e32 v69, v100, v101
	v_fmac_f32_e32 v93, 0xba800000, v69
	v_fmamk_f32 v92, v69, 0xba800000, v92
	v_mul_f32_e32 v101, v93, v93
	v_fmac_f32_e32 v101, v92, v92
	v_fmamk_f32 v88, v69, 0xba800000, v88
	v_fmac_f32_e32 v101, v88, v88
	v_fmac_f32_e32 v89, 0xba800000, v69
	v_fmac_f32_e32 v101, v89, v89
	v_fmamk_f32 v94, v69, 0xba800000, v94
	v_fmac_f32_e32 v101, v94, v94
	v_fmac_f32_e32 v95, 0xba800000, v69
	v_fmac_f32_e32 v101, v95, v95
	v_fmamk_f32 v86, v69, 0xba800000, v86
	v_fmac_f32_e32 v101, v86, v86
	v_fmac_f32_e32 v87, 0xba800000, v69
	v_fmac_f32_e32 v101, v87, v87
	v_fmamk_f32 v96, v69, 0xba800000, v96
	v_fmac_f32_e32 v101, v96, v96
	v_fmac_f32_e32 v97, 0xba800000, v69
	v_mul_f32_e32 v100, 0x3a800000, v69
	v_fmac_f32_e32 v101, v97, v97
	v_pk_add_f32 v[84:85], v[84:85], v[100:101] op_sel_hi:[1,0] neg_lo:[0,1] neg_hi:[0,1]
	s_nop 0
	v_pk_mul_f32 v[104:105], v[84:85], v[84:85]
	s_nop 0
	v_add_f32_e32 v69, v104, v101
	v_add_f32_e32 v69, v105, v69
	v_pk_add_f32 v[104:105], v[98:99], v[100:101] op_sel_hi:[1,0] neg_lo:[0,1] neg_hi:[0,1]
	v_pk_add_f32 v[100:101], v[82:83], v[100:101] op_sel_hi:[1,0] neg_lo:[0,1] neg_hi:[0,1]
	v_pk_mul_f32 v[106:107], v[104:105], v[104:105]
	v_cvt_pk_bf16_f32 v98, v98, v99
	v_cvt_pk_bf16_f32 v99, v82, v83
	global_store_dwordx2 v[102:103], v[98:99], off offset:1536
	v_add_f32_e32 v69, v106, v69
	v_add_f32_e32 v69, v107, v69
	v_pk_mul_f32 v[106:107], v[100:101], v[100:101]
	s_waitcnt vmcnt(0)
; DEVI unsigned cvt_pk_bf16(float lo, float hi) { unsigned r; asm volatile("v_cvt_pk_bf16_f32 %0, %1, %2" : "=v"(r) : "v"(lo), "v"(hi)); return r; }
; DEVI float bflo(unsigned w) { return __uint_as_float(w << 16); }
; DEVI float bfhi(unsigned w) { return __uint_as_float(w & 0xffff0000u); }
; DEVI void st_bf4(bf16_t* p, f32x4 v) { u32x2 w; w.x = cvt_pk_bf16(v[0], v[1]); w.y = cvt_pk_bf16(v[2], v[3]); *(u32x2*)p = w; }
; DEVI void write_h_reg(const f32x4 (&v)[4], const f32x4 (&sh)[4], const f32x4 (&sc)[4], bf16_t* hrow, int lane) {
;     float mu, rstd; row_stats(v, mu, rstd);
; #pragma unroll
;     for (int i = 0; i < 4; ++i) { float o[4];
; #pragma unroll
;         for (int j = 0; j < 4; ++j) o[j] = (v[i][j] - mu) * rstd * (1.f + sc[i][j]) + sh[i][j];
;         u32x2 w; w.x = cvt_pk_bf16(o[0], o[1]); w.y = cvt_pk_bf16(o[2], o[3]);
;         *(u32x2*)(hrow + lane * 4 + 256 * i) = w; }
; }
; DEVI void phase_ln_mid(const Params& p, int l) {
;     ...
;     for (int t = gw; t < T_; t += nw) {
;         const int b = t >> 12; f32x4 v[4]; const int tn = t + nw < T_ ? t + nw : t;
; #pragma unroll
;         for (int i = 0; i < 4; ++i) { v[i] = (f32x4){bflo(rw[i].x), bfhi(rw[i].x), bflo(rw[i].y), bfhi(rw[i].y)}; rn[i] = *(const u32x2*)(xab + (size_t)tn * 1024 + lane * 4 + 256 * i); }
;         if (b != bcur) { bcur = b; const float* ad = p.ada + ((size_t)l * 8 + b) * 6144;
; #pragma unroll
;             for (int i = 0; i < 4; ++i) { sh4[i] = *(const f32x4*)(ad + 3072 + lane * 4 + 256 * i); sc4[i] = *(const f32x4*)(ad + 4096 + lane * 4 + 256 * i); } }
;         float mu, rstd; row_stats(v, mu, rstd);
; #pragma unroll
;         for (int i = 0; i < 4; ++i) { const int c = lane * 4 + 256 * i; v[i] = (v[i] - mu) * rstd * lg4[i] + lb4[i]; st_bf4(xab + (size_t)t * 1024 + c, v[i]); }
;         write_h_reg(v, sh4, sc4, hb + (size_t)t * 1024, lane);
; #pragma unroll
;         for (int i = 0; i < 4; ++i) rw[i] = rn[i];
;     }
	v_add_f32_e32 v98, 1.0, v34
	v_add_f32_e32 v69, v106, v69
	v_add_f32_e32 v69, v107, v69
	s_nop 1
	v_add_f32_dpp v69, v69, v69 quad_perm:[1,0,3,2] row_mask:0xf bank_mask:0xf bound_ctrl:1
	s_nop 1
	v_add_f32_dpp v69, v69, v69 quad_perm:[2,3,0,1] row_mask:0xf bank_mask:0xf bound_ctrl:1
	s_nop 1
	v_add_f32_dpp v69, v69, v69 row_half_mirror row_mask:0xf bank_mask:0xf bound_ctrl:1
	s_nop 1
	v_add_f32_dpp v69, v69, v69 row_mirror row_mask:0xf bank_mask:0xf bound_ctrl:1
	s_nop 0
	v_readlane_b32 s20, v69, 16
	v_readlane_b32 s21, v69, 48
	v_readlane_b32 s4, v69, 0
	v_readlane_b32 s5, v69, 32
	v_mov_b32_e32 v106, s20
	v_mov_b32_e32 v107, s21
	v_pk_add_f32 v[106:107], s[4:5], v[106:107]
	s_nop 0
	v_add_f32_e32 v69, v106, v107
	v_fmamk_f32 v69, v69, 0x3a800000, v90
	v_mul_f32_e32 v106, 0x4b800000, v69
	v_cmp_gt_f32_e32 vcc, s23, v69
	s_nop 1
	v_cndmask_b32_e32 v69, v69, v106, vcc
	v_rsq_f32_e32 v69, v69
	s_nop 0
	v_mul_f32_e32 v82, 0x45800000, v69
	v_cndmask_b32_e32 v69, v69, v82, vcc
	v_mul_f32_e32 v92, v92, v69
	v_fma_f32 v92, v98, v92, v38
	v_mul_f32_e32 v93, v93, v69
	v_add_f32_e32 v98, 1.0, v35
	v_fma_f32 v93, v98, v93, v39
	v_mul_f32_e32 v88, v88, v69
	v_add_f32_e32 v98, 1.0, v36
	v_fma_f32 v98, v98, v88, v40
	v_mul_f32_e32 v88, v89, v69
	v_add_f32_e32 v89, 1.0, v37
	v_fma_f32 v89, v89, v88, v41
	v_lshl_add_u64 v[82:83], s[10:11], 0, v[70:71]
	v_cvt_pk_bf16_f32 v88, v92, v93
	v_cvt_pk_bf16_f32 v89, v98, v89
	global_store_dwordx2 v[82:83], v[88:89], off
	v_mul_f32_e32 v88, v94, v69
	v_add_f32_e32 v89, 1.0, v42
	v_fma_f32 v88, v89, v88, v50
	v_mul_f32_e32 v89, v95, v69
	v_add_f32_e32 v92, 1.0, v43
	v_fma_f32 v89, v92, v89, v51
	v_mul_f32_e32 v86, v86, v69
	v_add_f32_e32 v92, 1.0, v44
	v_fma_f32 v92, v92, v86, v52
	v_mul_f32_e32 v86, v87, v69
	v_add_f32_e32 v87, 1.0, v45
	v_fma_f32 v87, v87, v86, v53
	v_cvt_pk_bf16_f32 v86, v88, v89
	v_cvt_pk_bf16_f32 v87, v92, v87
	global_store_dwordx2 v[82:83], v[86:87], off offset:512
	v_mul_f32_e32 v86, v96, v69
	v_add_f32_e32 v87, 1.0, v46
	v_fma_f32 v86, v87, v86, v58
	v_mul_f32_e32 v87, v97, v69
	v_add_f32_e32 v88, 1.0, v47
	v_fma_f32 v87, v88, v87, v59
	v_mul_f32_e32 v84, v84, v69
	v_add_f32_e32 v88, 1.0, v48
	v_fma_f32 v88, v88, v84, v60
	v_mul_f32_e32 v84, v85, v69
	v_add_f32_e32 v85, 1.0, v49
	v_fma_f32 v85, v85, v84, v61
	v_cvt_pk_bf16_f32 v84, v86, v87
	v_cvt_pk_bf16_f32 v85, v88, v85
	global_store_dwordx2 v[82:83], v[84:85], off offset:1024
	v_mul_f32_e32 v84, v104, v69
	v_add_f32_e32 v85, 1.0, v54
	v_fma_f32 v84, v85, v84, v62
	v_mul_f32_e32 v85, v105, v69
	v_add_f32_e32 v86, 1.0, v55
	v_fma_f32 v85, v86, v85, v63
	v_mul_f32_e32 v86, v100, v69
	v_add_f32_e32 v87, 1.0, v56
	v_fma_f32 v86, v87, v86, v64
	v_mul_f32_e32 v69, v101, v69
	v_add_f32_e32 v87, 1.0, v57
	v_fma_f32 v69, v87, v69, v65
	v_cvt_pk_bf16_f32 v84, v84, v85
	v_cvt_pk_bf16_f32 v85, v86, v69
	global_store_dwordx2 v[82:83], v[84:85], off offset:1536
	v_lshl_add_u64 v[70:71], v[70:71], 0, s[18:19]
	v_mov_b64_e32 v[82:83], v[80:81]
	v_mov_b64_e32 v[84:85], v[78:79]
	v_mov_b64_e32 v[86:87], v[76:77]
	v_mov_b64_e32 v[88:89], v[74:75]
	s_andn2_b64 exec, exec, s[12:13]
	s_cbranch_execz .LBB0_1085
.LBB0_1083:
	v_mov_b32_e32 v69, v68
	v_add_u32_e32 v68, s86, v69
	v_cmp_gt_i32_e32 vcc, s22, v68
	s_nop 1
	v_cndmask_b32_e32 v74, v69, v68, vcc
	v_ashrrev_i32_e32 v75, 31, v74
	v_lshlrev_b64 v[74:75], 11, v[74:75]
	v_lshl_add_u64 v[92:93], v[72:73], 0, v[74:75]
	global_load_dwordx2 v[74:75], v[92:93], off
	global_load_dwordx2 v[76:77], v[92:93], off offset:512
	global_load_dwordx2 v[78:79], v[92:93], off offset:1024
	global_load_dwordx2 v[80:81], v[92:93], off offset:1536
	v_cmp_lt_i32_e32 vcc, s2, v68
	v_ashrrev_i32_e32 v69, 12, v69
	v_cmp_ne_u32_e64 s[4:5], v69, v91
	s_or_b64 s[12:13], vcc, s[12:13]
	s_and_saveexec_b64 s[20:21], s[4:5]
	s_cbranch_execz .LBB0_1082
	s_load_dwordx2 s[4:5], s[8:9], 0x108
	v_mul_hi_i32_i24_e32 v35, 0x6000, v69
	v_mul_i32_i24_e32 v34, 0x6000, v69
	v_mov_b32_e32 v91, v69
	s_waitcnt lgkmcnt(0)
	v_lshl_add_u64 v[34:35], s[4:5], 0, v[34:35]
	v_lshl_add_u64 v[34:35], v[34:35], 0, v[66:67]
	v_add_co_u32_e32 v96, vcc, 0x3000, v34
	v_lshl_add_u64 v[92:93], v[34:35], 0, s[14:15]
	s_nop 0
	v_addc_co_u32_e32 v97, vcc, 0, v35, vcc
	v_add_co_u32_e32 v98, vcc, 0x4000, v34
	v_lshl_add_u64 v[94:95], v[34:35], 0, s[16:17]
	s_nop 0
	v_addc_co_u32_e32 v99, vcc, 0, v35, vcc
	global_load_dwordx4 v[38:41], v[96:97], off
	global_load_dwordx4 v[34:37], v[98:99], off
	global_load_dwordx4 v[50:53], v[92:93], off offset:1024
	global_load_dwordx4 v[58:61], v[92:93], off offset:2048
	global_load_dwordx4 v[42:45], v[94:95], off offset:1024
	global_load_dwordx4 v[62:65], v[92:93], off offset:3072
	global_load_dwordx4 v[46:49], v[94:95], off offset:2048
	global_load_dwordx4 v[54:57], v[94:95], off offset:3072
	s_branch .LBB0_1082

; DEVI int vtid() { return tidx() & 255; }
; DEVI int vbid() { return bidx() * 2 + vhb(); }
; DEVI int vgrid() { return (int)gridDim.x * 2; }
; DEVI void phase_combine(const Params& p, char* smem, int l) {
;     const int lane = vtid() & 63, gw = vbid() * 4 + (vtid() >> 6), nw = vgrid() * 4;
;     const MoeTab mt = moe_tables(p, smem + 61440, l, vtid());
;     float* xo = p.out; bf16_t* xob = p.xb; bf16_t* hb = p.h; const bf16_t* xab = p.xa; const unsigned char* ysl = p.yslot; const int* tke = p.tok_e; const int* tkp = p.tok_pos;
;     asm volatile("" : "+s"(xo), "+s"(xob), "+s"(hb), "+s"(xab), "+s"(ysl), "+s"(tke), "+s"(tkp));
;     size_t slot_nx = (size_t)T_ * 8 + gw;
;     if (lane < 8 && gw < T_) slot_nx = (size_t)mt.rstart[tke[gw * 8 + lane]] + tkp[gw * 8 + lane];
.LBB0_1727:
	s_or_b64 exec, exec, s[4:5]
	s_lshr_b32 s4, s11, 6
	s_lshl_b32 s24, s10, 3
	s_and_b32 s41, s4, 0x3fffffc
	s_waitcnt lgkmcnt(0)
	s_barrier
	s_load_dwordx2 s[4:5], s[16:17], 0xf0
	s_load_dwordx4 s[8:11], s[16:17], 0x160
	s_load_dwordx2 s[18:19], s[16:17], 0x170
	s_load_dwordx4 s[12:15], s[16:17], 0x1f0
	s_load_dwordx2 s[6:7], s[16:17], 0x228
	s_add_i32 s25, s41, s24
	v_and_b32_e32 v34, 63, v5
	v_bfe_u32 v35, v4, 6, 2
	s_waitcnt lgkmcnt(0)
	s_cmpk_lt_u32 s25, 0x8000
	v_or_b32_e32 v137, s25, v35
	v_cmp_gt_u32_e64 s[4:5], 8, v34
	s_cselect_b64 s[20:21], -1, 0
	v_add_u32_e32 v82, 0x40000, v137
	s_and_b64 s[26:27], s[4:5], s[20:21]
	s_and_saveexec_b64 s[22:23], s[26:27]
	s_cbranch_execz .LBB0_1729
	v_lshl_or_b32 v2, v137, 3, v34
	v_mov_b32_e32 v3, 0
	v_lshlrev_b64 v[2:3], 2, v[2:3]
	v_lshl_add_u64 v[4:5], s[12:13], 0, v[2:3]
	global_load_dword v4, v[4:5], off
	v_lshl_add_u64 v[2:3], s[14:15], 0, v[2:3]
	global_load_dword v2, v[2:3], off
	s_waitcnt vmcnt(0) lgkmcnt(0)
	v_lshl_add_u32 v3, v4, 2, s2
	ds_read_b32 v3, v3 offset:61440
	s_waitcnt lgkmcnt(0)
	v_add_u32_e32 v82, v2, v3

; DEVI void phase_combine(const Params& p, char* smem, int l) {
;     ...
; #pragma unroll
;         for (int k = 0; k < 9; ++k)
; #pragma unroll
;             for (int i = 0; i < 4; ++i) { const f32x2 lo = __builtin_amdgcn_cvt_pk_f32_fp8((int)w[k][i], false), hi = __builtin_amdgcn_cvt_pk_f32_fp8((int)w[k][i], true);
;                 f[i][0] += lo[0]; f[i][1] += lo[1]; f[i][2] += hi[0]; f[i][3] += hi[1]; }
.LBB0_1731:
	s_or_b64 exec, exec, s[6:7]
	s_waitcnt vmcnt(0) lgkmcnt(0)
	v_cvt_pk_f32_fp8_e32 v[138:139], v122
	v_cvt_pk_f32_fp8_sdwa v[140:141], v122 src0_sel:WORD_1
	v_cvt_pk_f32_fp8_e32 v[142:143], v123
	v_cvt_pk_f32_fp8_sdwa v[122:123], v123 src0_sel:WORD_1
	v_cvt_pk_f32_fp8_e32 v[150:151], v114
	v_cvt_pk_f32_fp8_sdwa v[152:153], v114 src0_sel:WORD_1
	v_cvt_pk_f32_fp8_e32 v[154:155], v115
	v_cvt_pk_f32_fp8_sdwa v[114:115], v115 src0_sel:WORD_1
	v_cvt_pk_f32_fp8_e32 v[162:163], v118
	v_cvt_pk_f32_fp8_sdwa v[164:165], v118 src0_sel:WORD_1
	v_cvt_pk_f32_fp8_e32 v[166:167], v119
	v_cvt_pk_f32_fp8_sdwa v[118:119], v119 src0_sel:WORD_1
	v_cvt_pk_f32_fp8_e32 v[174:175], v106
	v_cvt_pk_f32_fp8_sdwa v[176:177], v106 src0_sel:WORD_1
	v_cvt_pk_f32_fp8_e32 v[178:179], v107
	v_cvt_pk_f32_fp8_sdwa v[106:107], v107 src0_sel:WORD_1
	v_cvt_pk_f32_fp8_sdwa v[146:147], v124 src0_sel:WORD_1
	v_cvt_pk_f32_fp8_e32 v[186:187], v110
	v_cvt_pk_f32_fp8_sdwa v[188:189], v110 src0_sel:WORD_1
	v_cvt_pk_f32_fp8_e32 v[190:191], v111
	v_cvt_pk_f32_fp8_sdwa v[110:111], v111 src0_sel:WORD_1
	v_pk_add_f32 v[142:143], v[142:143], 0 op_sel_hi:[1,0]
	v_pk_add_f32 v[122:123], v[122:123], 0 op_sel_hi:[1,0]
	v_cvt_pk_f32_fp8_sdwa v[158:159], v116 src0_sel:WORD_1
	v_cvt_pk_f32_fp8_e32 v[198:199], v98
	v_cvt_pk_f32_fp8_sdwa v[200:201], v98 src0_sel:WORD_1
	v_cvt_pk_f32_fp8_e32 v[202:203], v99
	v_cvt_pk_f32_fp8_sdwa v[98:99], v99 src0_sel:WORD_1
	v_pk_add_f32 v[114:115], v[122:123], v[114:115]
	v_pk_add_f32 v[122:123], v[142:143], v[154:155]
	v_cvt_pk_f32_fp8_sdwa v[170:171], v120 src0_sel:WORD_1
	v_cvt_pk_f32_fp8_e32 v[210:211], v102
	v_cvt_pk_f32_fp8_sdwa v[212:213], v102 src0_sel:WORD_1
	v_cvt_pk_f32_fp8_e32 v[214:215], v103
	v_cvt_pk_f32_fp8_sdwa v[102:103], v103 src0_sel:WORD_1
	v_pk_add_f32 v[122:123], v[122:123], v[166:167]
	v_pk_add_f32 v[114:115], v[114:115], v[118:119]
	v_cvt_pk_f32_fp8_e32 v[144:145], v124
	v_cvt_pk_f32_fp8_sdwa v[182:183], v108 src0_sel:WORD_1
	v_cvt_pk_f32_fp8_e32 v[222:223], v94
	v_cvt_pk_f32_fp8_sdwa v[224:225], v94 src0_sel:WORD_1
	v_cvt_pk_f32_fp8_e32 v[226:227], v95
	v_cvt_pk_f32_fp8_sdwa v[94:95], v95 src0_sel:WORD_1
	v_pk_add_f32 v[106:107], v[114:115], v[106:107]
	v_pk_add_f32 v[114:115], v[122:123], v[178:179]
	v_cvt_pk_f32_fp8_e32 v[156:157], v116
	v_cvt_pk_f32_fp8_sdwa v[194:195], v112 src0_sel:WORD_1
	v_pk_add_f32 v[114:115], v[114:115], v[190:191]
	v_pk_add_f32 v[106:107], v[106:107], v[110:111]
	v_pk_add_f32 v[110:111], v[146:147], 0 op_sel_hi:[1,0]
	v_cvt_pk_f32_fp8_e32 v[168:169], v120
	v_cvt_pk_f32_fp8_sdwa v[206:207], v100 src0_sel:WORD_1
	v_pk_add_f32 v[98:99], v[106:107], v[98:99]
	v_pk_add_f32 v[106:107], v[114:115], v[202:203]
	v_pk_add_f32 v[110:111], v[110:111], v[158:159]
	v_cvt_pk_f32_fp8_e32 v[180:181], v108
	v_cvt_pk_f32_fp8_sdwa v[218:219], v104 src0_sel:WORD_1
	v_pk_add_f32 v[138:139], v[138:139], 0 op_sel_hi:[1,0]
	v_pk_add_f32 v[106:107], v[106:107], v[214:215]
	v_pk_add_f32 v[98:99], v[98:99], v[102:103]
	v_pk_add_f32 v[110:111], v[110:111], v[170:171]
	v_cvt_pk_f32_fp8_e32 v[148:149], v125
	v_cvt_pk_f32_fp8_sdwa v[124:125], v125 src0_sel:WORD_1
	v_cvt_pk_f32_fp8_e32 v[192:193], v112
	v_cvt_pk_f32_fp8_sdwa v[230:231], v96 src0_sel:WORD_1
	v_cvt_pk_f32_fp8_e32 v[234:235], v90
	v_cvt_pk_f32_fp8_sdwa v[236:237], v90 src0_sel:WORD_1
	v_pk_add_f32 v[138:139], v[138:139], v[150:151]
	v_cvt_pk_f32_fp8_e32 v[150:151], v91
	v_cvt_pk_f32_fp8_sdwa v[90:91], v91 src0_sel:WORD_1
	v_pk_add_f32 v[94:95], v[98:99], v[94:95]
	v_pk_add_f32 v[98:99], v[106:107], v[226:227]
	v_pk_add_f32 v[106:107], v[144:145], 0 op_sel_hi:[1,0]
	v_pk_add_f32 v[110:111], v[110:111], v[182:183]
	v_cvt_pk_f32_fp8_e32 v[160:161], v117
	v_cvt_pk_f32_fp8_sdwa v[116:117], v117 src0_sel:WORD_1
	v_cvt_pk_f32_fp8_e32 v[204:205], v100
	v_cvt_pk_f32_fp8_sdwa v[102:103], v92 src0_sel:WORD_1
	v_pk_add_f32 v[106:107], v[106:107], v[156:157]
	v_pk_add_f32 v[110:111], v[110:111], v[194:195]
	v_cvt_pk_f32_fp8_e32 v[172:173], v121
	v_cvt_pk_f32_fp8_sdwa v[120:121], v121 src0_sel:WORD_1
	v_cvt_pk_f32_fp8_e32 v[216:217], v104
	v_pk_add_f32 v[140:141], v[140:141], 0 op_sel_hi:[1,0]
	v_pk_add_f32 v[106:107], v[106:107], v[168:169]
	v_pk_add_f32 v[110:111], v[110:111], v[206:207]
	v_cvt_pk_f32_fp8_e32 v[184:185], v109
	v_cvt_pk_f32_fp8_sdwa v[108:109], v109 src0_sel:WORD_1
	v_cvt_pk_f32_fp8_e32 v[228:229], v96
	v_pk_add_f32 v[140:141], v[140:141], v[152:153]
	v_pk_add_f32 v[106:107], v[106:107], v[180:181]
	v_pk_add_f32 v[110:111], v[110:111], v[218:219]
	v_cvt_pk_f32_fp8_e32 v[196:197], v113
	v_cvt_pk_f32_fp8_sdwa v[112:113], v113 src0_sel:WORD_1
	v_pk_add_f32 v[140:141], v[140:141], v[164:165]
	v_pk_add_f32 v[90:91], v[94:95], v[90:91]
	v_cvt_pk_f32_fp8_e32 v[94:95], v92
	v_pk_add_f32 v[106:107], v[106:107], v[192:193]
	v_pk_add_f32 v[110:111], v[110:111], v[230:231]
	v_pk_add_f32 v[114:115], v[124:125], 0 op_sel_hi:[1,0]
	v_cvt_pk_f32_fp8_e32 v[208:209], v101
	v_cvt_pk_f32_fp8_sdwa v[100:101], v101 src0_sel:WORD_1
	v_pk_add_f32 v[140:141], v[140:141], v[176:177]
	v_pk_add_f32 v[106:107], v[106:107], v[204:205]
	v_pk_add_f32 v[102:103], v[110:111], v[102:103]
	v_pk_add_f32 v[110:111], v[148:149], 0 op_sel_hi:[1,0]
	v_pk_add_f32 v[114:115], v[114:115], v[116:117]
	v_cvt_pk_f32_fp8_e32 v[220:221], v105
	v_cvt_pk_f32_fp8_sdwa v[104:105], v105 src0_sel:WORD_1
	v_pk_add_f32 v[138:139], v[138:139], v[162:163]
	v_pk_add_f32 v[140:141], v[140:141], v[188:189]
	v_pk_add_f32 v[106:107], v[106:107], v[216:217]
	v_pk_add_f32 v[110:111], v[110:111], v[160:161]
	v_pk_add_f32 v[114:115], v[114:115], v[120:121]
	v_cvt_pk_f32_fp8_e32 v[232:233], v97
	v_cvt_pk_f32_fp8_sdwa v[96:97], v97 src0_sel:WORD_1
; DEVI float bflo(unsigned w) { return __uint_as_float(w << 16); }
; DEVI float bfhi(unsigned w) { return __uint_as_float(w & 0xffff0000u); }
; DEVI void phase_combine(const Params& p, char* smem, int l) {
;     ...
; #pragma unroll
;         for (int k = 0; k < 9; ++k)
; #pragma unroll
;             for (int i = 0; i < 4; ++i) { const f32x2 lo = __builtin_amdgcn_cvt_pk_f32_fp8((int)w[k][i], false), hi = __builtin_amdgcn_cvt_pk_f32_fp8((int)w[k][i], true);
;                 f[i][0] += lo[0]; f[i][1] += lo[1]; f[i][2] += hi[0]; f[i][3] += hi[1]; }
;         f32x4 v[4];
; #pragma unroll
;         for (int i = 0; i < 4; ++i) { const unsigned x0 = i < 2 ? xr0[2 * i] : xr1[2 * i - 4], x1 = i < 2 ? xr0[2 * i + 1] : xr1[2 * i - 3];
;             v[i] = (f32x4){bflo(x0), bfhi(x0), bflo(x1), bfhi(x1)} * ALPHA + gate4[i] * (f[i] * (1.f / YS_SCALE)); }
;         float mu, rstd; row_stats(v, mu, rstd);
; #pragma unroll
;         for (int i = 0; i < 4; ++i) v[i] = (v[i] - mu) * rstd * lg4[i] + lb4[i];
	v_pk_add_f32 v[138:139], v[138:139], v[174:175]
	v_pk_add_f32 v[140:141], v[140:141], v[200:201]
	v_pk_add_f32 v[106:107], v[106:107], v[228:229]
	v_pk_add_f32 v[110:111], v[110:111], v[172:173]
	v_pk_add_f32 v[108:109], v[114:115], v[108:109]
	v_pk_add_f32 v[138:139], v[138:139], v[186:187]
	v_pk_add_f32 v[140:141], v[140:141], v[212:213]
	v_pk_add_f32 v[94:95], v[106:107], v[94:95]
	v_cvt_pk_f32_fp8_e32 v[106:107], v93
	v_cvt_pk_f32_fp8_sdwa v[92:93], v93 src0_sel:WORD_1
	v_pk_add_f32 v[110:111], v[110:111], v[184:185]
	v_pk_add_f32 v[108:109], v[108:109], v[112:113]
	v_pk_add_f32 v[138:139], v[138:139], v[198:199]
	v_pk_add_f32 v[140:141], v[140:141], v[224:225]
	v_pk_add_f32 v[110:111], v[110:111], v[196:197]
	v_pk_add_f32 v[100:101], v[108:109], v[100:101]
	v_pk_add_f32 v[138:139], v[138:139], v[210:211]
	v_pk_add_f32 v[140:141], v[140:141], v[236:237]
	v_pk_add_f32 v[108:109], v[110:111], v[208:209]
	v_pk_add_f32 v[100:101], v[100:101], v[104:105]
	v_pk_add_f32 v[138:139], v[138:139], v[222:223]
	v_pk_add_f32 v[98:99], v[98:99], v[150:151]
	v_pk_add_f32 v[108:109], v[108:109], v[220:221]
	v_pk_add_f32 v[96:97], v[100:101], v[96:97]
	v_pk_mul_f32 v[104:105], v[140:141], s[30:31] op_sel_hi:[1,0]
	v_pk_add_f32 v[138:139], v[138:139], v[234:235]
	v_pk_add_f32 v[100:101], v[108:109], v[232:233]
	v_pk_add_f32 v[92:93], v[96:97], v[92:93]
	v_lshlrev_b32_e32 v96, 16, v86
	v_and_b32_e32 v97, 0xffff0000, v86
	v_lshlrev_b32_e32 v86, 16, v87
	v_and_b32_e32 v87, 0xffff0000, v87
	v_pk_mul_f32 v[104:105], v[36:37], v[104:105]
	v_pk_mul_f32 v[90:91], v[90:91], s[30:31] op_sel_hi:[1,0]
	v_pk_mul_f32 v[98:99], v[98:99], s[30:31] op_sel_hi:[1,0]
	v_pk_add_f32 v[100:101], v[100:101], v[106:107]
	v_pk_mul_f32 v[106:107], v[138:139], s[30:31] op_sel_hi:[1,0]
	v_pk_fma_f32 v[86:87], v[86:87], s[34:35], v[104:105] op_sel_hi:[1,0,1]
	v_lshlrev_b32_e32 v104, 16, v88
	v_and_b32_e32 v105, 0xffff0000, v88
	v_lshlrev_b32_e32 v88, 16, v89
	v_and_b32_e32 v89, 0xffff0000, v89
	v_pk_mul_f32 v[98:99], v[38:39], v[98:99]
	v_pk_mul_f32 v[90:91], v[40:41], v[90:91]
	v_pk_mul_f32 v[94:95], v[94:95], s[30:31] op_sel_hi:[1,0]
	v_pk_mul_f32 v[106:107], v[34:35], v[106:107]
	v_pk_fma_f32 v[88:89], v[88:89], s[34:35], v[90:91] op_sel_hi:[1,0,1]
	v_pk_fma_f32 v[90:91], v[104:105], s[34:35], v[98:99] op_sel_hi:[1,0,1]
	v_lshlrev_b32_e32 v98, 16, v82
	v_and_b32_e32 v99, 0xffff0000, v82
	v_pk_mul_f32 v[94:95], v[42:43], v[94:95]
	v_pk_mul_f32 v[92:93], v[92:93], s[30:31] op_sel_hi:[1,0]
	v_pk_mul_f32 v[100:101], v[100:101], s[30:31] op_sel_hi:[1,0]
	v_pk_fma_f32 v[96:97], v[96:97], s[34:35], v[106:107] op_sel_hi:[1,0,1]
	v_pk_mul_f32 v[102:103], v[102:103], s[30:31] op_sel_hi:[1,0]
	v_pk_fma_f32 v[94:95], v[98:99], s[34:35], v[94:95] op_sel_hi:[1,0,1]
	v_lshlrev_b32_e32 v98, 16, v84
	v_and_b32_e32 v99, 0xffff0000, v84
	v_lshlrev_b32_e32 v84, 16, v85
	v_and_b32_e32 v85, 0xffff0000, v85
	v_pk_mul_f32 v[100:101], v[46:47], v[100:101]
	v_pk_mul_f32 v[92:93], v[48:49], v[92:93]
	v_lshlrev_b32_e32 v82, 16, v83
	v_and_b32_e32 v83, 0xffff0000, v83
	v_pk_mul_f32 v[102:103], v[44:45], v[102:103]
	v_pk_fma_f32 v[84:85], v[84:85], s[34:35], v[92:93] op_sel_hi:[1,0,1]
	v_pk_fma_f32 v[92:93], v[98:99], s[34:35], v[100:101] op_sel_hi:[1,0,1]
	v_pk_mov_b32 v[98:99], v[96:97], v[86:87] op_sel:[1,0]
	v_mov_b32_e32 v100, v96
	v_mov_b32_e32 v101, v87
	v_pk_fma_f32 v[82:83], v[82:83], s[34:35], v[102:103] op_sel_hi:[1,0,1]
	v_pk_add_f32 v[98:99], v[98:99], v[100:101]
	v_pk_mov_b32 v[100:101], v[90:91], v[88:89] op_sel:[1,0]
	v_mov_b32_e32 v102, v90
	v_mov_b32_e32 v103, v89
	v_pk_add_f32 v[100:101], v[100:101], v[102:103]
	v_add_f32_e32 v98, v98, v99
	v_pk_add_f32 v[100:101], v[100:101], v[100:101] op_sel:[0,1] op_sel_hi:[1,0]
	v_add_f32_e32 v98, 0, v98
	v_add_f32_e32 v102, v94, v95
	v_add_f32_e32 v104, v82, v83
	v_mov_b32_e32 v99, v92
	v_mov_b32_e32 v101, v93
	v_mov_b32_e32 v103, v84
	v_mov_b32_e32 v105, v85
	v_pk_add_f32 v[98:99], v[98:99], v[100:101]
	v_pk_add_f32 v[100:101], v[102:103], v[104:105]
	v_add_u32_e32 v132, s31, v132
	v_pk_add_f32 v[98:99], v[98:99], v[100:101]
	v_mov_b32_e32 v137, v135
	v_add_f32_e32 v98, v98, v99
	s_nop 1
	v_add_f32_dpp v98, v98, v98 quad_perm:[1,0,3,2] row_mask:0xf bank_mask:0xf bound_ctrl:1
	s_nop 1
	v_add_f32_dpp v98, v98, v98 quad_perm:[2,3,0,1] row_mask:0xf bank_mask:0xf bound_ctrl:1
	s_nop 1
	v_add_f32_dpp v98, v98, v98 row_half_mirror row_mask:0xf bank_mask:0xf bound_ctrl:1
	s_nop 1
	v_add_f32_dpp v98, v98, v98 row_mirror row_mask:0xf bank_mask:0xf bound_ctrl:1
	s_nop 0
	v_readlane_b32 s22, v98, 16
	v_readlane_b32 s41, v98, 48
	v_readlane_b32 s6, v98, 0
	v_readlane_b32 s7, v98, 32
	v_mov_b32_e32 v98, s22
	v_mov_b32_e32 v99, s41
	v_pk_add_f32 v[98:99], s[6:7], v[98:99]
	s_nop 0
	v_add_f32_e32 v106, v98, v99
	v_fmamk_f32 v97, v106, 0xba800000, v97
	v_mul_f32_e32 v99, v97, v97
	v_fmac_f32_e32 v96, 0xba800000, v106
	v_fmac_f32_e32 v99, v96, v96
	v_fmamk_f32 v86, v106, 0xba800000, v86
	v_fmac_f32_e32 v99, v86, v86
	v_fmac_f32_e32 v87, 0xba800000, v106
	v_fmac_f32_e32 v99, v87, v87
	v_fmamk_f32 v90, v106, 0xba800000, v90
	v_fmac_f32_e32 v99, v90, v90
	v_fmac_f32_e32 v91, 0xba800000, v106
	v_fmac_f32_e32 v99, v91, v91
	v_fmamk_f32 v88, v106, 0xba800000, v88
	v_fmac_f32_e32 v99, v88, v88
	v_fmac_f32_e32 v89, 0xba800000, v106
	v_fmac_f32_e32 v99, v89, v89
	v_fmamk_f32 v94, v106, 0xba800000, v94
	v_fmac_f32_e32 v99, v94, v94
	v_fmac_f32_e32 v95, 0xba800000, v106
	v_mul_f32_e32 v98, 0x3a800000, v106
	v_fmac_f32_e32 v99, v95, v95
	v_pk_add_f32 v[100:101], v[82:83], v[98:99] op_sel_hi:[1,0] neg_lo:[0,1] neg_hi:[0,1]
	v_fmamk_f32 v83, v106, 0xba800000, v83
; DEVI unsigned cvt_pk_bf16(float lo, float hi) { unsigned r; asm volatile("v_cvt_pk_bf16_f32 %0, %1, %2" : "=v"(r) : "v"(lo), "v"(hi)); return r; }
; DEVI void row_stats(const f32x4 (&v)[4], float& mu, float& rstd) {
;     float s = 0.f;
; #pragma unroll
;     for (int i = 0; i < 4; ++i) s += (v[i][0] + v[i][1]) + (v[i][2] + v[i][3]);
;     mu = wave_sum(s) * (1.f / 1024.f);
;     float q = 0.f;
; #pragma unroll
;     for (int i = 0; i < 4; ++i)
; #pragma unroll
;         for (int j = 0; j < 4; ++j) { const float d = v[i][j] - mu; q += d * d; }
;     rstd = rsqrtf(wave_sum(q) * (1.f / 1024.f) + LN_EPS);
; }
; DEVI void phase_combine(const Params& p, char* smem, int l) {
;     ...
;         float mu, rstd; row_stats(v, mu, rstd);
; #pragma unroll
;         for (int i = 0; i < 4; ++i) v[i] = (v[i] - mu) * rstd * lg4[i] + lb4[i];
;         if (l == NL_ - 1) {
; #pragma unroll
;             for (int i = 0; i < 4; ++i) *(f32x4*)(xo + (size_t)t * 1024 + lane * 16 + 4 * i) = v[i];
;         } else {
;             { const u32x4 o0 = {cvt_pk_bf16(v[0][0], v[0][1]), cvt_pk_bf16(v[0][2], v[0][3]), cvt_pk_bf16(v[1][0], v[1][1]), cvt_pk_bf16(v[1][2], v[1][3])};
;               const u32x4 o1 = {cvt_pk_bf16(v[2][0], v[2][1]), cvt_pk_bf16(v[2][2], v[2][3]), cvt_pk_bf16(v[3][0], v[3][1]), cvt_pk_bf16(v[3][2], v[3][3])};
;               *(u32x4*)(xob + (size_t)t * 1024 + lane * 16) = o0; *(u32x4*)(xob + (size_t)t * 1024 + lane * 16 + 8) = o1; }
;             float mu2, rstd2; row_stats(v, mu2, rstd2); unsigned hw[8];
; #pragma unroll
;             for (int i = 0; i < 4; ++i) { float o[4];
; #pragma unroll
;                 for (int j = 0; j < 4; ++j) o[j] = (v[i][j] - mu2) * rstd2 * (1.f + sc4[i][j]) + sh4[i][j];
;                 hw[2 * i] = cvt_pk_bf16(o[0], o[1]); hw[2 * i + 1] = cvt_pk_bf16(o[2], o[3]); }
	v_pk_mul_f32 v[100:101], v[100:101], v[100:101]
	v_fmac_f32_e32 v82, 0xba800000, v106
	v_add_f32_e32 v99, v100, v99
	v_add_f32_e32 v99, v101, v99
	v_pk_add_f32 v[100:101], v[92:93], v[98:99] op_sel_hi:[1,0] neg_lo:[0,1] neg_hi:[0,1]
	v_fmamk_f32 v93, v106, 0xba800000, v93
	v_pk_mul_f32 v[100:101], v[100:101], v[100:101]
	v_fmac_f32_e32 v92, 0xba800000, v106
	v_add_f32_e32 v99, v100, v99
	v_add_f32_e32 v100, v101, v99
	v_pk_add_f32 v[98:99], v[84:85], v[98:99] op_sel_hi:[1,0] neg_lo:[0,1] neg_hi:[0,1]
	v_fmamk_f32 v85, v106, 0xba800000, v85
	v_pk_mul_f32 v[98:99], v[98:99], v[98:99]
	v_fmac_f32_e32 v84, 0xba800000, v106
	v_add_f32_e32 v98, v98, v100
	v_add_f32_e32 v98, v99, v98
	s_nop 1
	v_add_f32_dpp v98, v98, v98 quad_perm:[1,0,3,2] row_mask:0xf bank_mask:0xf bound_ctrl:1
	s_nop 1
	v_add_f32_dpp v98, v98, v98 quad_perm:[2,3,0,1] row_mask:0xf bank_mask:0xf bound_ctrl:1
	s_nop 1
	v_add_f32_dpp v98, v98, v98 row_half_mirror row_mask:0xf bank_mask:0xf bound_ctrl:1
	s_nop 1
	v_add_f32_dpp v98, v98, v98 row_mirror row_mask:0xf bank_mask:0xf bound_ctrl:1
	s_nop 0
	v_readlane_b32 s22, v98, 16
	v_readlane_b32 s41, v98, 48
	v_readlane_b32 s6, v98, 0
	v_readlane_b32 s7, v98, 32
	v_mov_b32_e32 v98, s22
	v_mov_b32_e32 v99, s41
	v_pk_add_f32 v[98:99], s[6:7], v[98:99]
	s_nop 0
	v_add_f32_e32 v98, v98, v99
	v_fmamk_f32 v98, v98, 0x3a800000, v134
	v_mul_f32_e32 v99, 0x4b800000, v98
	v_cmp_gt_f32_e32 vcc, s40, v98
	s_nop 1
	v_cndmask_b32_e32 v98, v98, v99, vcc
	v_rsq_f32_e32 v98, v98
	s_nop 0
	v_mul_f32_e32 v99, 0x45800000, v98
	v_cndmask_b32_e32 v98, v98, v99, vcc
	v_pk_mul_f32 v[86:87], v[86:87], v[98:99] op_sel_hi:[1,0]
	v_pk_mul_f32 v[96:97], v[96:97], v[98:99] op_sel_hi:[1,0]
	v_pk_fma_f32 v[100:101], v[12:13], v[86:87], v[32:33]
	v_pk_fma_f32 v[96:97], v[10:11], v[96:97], v[30:31]
	v_pk_mul_f32 v[86:87], v[88:89], v[98:99] op_sel_hi:[1,0]
	v_pk_mul_f32 v[88:89], v[90:91], v[98:99] op_sel_hi:[1,0]
	v_pk_fma_f32 v[102:103], v[8:9], v[86:87], v[28:29]
	v_pk_fma_f32 v[90:91], v[6:7], v[88:89], v[26:27]
	v_pk_mov_b32 v[106:107], v[96:97], v[100:101] op_sel:[1,0]
	v_mov_b32_e32 v108, v96
	v_mov_b32_e32 v109, v101
	v_pk_mul_f32 v[82:83], v[82:83], v[98:99] op_sel_hi:[1,0]
	v_pk_add_f32 v[106:107], v[106:107], v[108:109]
	v_pk_mov_b32 v[108:109], v[90:91], v[102:103] op_sel:[1,0]
	v_mov_b32_e32 v110, v90
	v_mov_b32_e32 v111, v103
	v_pk_mul_f32 v[86:87], v[94:95], v[98:99] op_sel_hi:[1,0]
	v_pk_fma_f32 v[104:105], v[4:5], v[82:83], v[24:25]
	v_pk_mul_f32 v[82:83], v[84:85], v[98:99] op_sel_hi:[1,0]
	v_pk_mul_f32 v[84:85], v[92:93], v[98:99] op_sel_hi:[1,0]
	v_pk_add_f32 v[108:109], v[108:109], v[110:111]
	v_pk_fma_f32 v[94:95], v[2:3], v[86:87], v[22:23]
	v_pk_fma_f32 v[92:93], v[14:15], v[84:85], v[18:19]
	v_pk_fma_f32 v[98:99], v[16:17], v[82:83], v[20:21]
	v_add_f32_e32 v106, v106, v107
	v_pk_add_f32 v[108:109], v[108:109], v[108:109] op_sel_hi:[0,1]
	v_add_f32_e32 v107, 0, v106
	v_add_f32_e32 v111, v94, v95
	v_add_f32_e32 v113, v104, v105
	v_mov_b32_e32 v110, v92
	v_mov_b32_e32 v112, v93
	v_mov_b32_e32 v108, v98
	v_mov_b32_e32 v106, v99
	v_pk_add_f32 v[110:111], v[110:111], v[112:113]
	v_pk_add_f32 v[106:107], v[108:109], v[106:107]
	v_cvt_pk_bf16_f32 v82, v96, v97
	v_cvt_pk_bf16_f32 v83, v100, v101
	v_cvt_pk_bf16_f32 v84, v90, v91
	v_cvt_pk_bf16_f32 v85, v102, v103
	v_cvt_pk_bf16_f32 v86, v94, v95
	s_nop 0
	v_pk_add_f32 v[106:107], v[110:111], v[106:107]
	v_cvt_pk_bf16_f32 v87, v104, v105
	v_cvt_pk_bf16_f32 v88, v92, v93
	v_cvt_pk_bf16_f32 v89, v98, v99
	s_nop 0
	v_add_f32_e32 v106, v106, v107
	s_nop 1
	v_add_f32_dpp v106, v106, v106 quad_perm:[1,0,3,2] row_mask:0xf bank_mask:0xf bound_ctrl:1
	s_nop 1
	v_add_f32_dpp v106, v106, v106 quad_perm:[2,3,0,1] row_mask:0xf bank_mask:0xf bound_ctrl:1
	s_nop 1
	v_add_f32_dpp v106, v106, v106 row_half_mirror row_mask:0xf bank_mask:0xf bound_ctrl:1
	s_nop 1
	v_add_f32_dpp v106, v106, v106 row_mirror row_mask:0xf bank_mask:0xf bound_ctrl:1
	s_nop 0
	v_readlane_b32 s22, v106, 16
	v_readlane_b32 s41, v106, 48
	v_readlane_b32 s6, v106, 0
	v_readlane_b32 s7, v106, 32
	v_mov_b32_e32 v106, s22
	v_mov_b32_e32 v107, s41
	v_pk_add_f32 v[106:107], s[6:7], v[106:107]
	s_nop 0
	v_add_f32_e32 v107, v106, v107
	v_fmac_f32_e32 v97, 0xba800000, v107
	v_fmamk_f32 v96, v107, 0xba800000, v96
	v_mul_f32_e32 v110, v97, v97
	v_fmac_f32_e32 v110, v96, v96
	v_fmamk_f32 v100, v107, 0xba800000, v100
	v_fmac_f32_e32 v110, v100, v100
	v_fmac_f32_e32 v101, 0xba800000, v107
	v_fmac_f32_e32 v110, v101, v101
	v_fmamk_f32 v90, v107, 0xba800000, v90
	v_fmac_f32_e32 v110, v90, v90
	v_fmac_f32_e32 v91, 0xba800000, v107
	v_fmac_f32_e32 v110, v91, v91
	v_fmamk_f32 v102, v107, 0xba800000, v102
	v_fmac_f32_e32 v110, v102, v102
	v_fmac_f32_e32 v103, 0xba800000, v107
	v_mul_f32_e32 v106, 0x3a800000, v107
	v_fmac_f32_e32 v110, v103, v103
	v_fmamk_f32 v94, v107, 0xba800000, v94
	v_fmac_f32_e32 v110, v94, v94
	v_fmac_f32_e32 v95, 0xba800000, v107
	v_pk_add_f32 v[104:105], v[104:105], v[106:107] op_sel_hi:[1,0] neg_lo:[0,1] neg_hi:[0,1]
	v_fmac_f32_e32 v110, v95, v95
	v_pk_mul_f32 v[108:109], v[104:105], v[104:105]
	s_nop 0
	v_add_f32_e32 v107, v108, v110
	v_add_f32_e32 v107, v109, v107
	v_pk_add_f32 v[92:93], v[92:93], v[106:107] op_sel_hi:[1,0] neg_lo:[0,1] neg_hi:[0,1]
	s_nop 0
	v_pk_mul_f32 v[108:109], v[92:93], v[92:93]
	s_nop 0
	v_add_f32_e32 v107, v108, v107
	v_pk_add_f32 v[98:99], v[98:99], v[106:107] op_sel_hi:[1,0] neg_lo:[0,1] neg_hi:[0,1]
	v_add_f32_e32 v108, v109, v107
; DEVI unsigned cvt_pk_bf16(float lo, float hi) { unsigned r; asm volatile("v_cvt_pk_bf16_f32 %0, %1, %2" : "=v"(r) : "v"(lo), "v"(hi)); return r; }
; DEVI void phase_combine(const Params& p, char* smem, int l) {
;     ...
;     for (int t = gw; t < T_; t += nw) {
;         const int b = t >> 12;
;         const size_t slot = slot_nx;
;         { const int tn = t + nw; slot_nx = (size_t)T_ * 8 + tn;
;           if (lane < 8 && tn < T_) slot_nx = (size_t)mt.rstart[tke[tn * 8 + lane]] + tkp[tn * 8 + lane]; }
;         u32x4 w[9];
; #pragma unroll
;         for (int k = 0; k < 9; ++k) { const size_t sl = (size_t)(unsigned)__builtin_amdgcn_readlane((int)(unsigned)slot, k);
;             w[k] = *(const u32x4*)(ysl + sl * 1024 + lane * 16); }
;         const u32x4 xr0 = *(const u32x4*)(xab + (size_t)t * 1024 + lane * 16), xr1 = *(const u32x4*)(xab + (size_t)t * 1024 + lane * 16 + 8);
;     ...
;             { const u32x4 o0 = {cvt_pk_bf16(v[0][0], v[0][1]), cvt_pk_bf16(v[0][2], v[0][3]), cvt_pk_bf16(v[1][0], v[1][1]), cvt_pk_bf16(v[1][2], v[1][3])};
;               const u32x4 o1 = {cvt_pk_bf16(v[2][0], v[2][1]), cvt_pk_bf16(v[2][2], v[2][3]), cvt_pk_bf16(v[3][0], v[3][1]), cvt_pk_bf16(v[3][2], v[3][3])};
;               *(u32x4*)(xob + (size_t)t * 1024 + lane * 16) = o0; *(u32x4*)(xob + (size_t)t * 1024 + lane * 16 + 8) = o1; }
;             float mu2, rstd2; row_stats(v, mu2, rstd2); unsigned hw[8];
; #pragma unroll
;             for (int i = 0; i < 4; ++i) { float o[4];
; #pragma unroll
;                 for (int j = 0; j < 4; ++j) o[j] = (v[i][j] - mu2) * rstd2 * (1.f + sc4[i][j]) + sh4[i][j];
;                 hw[2 * i] = cvt_pk_bf16(o[0], o[1]); hw[2 * i + 1] = cvt_pk_bf16(o[2], o[3]); }
;             *(u32x4*)(hb + (size_t)t * 1024 + lane * 16) = (u32x4){hw[0], hw[1], hw[2], hw[3]}; *(u32x4*)(hb + (size_t)t * 1024 + lane * 16 + 8) = (u32x4){hw[4], hw[5], hw[6], hw[7]};
	v_pk_mul_f32 v[106:107], v[98:99], v[98:99]
	s_nop 0
	v_add_f32_e32 v106, v106, v108
	v_add_f32_e32 v106, v107, v106
	s_nop 1
	v_add_f32_dpp v106, v106, v106 quad_perm:[1,0,3,2] row_mask:0xf bank_mask:0xf bound_ctrl:1
	s_nop 1
	v_add_f32_dpp v106, v106, v106 quad_perm:[2,3,0,1] row_mask:0xf bank_mask:0xf bound_ctrl:1
	s_nop 1
	v_add_f32_dpp v106, v106, v106 row_half_mirror row_mask:0xf bank_mask:0xf bound_ctrl:1
	s_nop 1
	v_add_f32_dpp v106, v106, v106 row_mirror row_mask:0xf bank_mask:0xf bound_ctrl:1
	s_nop 0
	v_readlane_b32 s22, v106, 16
	v_readlane_b32 s41, v106, 48
	v_readlane_b32 s6, v106, 0
	v_readlane_b32 s7, v106, 32
	v_mov_b32_e32 v106, s22
	v_mov_b32_e32 v107, s41
	v_pk_add_f32 v[106:107], s[6:7], v[106:107]
	s_nop 0
	v_add_f32_e32 v106, v106, v107
	v_fmamk_f32 v106, v106, 0x3a800000, v134
	v_mul_f32_e32 v107, 0x4b800000, v106
	v_cmp_gt_f32_e32 vcc, s40, v106
	s_nop 1
	v_cndmask_b32_e32 v106, v106, v107, vcc
	v_rsq_f32_e32 v108, v106
	v_lshl_add_u64 v[106:107], s[18:19], 0, v[130:131]
	global_store_dwordx4 v[106:107], v[82:85], off
	global_store_dwordx4 v[106:107], v[86:89], off offset:16
	s_nop 0
	v_mul_f32_e32 v82, 0x45800000, v108
	v_cndmask_b32_e32 v88, v108, v82, vcc
	v_mul_f32_e32 v82, v96, v88
	v_add_f32_e32 v83, 1.0, v70
	v_fma_f32 v82, v83, v82, v50
	v_mul_f32_e32 v83, v97, v88
	v_add_f32_e32 v84, 1.0, v71
	v_fma_f32 v83, v84, v83, v51
	v_mul_f32_e32 v84, v100, v88
	v_add_f32_e32 v85, 1.0, v72
	v_fma_f32 v84, v85, v84, v52
	v_mul_f32_e32 v85, v101, v88
	v_add_f32_e32 v86, 1.0, v73
	v_fma_f32 v85, v86, v85, v53
	v_cvt_pk_bf16_f32 v82, v82, v83
	v_cvt_pk_bf16_f32 v83, v84, v85
	v_mul_f32_e32 v84, v90, v88
	v_add_f32_e32 v85, 1.0, v74
	v_fma_f32 v84, v85, v84, v54
	v_mul_f32_e32 v85, v91, v88
	v_add_f32_e32 v86, 1.0, v75
	v_fma_f32 v85, v86, v85, v55
	v_mul_f32_e32 v86, v102, v88
	v_add_f32_e32 v87, 1.0, v76
	v_fma_f32 v86, v87, v86, v56
	v_mul_f32_e32 v87, v103, v88
	v_add_f32_e32 v89, 1.0, v77
	v_fma_f32 v87, v89, v87, v57
	v_cvt_pk_bf16_f32 v84, v84, v85
	v_cvt_pk_bf16_f32 v85, v86, v87
	v_mul_f32_e32 v86, v94, v88
	v_add_f32_e32 v87, 1.0, v66
	v_fma_f32 v86, v87, v86, v58
	v_mul_f32_e32 v87, v95, v88
	v_add_f32_e32 v89, 1.0, v67
	v_fma_f32 v87, v89, v87, v59
	v_mul_f32_e32 v89, v104, v88
	v_add_f32_e32 v90, 1.0, v68
	v_fma_f32 v89, v90, v89, v60
	v_mul_f32_e32 v90, v105, v88
	v_add_f32_e32 v91, 1.0, v69
	v_fma_f32 v90, v91, v90, v61
	v_cvt_pk_bf16_f32 v86, v86, v87
	v_cvt_pk_bf16_f32 v87, v89, v90
	v_mul_f32_e32 v89, v92, v88
	v_add_f32_e32 v90, 1.0, v78
	v_fma_f32 v89, v90, v89, v62
	v_mul_f32_e32 v90, v93, v88
	v_add_f32_e32 v91, 1.0, v79
	v_fma_f32 v90, v91, v90, v63
	v_mul_f32_e32 v91, v98, v88
	v_add_f32_e32 v92, 1.0, v80
	v_fma_f32 v91, v92, v91, v64
	v_mul_f32_e32 v88, v99, v88
	v_add_f32_e32 v92, 1.0, v81
	v_fma_f32 v92, v92, v88, v65
	v_cvt_pk_bf16_f32 v88, v89, v90
	v_cvt_pk_bf16_f32 v89, v91, v92
	v_lshl_add_u64 v[90:91], s[8:9], 0, v[130:131]
	global_store_dwordx4 v[90:91], v[82:85], off
	global_store_dwordx4 v[90:91], v[86:89], off offset:16
	v_lshl_add_u64 v[130:131], v[130:131], 0, s[36:37]
	v_mov_b32_e32 v82, v133
	s_andn2_b64 exec, exec, s[20:21]
	s_cbranch_execz .LBB0_1736
.LBB0_1732:
	v_add_u32_e32 v135, s86, v137
	v_cmp_gt_i32_e64 s[6:7], s38, v135
	v_add_u32_e32 v133, 0x40000, v135
	v_cmp_lt_i32_e32 vcc, s35, v135
	s_and_b64 s[42:43], s[4:5], s[6:7]
	s_and_b64 s[6:7], exec, vcc
	s_or_b64 s[20:21], s[6:7], s[20:21]
	v_readlane_b32 s22, v82, 0
	s_lshl_b64 s[6:7], s[22:23], 10
	v_readlane_b32 s22, v82, 1
	v_lshl_add_u64 v[84:85], v[128:129], 0, s[6:7]
	s_lshl_b64 s[6:7], s[22:23], 10
	v_readlane_b32 s22, v82, 2
	v_lshl_add_u64 v[86:87], v[128:129], 0, s[6:7]
	s_lshl_b64 s[6:7], s[22:23], 10
	v_readlane_b32 s22, v82, 3
	global_load_dwordx4 v[122:125], v[84:85], off
	global_load_dwordx4 v[114:117], v[86:87], off
	v_lshl_add_u64 v[84:85], v[128:129], 0, s[6:7]
	s_lshl_b64 s[6:7], s[22:23], 10
	v_readlane_b32 s22, v82, 4
	v_lshl_add_u64 v[86:87], v[128:129], 0, s[6:7]
	s_lshl_b64 s[6:7], s[22:23], 10
	v_readlane_b32 s22, v82, 5
	global_load_dwordx4 v[118:121], v[84:85], off
	global_load_dwordx4 v[106:109], v[86:87], off
	v_lshl_add_u64 v[84:85], v[128:129], 0, s[6:7]
	s_lshl_b64 s[6:7], s[22:23], 10
	v_readlane_b32 s22, v82, 6
	v_lshl_add_u64 v[86:87], v[128:129], 0, s[6:7]
	s_lshl_b64 s[6:7], s[22:23], 10
	v_readlane_b32 s22, v82, 7
	global_load_dwordx4 v[110:113], v[84:85], off
	global_load_dwordx4 v[98:101], v[86:87], off
	v_lshl_add_u64 v[84:85], v[128:129], 0, s[6:7]
	s_lshl_b64 s[6:7], s[22:23], 10
	v_readlane_b32 s22, v82, 8
	v_lshl_add_u64 v[86:87], v[128:129], 0, s[6:7]
	s_lshl_b64 s[6:7], s[22:23], 10
	v_lshl_add_u64 v[82:83], v[128:129], 0, s[6:7]
	global_load_dwordx4 v[102:105], v[84:85], off
	global_load_dwordx4 v[94:97], v[86:87], off
	global_load_dwordx4 v[90:93], v[82:83], off
	v_lshl_add_u64 v[82:83], s[10:11], 0, v[130:131]
	global_load_dwordx4 v[86:89], v[82:83], off
	s_nop 0
	global_load_dwordx4 v[82:85], v[82:83], off offset:16
	s_and_saveexec_b64 s[6:7], s[42:43]
	s_cbranch_execz .Lmy_cmb_skip_a
	v_ashrrev_i32_e32 v133, 31, v132
	v_lshlrev_b64 v[250:251], 2, v[132:133]
	v_lshl_add_u64 v[252:253], s[12:13], 0, v[250:251]
	global_load_dword v254, v[252:253], off
	v_lshl_add_u64 v[250:251], s[14:15], 0, v[250:251]
	global_load_dword v255, v[250:251], off
	s_waitcnt vmcnt(0) lgkmcnt(0)
	v_lshl_add_u32 v254, v254, 2, s2
	ds_read_b32 v254, v254 offset:61440
	s_waitcnt lgkmcnt(0)
	v_add_u32_e32 v133, v255, v254

; DEVI CvSlice cv_slice(const Params& p, int l, int s, int lane) {
;     CvSlice c;
;     if (s < NS_W13) {
;         const int e = s >> 9, r = s & 511, hb = r & 7, mat = (r >> 3) & 1, ks = r >> 4;
;         const float* W = mat ? (e < NE ? p.w3 + ((size_t)l * NE + e) * 1024 * 256 : p.ws3 + (size_t)l * 1024 * 256)
;                              : (e < NE ? p.w1 + ((size_t)l * NE + e) * 1024 * 256 : p.ws1 + (size_t)l * 1024 * 256);
;         const int hc0 = hb * 32;
;         c.src = W + hc0 + (lane & 7) * 4; c.ld = 256; c.dst = p.w13t + (size_t)e * 512 * 1024; c.K = 1024;
;         c.r0 = (hc0 >> 7) * 256 + ((hc0 >> 5) & 3) * 32 + mat * 16; c.k0 = ks * 32; c.perm = 0;
;     } else {
;         s -= NS_W13;
;         const int e = s >> 8, r = s & 255, nb = r & 31, ks = r >> 5;
;         const float* W2 = e < NE ? p.w2 + ((size_t)l * NE + e) * 256 * 1024 : p.ws2 + (size_t)l * 256 * 1024;
;         c.src = W2 + nb * 32 + (lane & 7) * 4; c.ld = 1024; c.dst = p.w2t + (size_t)e * 1024 * 256; c.K = 256; c.r0 = (nb >> 3) * 256 + ((nb & 7) >> 1) * 32 + (nb & 1) * 8; c.k0 = ks * 32; c.perm = 1;
;     }
;     return c;
; }
; DEVI void cv_next(const Params& p, int l, int s, int lane, int stride, CvRun& run) {
;     ...
;     run.c = cv_slice(p, l, s, lane); run.left = 0;
;     if ((stride & 511) == 0) {
;         if (s < NS_W13) { const int e = s >> 9, es = stride >> 9; if (e < NE) { run.left = (NE - 1 - e) / es; run.sstep = (long)es * 1024 * 256; run.dstep = (long)es * 512 * 1024; } }
;         else { const int e = (s - NS_W13) >> 8, es = stride >> 8; if (e < NE) { run.left = (NE - 1 - e) / es; run.sstep = (long)es * 256 * 1024; run.dstep = (long)es * 1024 * 256; } } }
; }
; DEVI void cv_issue(const Params& p, int l, int s, int lane, CvRegs& R, CvRun& run) {
;     R.live = s < NS_SLICES ? 1 : 0;
;     if (R.live) { cv_next(p, l, s, lane, (int)gridDim.x * 8, run); R.c = run.c; const int kq = lane >> 3;
;         const float* sp = R.c.src + (size_t)(R.c.k0 + 2 * kq) * R.c.ld;
; DEVI void attn_unit8(const Params& p, char* smem, int unit, int l, int& cvs  , CvRun& crun) {
;     ...
;     for (int T = 0; T + 1 < NTILE; ++T) {
;         const char* Kb = K_lds + s0 * 24576; const int vb = vb0 + s0 * 16384;
;         CvRegs cvr; cv_issue(p, l, cvs, lane, cvr, crun); cvs += (int)gridDim.x * 8;
;         qkt(pB0, pB1, Kb + 12288, qr, r32, hi, cinit);
.LBB0_2230:
	s_mul_i32 s98, s71, 0x6000
	s_add_i32 s98, s98, 0
	v_add_u32_e32 v86, s98, v129
	ds_read_b128 v[82:85], v86 offset:12288
	ds_read_b128 v[124:127], v86 offset:18432
	s_cmp_lt_i32 s54, 0x30300
	s_mov_b32 s2, s61
	s_cselect_b64 s[14:15], -1, 0
	s_cmp_gt_i32 s54, 0x302ff
	s_mov_b32 s61, s6
	s_cbranch_scc1 .LBB0_2260
	s_cmp_lt_i32 s56, 1
	s_mov_b64 s[16:17], -1
	s_cbranch_scc0 .LBB0_2257
	s_cmp_gt_i32 s54, 0x201ff
	s_cselect_b64 s[16:17], -1, 0
	s_mov_b64 s[6:7], -1
	s_and_b64 vcc, exec, s[16:17]
	s_cbranch_vccz .LBB0_2234
	s_add_i32 s6, s54, 0xfffdfe00
	s_lshr_b32 s8, s6, 8
	s_and_b32 s10, s54, 0xe0
	s_cmp_lt_u32 s6, 0x10000
	s_cselect_b64 s[6:7], -1, 0
	s_and_b32 s11, s89, 0x3fc0000
	s_bitset1_b32 s11, 26
	s_and_b64 s[6:7], s[6:7], exec
	s_cselect_b32 s6, 0xc0, s79
	s_cselect_b32 s11, s11, 0x40000
	s_add_u32 s6, s24, s6
	s_addc_u32 s7, s25, 0
	s_load_dwordx2 s[6:7], s[6:7], 0x0
	s_lshl_b32 s11, s11, 2
	s_load_dwordx2 s[20:21], s[24:25], 0x158
	s_waitcnt lgkmcnt(0)
	s_add_u32 s6, s6, s11
	s_addc_u32 s7, s7, 0
	s_and_b32 s11, s84, 0x3e0
	s_lshl_b32 s11, s11, 2
	s_add_u32 s18, s6, s11
	s_addc_u32 s19, s7, 0
	s_lshl_b64 s[6:7], s[8:9], 19
	s_add_u32 s20, s20, s6
	s_addc_u32 s21, s21, s7
	s_and_b32 s6, s84, 0x300
	s_and_b32 s7, s85, 0x60
	s_or_b32 s6, s6, s7
	s_and_b32 s7, s88, 8
	s_or_b32 s8, s6, s7
	s_mov_b64 s[6:7], 0

; template <bool FIRST> DEVI bool partialSM(f32x16& p0, f32x16& p1, float& m_reg, float& alpha) {
;     float pmax = p0[0];
; #pragma unroll
;     for (int r = 1; r < 16; ++r) pmax = fmaxf(pmax, p0[r]);
; #pragma unroll
;     for (int r = 0; r < 16; ++r) pmax = fmaxf(pmax, p1[r]);
;     { auto rr = __builtin_amdgcn_permlane32_swap(__float_as_uint(pmax), __float_as_uint(pmax), false, false);
;       pmax = fmaxf(__uint_as_float(rr[0]), __uint_as_float(rr[1])); }
;     if (FIRST) { m_reg = pmax; alpha = 1.f;
; #pragma unroll
;         for (int r = 0; r < 16; ++r) { p0[r] = __builtin_amdgcn_exp2f(p0[r] - pmax); p1[r] = p1[r] - pmax; }
;         return false;
;     } else if (__builtin_expect(__all(pmax <= ATT_THR), 1)) { alpha = 1.f;
; #pragma unroll
;         for (int r = 0; r < 16; ++r) p0[r] = __builtin_amdgcn_exp2f(p0[r]);
;         return false;
;     } else { const float d = fmaxf(pmax, 0.f); alpha = __builtin_amdgcn_exp2f(-d); m_reg += d;
; #pragma unroll
;         for (int r = 0; r < 16; ++r) { p0[r] = __builtin_amdgcn_exp2f(p0[r] - d); p1[r] = p1[r] - d; }
;         return true;
;     }
; }
; DEVI void finishSM(f32x16& p0, f32x16& p1, float alpha, float& l_reg, bf16x8& pa0, bf16x8& pa1, bf16x8& pa2, bf16x8& pa3) {
; #pragma unroll
;     for (int r = 0; r < 16; ++r) p1[r] = __builtin_amdgcn_exp2f(p1[r]);
;     f32x2 s2 = (f32x2){p0[0], p0[1]} + (f32x2){p1[0], p1[1]};
; #pragma unroll
;     for (int r = 2; r < 16; r += 2) s2 += (f32x2){p0[r], p0[r + 1]} + (f32x2){p1[r], p1[r + 1]};
;     float ps = s2[0] + s2[1];
;     { auto rr = __builtin_amdgcn_permlane32_swap(__float_as_uint(ps), __float_as_uint(ps), false, false);
;       ps = __uint_as_float(rr[0]) + __uint_as_float(rr[1]); }
;     l_reg = l_reg * alpha + ps;
;     ...
;     PK4(p0, 0, pa0); PK4(p0, 8, pa1); PK4(p1, 0, pa2); PK4(p1, 8, pa3);
;     ...
; }
; DEVI void qkt(f32x16& p0, f32x16& p1, const char* Kb, const bf16x8 (&qr)[6], int r32, int hi, const f32x16& cinit) {
; #pragma unroll
;     for (int d0 = 0; d0 < 6; ++d0) { const int cb = (d0 * 16 + hi * 8) * 2;
;         const bf16x8 k0 = *(const bf16x8*)(Kb + KSWZ(r32, cb)), k1 = *(const bf16x8*)(Kb + KSWZ(32 + r32, cb));
;         p0 = __builtin_amdgcn_mfma_f32_32x32x16_bf16(k0, qr[d0], d0 == 0 ? cinit : p0, 0, 0, 0);
;         p1 = __builtin_amdgcn_mfma_f32_32x32x16_bf16(k1, qr[d0], d0 == 0 ? cinit : p1, 0, 0, 0); }
; }
.LBB0_2260:
	v_add_u32_e32 v174, s98, v205
	v_exp_f32_e32 v66, v66
	v_exp_f32_e32 v67, v67
	s_waitcnt lgkmcnt(1)
	v_mfma_f32_32x32x16_bf16 v[98:113], v[82:85], v[150:153], v[34:49]
	v_add_u32_e32 v82, s98, v184
	v_add_u32_e32 v83, s98, v185
	ds_read_b128 v[210:213], v82 offset:12288
	ds_read_b128 v[214:217], v82 offset:18432
	ds_read_b128 v[218:221], v83 offset:12288
	ds_read_b128 v[222:225], v83 offset:18432
	v_exp_f32_e32 v68, v68
	v_exp_f32_e32 v69, v69
	v_exp_f32_e32 v70, v70
	v_exp_f32_e32 v71, v71
	s_waitcnt lgkmcnt(4)
	v_mfma_f32_32x32x16_bf16 v[82:97], v[124:127], v[150:153], v[34:49]
	ds_read_b128 v[124:127], v174 offset:12288
	ds_read_b128 v[226:229], v174 offset:18432
	v_exp_f32_e32 v72, v72
	v_exp_f32_e32 v73, v73
	v_exp_f32_e32 v74, v74
	v_exp_f32_e32 v75, v75
	v_exp_f32_e32 v76, v76
	v_exp_f32_e32 v77, v77
	s_waitcnt lgkmcnt(5)
	v_mfma_f32_32x32x16_bf16 v[98:113], v[210:213], v[138:141], v[98:113]
	v_add_u32_e32 v174, s98, v206
	v_exp_f32_e32 v78, v78
	v_exp_f32_e32 v79, v79
	ds_read_b128 v[230:233], v174 offset:12288
	ds_read_b128 v[234:237], v174 offset:18432
	v_exp_f32_e32 v80, v80
	v_exp_f32_e32 v81, v81
	v_add_u32_e32 v174, s98, v207
	s_waitcnt lgkmcnt(6)
	v_mfma_f32_32x32x16_bf16 v[82:97], v[214:217], v[138:141], v[82:97]
	v_add_f32_e64 v214, v50, v66
	v_add_f32_e64 v215, v51, v67
	v_add_f32_e64 v216, v52, v68
	v_add_f32_e64 v217, v53, v69
	v_lshl_add_u32 v203, s71, 14, v115
	v_pk_add_f32 v[214:215], v[216:217], v[214:215]
	v_pk_add_f32 v[216:217], v[54:55], v[70:71]
	ds_read_b128 v[210:213], v174 offset:12288
	ds_read_b128 v[238:241], v174 offset:18432
	v_pk_add_f32 v[214:215], v[216:217], v[214:215]
	s_waitcnt lgkmcnt(7)
	v_mfma_f32_32x32x16_bf16 v[98:113], v[218:221], v[134:137], v[98:113]
	v_add_f32_e64 v216, v56, v72
	v_add_f32_e64 v217, v57, v73
	v_cvt_pk_bf16_f32 v50, v50, v51
	v_cvt_pk_bf16_f32 v51, v52, v53
	v_cvt_pk_bf16_f32 v52, v54, v55
	v_cvt_pk_bf16_f32 v53, v56, v57
	v_cvt_pk_bf16_f32 v54, v58, v59
	v_add_f32_e64 v214, v216, v214
	v_add_f32_e64 v215, v217, v215
	s_waitcnt lgkmcnt(6)
	v_mfma_f32_32x32x16_bf16 v[82:97], v[222:225], v[134:137], v[82:97]
	v_add_f32_e64 v216, v58, v74
	v_add_f32_e64 v217, v59, v75
	v_cvt_pk_bf16_f32 v55, v60, v61
	v_cvt_pk_bf16_f32 v56, v62, v63
	v_cvt_pk_bf16_f32 v57, v64, v65
	v_cvt_pk_bf16_f32 v58, v66, v67
	v_cvt_pk_bf16_f32 v59, v68, v69
	v_add_f32_e64 v214, v216, v214
	v_add_f32_e64 v215, v217, v215
	s_waitcnt lgkmcnt(5)
	v_mfma_f32_32x32x16_bf16 v[98:113], v[124:127], v[130:133], v[98:113]
	v_add_f32_e64 v216, v60, v76
	v_add_f32_e64 v217, v61, v77
	v_add_f32_e64 v126, v62, v78
	v_add_f32_e64 v127, v63, v79
	v_add_f32_e64 v124, v216, v214
	v_add_f32_e64 v125, v217, v215
	v_cvt_pk_bf16_f32 v60, v70, v71
	v_cvt_pk_bf16_f32 v61, v72, v73
	v_cvt_pk_bf16_f32 v62, v74, v75
	v_cvt_pk_bf16_f32 v63, v76, v77
	s_waitcnt lgkmcnt(4)
	v_mfma_f32_32x32x16_bf16 v[82:97], v[226:229], v[130:133], v[82:97]
	v_add_f32_e64 v124, v126, v124
	v_add_f32_e64 v125, v127, v125
	v_add_f32_e64 v126, v64, v80
	v_add_f32_e64 v127, v65, v81
	v_cvt_pk_bf16_f32 v64, v78, v79
	v_cvt_pk_bf16_f32 v65, v80, v81
	ds_read_b64_tr_b16 v[66:67], v203 offset:0
	ds_read_b64_tr_b16 v[68:69], v203 offset:0x400
	ds_read_b64_tr_b16 v[70:71], v203 offset:0x800
	s_waitcnt lgkmcnt(6)
	v_mfma_f32_32x32x16_bf16 v[98:113], v[230:233], v[146:149], v[98:113]
	ds_read_b64_tr_b16 v[72:73], v203 offset:0xc00
	ds_read_b64_tr_b16 v[74:75], v203 offset:0x1000
	ds_read_b64_tr_b16 v[76:77], v203 offset:0x1400
	ds_read_b64_tr_b16 v[78:79], v203 offset:0x1800
	ds_read_b64_tr_b16 v[80:81], v203 offset:0x1c00
	v_add_f32_e64 v124, v126, v124
	v_add_f32_e64 v125, v127, v125
	s_waitcnt lgkmcnt(10)
	v_mfma_f32_32x32x16_bf16 v[82:97], v[234:237], v[146:149], v[82:97]
	v_pk_add_f32 v[124:125], v[124:125], v[124:125] op_sel:[0,1] op_sel_hi:[1,0]
	s_nop 0
	v_mov_b32_e32 v125, v124
	s_nop 1
	v_permlane32_swap_b32_e32 v124, v125
	s_waitcnt lgkmcnt(9)
	v_mfma_f32_32x32x16_bf16 v[98:113], v[210:213], v[142:145], v[98:113]
	ds_read_b64_tr_b16 v[210:211], v203 offset:0x200
	ds_read_b64_tr_b16 v[212:213], v203 offset:0x600
	ds_read_b64_tr_b16 v[214:215], v203 offset:0xa00
	ds_read_b64_tr_b16 v[216:217], v203 offset:0xe00
	ds_read_b64_tr_b16 v[218:219], v203 offset:0x1200
	ds_read_b64_tr_b16 v[220:221], v203 offset:0x1600
	ds_read_b64_tr_b16 v[222:223], v203 offset:0x1a00
	s_waitcnt lgkmcnt(15)
	v_mfma_f32_32x32x16_bf16 v[82:97], v[238:241], v[142:145], v[82:97]
	ds_read_b64_tr_b16 v[224:225], v203 offset:0x1e00
	s_waitcnt lgkmcnt(14)
	v_mfma_f32_32x32x16_bf16 v[18:33], v[50:53], v[66:69], v[18:33]
	s_waitcnt lgkmcnt(12)
	v_mfma_f32_32x32x16_bf16 v[18:33], v[54:57], v[70:73], v[18:33]
	s_waitcnt lgkmcnt(10)
	v_mfma_f32_32x32x16_bf16 v[18:33], v[58:61], v[74:77], v[18:33]
	s_waitcnt lgkmcnt(8)
	v_mfma_f32_32x32x16_bf16 v[18:33], v[62:65], v[78:81], v[18:33]
	s_waitcnt lgkmcnt(6)
	v_mfma_f32_32x32x16_bf16 v[2:17], v[50:53], v[210:213], v[2:17]
	s_nop 4
	v_max_f32_e32 v249, v99, v99
	v_max_f32_e32 v250, v98, v98
	v_max_f32_e32 v249, v250, v249
	v_max3_f32 v249, v249, v100, v101
	v_max3_f32 v249, v249, v102, v103
	v_max3_f32 v251, v249, v104, v105
	v_max3_f32 v251, v251, v106, v107
	s_waitcnt lgkmcnt(4)
	v_exp_f32_e32 v50, v98
	v_exp_f32_e32 v51, v99
	v_exp_f32_e32 v52, v100
	v_exp_f32_e32 v53, v101
	v_mov_b64_e32 v[66:67], v[82:83]
	v_mov_b64_e32 v[68:69], v[84:85]
	v_mfma_f32_32x32x16_bf16 v[2:17], v[54:57], v[214:217], v[2:17]
	v_max3_f32 v251, v251, v108, v109
	v_max3_f32 v251, v251, v110, v111
	v_max3_f32 v251, v251, v112, v113
	v_max3_f32 v251, v251, v82, v83
	v_max3_f32 v251, v251, v84, v85
	v_max3_f32 v251, v251, v86, v87
	v_max3_f32 v251, v251, v88, v89
	s_waitcnt lgkmcnt(2)
	v_exp_f32_e32 v54, v102
	v_exp_f32_e32 v55, v103
	v_exp_f32_e32 v56, v104
	v_exp_f32_e32 v57, v105
	v_mov_b64_e32 v[70:71], v[86:87]
	v_mov_b64_e32 v[72:73], v[88:89]
	v_mfma_f32_32x32x16_bf16 v[2:17], v[58:61], v[218:221], v[2:17]
	v_max3_f32 v251, v251, v90, v91
	v_max3_f32 v251, v251, v92, v93
	v_max3_f32 v251, v251, v94, v95
	v_max3_f32 v251, v251, v96, v97
	v_mov_b32_e32 v252, v251
	s_nop 1
	v_permlane32_swap_b32_e32 v251, v252
	s_waitcnt lgkmcnt(0)
	v_exp_f32_e32 v58, v106
	v_exp_f32_e32 v59, v107
	v_exp_f32_e32 v60, v108
	v_exp_f32_e32 v61, v109
	v_mov_b64_e32 v[74:75], v[90:91]
	v_mov_b64_e32 v[76:77], v[92:93]
	v_mfma_f32_32x32x16_bf16 v[2:17], v[62:65], v[222:225], v[2:17]
	v_exp_f32_e32 v62, v110
	v_exp_f32_e32 v63, v111
	v_exp_f32_e32 v64, v112
	v_exp_f32_e32 v65, v113
	v_mov_b64_e32 v[78:79], v[94:95]
	v_mov_b64_e32 v[80:81], v[96:97]
	v_max_f32_e32 v252, v252, v252
	v_max_f32_e32 v251, v251, v251
	v_max_f32_e32 v126, v251, v252
	v_cmp_ge_f32_e32 vcc, s80, v126
	s_cmp_lg_u64 vcc, exec
	s_cselect_b64 s[6:7], -1, 0
	s_cbranch_scc1 .LBB0_2269
	v_mov_b32_e32 v209, 1.0
	v_mov_b32_e32 v210, v204
	s_branch .LBB0_2263

; DEVI int vtid() { return tidx() & 255; }
; DEVI int vbid() { return bidx() * 2 + vhb(); }
; DEVI int vgrid() { return (int)gridDim.x * 2; }
; DEVI float bflo(unsigned w) { return __uint_as_float(w << 16); }
; DEVI float bfhi(unsigned w) { return __uint_as_float(w & 0xffff0000u); }
; DEVI void row_stats(const f32x4 (&v)[4], float& mu, float& rstd) {
;     float s = 0.f;
; #pragma unroll
;     for (int i = 0; i < 4; ++i) s += (v[i][0] + v[i][1]) + (v[i][2] + v[i][3]);
;     mu = wave_sum(s) * (1.f / 1024.f);
; DEVI void phase_ln_mid(const Params& p, int l) {
;     const int lane = vtid() & 63, gw = vbid() * 4 + (vtid() >> 6), nw = vgrid() * 4;
;     bf16_t* xab = p.xa; bf16_t* hb = p.h; asm volatile("" : "+s"(xab), "+s"(hb));
;     f32x4 lg4[4], lb4[4], sh4[4], sc4[4]; int bcur = -1;
; #pragma unroll
;     for (int i = 0; i < 4; ++i) { const int c = lane * 4 + 256 * i; lg4[i] = *(const f32x4*)(p.ln1_g + l * 1024 + c); lb4[i] = *(const f32x4*)(p.ln1_b + l * 1024 + c); sh4[i] = lg4[i]; sc4[i] = lg4[i]; }
;     u32x2 rw[4], rn[4];
; #pragma unroll
;     for (int i = 0; i < 4; ++i) rw[i] = *(const u32x2*)(xab + (size_t)(gw < T_ ? gw : 0) * 1024 + lane * 4 + 256 * i);
;     for (int t = gw; t < T_; t += nw) {
;         const int b = t >> 12; f32x4 v[4]; const int tn = t + nw < T_ ? t + nw : t;
; #pragma unroll
;         for (int i = 0; i < 4; ++i) { v[i] = (f32x4){bflo(rw[i].x), bfhi(rw[i].x), bflo(rw[i].y), bfhi(rw[i].y)}; rn[i] = *(const u32x2*)(xab + (size_t)tn * 1024 + lane * 4 + 256 * i); }
;         if (b != bcur) { bcur = b; const float* ad = p.ada + ((size_t)l * 8 + b) * 6144;
; #pragma unroll
;             for (int i = 0; i < 4; ++i) { sh4[i] = *(const f32x4*)(ad + 3072 + lane * 4 + 256 * i); sc4[i] = *(const f32x4*)(ad + 4096 + lane * 4 + 256 * i); } }
;         float mu, rstd; row_stats(v, mu, rstd);
.LBB0_2644:
	s_or_b64 exec, exec, s[4:5]
	s_mov_b64 s[6:7], s[0:1]
	s_waitcnt lgkmcnt(0)
	v_mov_b32_e32 v1, v0
	s_mov_b32 s2, s84
	v_mov_b32_e32 v2, v0
	s_barrier
	s_lshl_b32 s2, s2, 3
	v_readfirstlane_b32 s4, v2
	s_lshr_b32 s4, s4, 6
	s_and_b32 s4, s4, 0x3fffffc
	v_mov_b32_e32 v30, v0
	s_add_i32 s4, s4, s2
	s_load_dwordx4 s[8:11], s[6:7], 0x160
	s_cmpk_gt_u32 s4, 0x7fff
	s_movk_i32 s2, 0x7fff
	s_waitcnt lgkmcnt(0)
	s_cbranch_scc1 .LBB0_2650
	s_load_dwordx4 s[12:15], s[6:7], 0x90
	v_lshlrev_b32_e32 v2, 2, v1
	v_and_b32_e32 v34, 0xfc, v2
	v_lshlrev_b32_e32 v31, 2, v34
	v_or_b32_e32 v33, 0x800, v31
	s_waitcnt lgkmcnt(0)
	s_add_u32 s12, s12, 0x1000
	s_addc_u32 s13, s13, 0
	v_or_b32_e32 v35, 0xc00, v31
	v_lshrrev_b32_e32 v30, 6, v30
	v_or_b32_e32 v32, 0x400, v31
	global_load_dwordx4 v[2:5], v31, s[12:13]
	global_load_dwordx4 v[6:9], v32, s[12:13]
	global_load_dwordx4 v[10:13], v33, s[12:13]
	global_load_dwordx4 v[14:17], v35, s[12:13]
	s_add_u32 s12, s14, 0x1000
	v_and_or_b32 v68, v30, 3, s4
	s_addc_u32 s13, s15, 0
	v_mov_b32_e32 v67, 0
	v_lshlrev_b32_e32 v66, 11, v68
	global_load_dwordx4 v[18:21], v31, s[12:13]
	global_load_dwordx4 v[22:25], v32, s[12:13]
	global_load_dwordx4 v[26:29], v33, s[12:13]
	v_lshl_add_u64 v[30:31], s[10:11], 0, v[66:67]
	v_lshlrev_b32_e32 v66, 1, v34
	v_lshl_add_u64 v[36:37], v[30:31], 0, v[66:67]
	global_load_dwordx2 v[82:83], v[36:37], off offset:1536
	global_load_dwordx2 v[84:85], v[36:37], off offset:1024
	global_load_dwordx2 v[86:87], v[36:37], off offset:512
	global_load_dwordx2 v[88:89], v[36:37], off
	global_load_dwordx4 v[30:33], v35, s[12:13]
	v_mov_b32_e32 v69, v67
	v_and_b32_e32 v35, 63, v1
	v_lshlrev_b64 v[70:71], 11, v[68:69]
	v_lshl_or_b32 v70, v35, 3, v70
	v_lshl_add_u64 v[72:73], s[10:11], 0, v[66:67]
	v_lshlrev_b32_e32 v66, 2, v34
	s_ashr_i32 s87, s86, 31
	v_mov_b32_e32 v90, -1
	s_mov_b64 s[12:13], 0
	s_mov_b32 s22, 0x8000
	s_mov_b64 s[14:15], 0x3000
	s_mov_b64 s[16:17], 0x4000
	v_mov_b32_e32 v1, 0x3727c5ac
	s_mov_b32 s23, 0x800000
	s_lshl_b64 s[18:19], s[86:87], 11
	s_waitcnt vmcnt(0)
	v_mov_b64_e32 v[36:37], v[4:5]
	v_mov_b64_e32 v[44:45], v[8:9]
	v_mov_b64_e32 v[48:49], v[12:13]
	v_mov_b64_e32 v[56:57], v[16:17]
	v_mov_b64_e32 v[34:35], v[2:3]
	v_mov_b64_e32 v[42:43], v[6:7]
	v_mov_b64_e32 v[46:47], v[10:11]
	v_mov_b64_e32 v[54:55], v[14:15]
	v_mov_b32_e32 v38, v2
	v_mov_b32_e32 v39, v3
	v_mov_b32_e32 v40, v4
	v_mov_b32_e32 v41, v5
	v_mov_b32_e32 v50, v6
	v_mov_b32_e32 v51, v7
	v_mov_b32_e32 v52, v8
	v_mov_b32_e32 v53, v9
	v_mov_b32_e32 v58, v10
	v_mov_b32_e32 v59, v11
	v_mov_b32_e32 v60, v12
	v_mov_b32_e32 v61, v13
	v_mov_b32_e32 v62, v14
	v_mov_b32_e32 v63, v15
	v_mov_b32_e32 v64, v16
	v_mov_b32_e32 v65, v17
	s_branch .LBB0_2647
.LBB0_2646:
	s_or_b64 exec, exec, s[20:21]
	s_waitcnt lgkmcnt(0)
	v_lshlrev_b32_e32 v93, 16, v89
	v_lshlrev_b32_e32 v92, 16, v88
	v_and_b32_e32 v89, 0xffff0000, v89
	v_and_b32_e32 v88, 0xffff0000, v88
	v_lshlrev_b32_e32 v95, 16, v87
	v_lshlrev_b32_e32 v94, 16, v86
	v_and_b32_e32 v87, 0xffff0000, v87
	v_and_b32_e32 v86, 0xffff0000, v86
	v_lshlrev_b32_e32 v96, 16, v84
	v_and_b32_e32 v97, 0xffff0000, v84
	v_and_b32_e32 v84, 0xffff0000, v85
	v_lshlrev_b32_e32 v85, 16, v85
	v_pk_add_f32 v[100:101], v[92:93], v[88:89]
	v_pk_add_f32 v[102:103], v[94:95], v[86:87]
	v_and_b32_e32 v98, 0xffff0000, v82
	v_lshlrev_b32_e32 v99, 16, v82
	v_and_b32_e32 v82, 0xffff0000, v83
	v_lshlrev_b32_e32 v83, 16, v83
	v_add_f32_e32 v69, v100, v101
	v_pk_add_f32 v[102:103], v[102:103], v[102:103] op_sel_hi:[0,1]
	v_pk_add_f32 v[106:107], v[84:85], v[84:85] op_sel_hi:[0,1]
	v_add_f32_e32 v101, 0, v69
	v_add_f32_e32 v105, v96, v97
	v_mov_b32_e32 v104, v99
	v_mov_b32_e32 v106, v98
	v_mov_b32_e32 v102, v83
	v_mov_b32_e32 v100, v82
	v_pk_add_f32 v[104:105], v[104:105], v[106:107]
	v_pk_add_f32 v[100:101], v[102:103], v[100:101]
	s_nop 0
	v_pk_add_f32 v[100:101], v[104:105], v[100:101]
	s_nop 0
	v_add_f32_e32 v69, v100, v101
	s_nop 1
	v_add_f32_dpp v69, v69, v69 quad_perm:[1,0,3,2] row_mask:0xf bank_mask:0xf bound_ctrl:1
	s_nop 1
	v_add_f32_dpp v69, v69, v69 quad_perm:[2,3,0,1] row_mask:0xf bank_mask:0xf bound_ctrl:1
	s_nop 1
	v_add_f32_dpp v69, v69, v69 row_half_mirror row_mask:0xf bank_mask:0xf bound_ctrl:1
	s_nop 1
	v_add_f32_dpp v69, v69, v69 row_mirror row_mask:0xf bank_mask:0xf bound_ctrl:1
	s_nop 0
	v_readlane_b32 s20, v69, 16
	v_readlane_b32 s21, v69, 48
	v_readlane_b32 s4, v69, 0
	v_readlane_b32 s5, v69, 32
	v_mov_b32_e32 v100, s20
	v_mov_b32_e32 v101, s21
	v_pk_add_f32 v[100:101], s[4:5], v[100:101]
	s_nop 0
	v_add_f32_e32 v69, v100, v101
	v_fmac_f32_e32 v88, 0xba800000, v69
	v_fmac_f32_e32 v92, 0xba800000, v69
	v_mul_f32_e32 v91, v88, v88
	v_fmac_f32_e32 v91, v92, v92
	v_fmac_f32_e32 v93, 0xba800000, v69
	v_fmac_f32_e32 v91, v93, v93
	v_fmac_f32_e32 v89, 0xba800000, v69
	v_fmac_f32_e32 v91, v89, v89
	v_fmac_f32_e32 v94, 0xba800000, v69
	v_fmac_f32_e32 v91, v94, v94
	v_fmac_f32_e32 v86, 0xba800000, v69
	v_fmac_f32_e32 v91, v86, v86
	v_fmac_f32_e32 v95, 0xba800000, v69
	v_fmac_f32_e32 v91, v95, v95
	v_fmac_f32_e32 v87, 0xba800000, v69
	v_mul_f32_e32 v100, 0x3a800000, v69
	v_fmac_f32_e32 v91, v87, v87
	v_fmac_f32_e32 v96, 0xba800000, v69
	v_fmac_f32_e32 v91, v96, v96
	v_fmac_f32_e32 v97, 0xba800000, v69
	v_pk_add_f32 v[102:103], v[84:85], v[100:101] op_sel_hi:[1,0] neg_lo:[0,1] neg_hi:[0,1]
	v_fmac_f32_e32 v91, v97, v97
	v_pk_mul_f32 v[102:103], v[102:103], v[102:103]
	v_fmac_f32_e32 v84, 0xba800000, v69
	v_add_f32_e32 v91, v103, v91
	v_add_f32_e32 v91, v102, v91
	v_pk_add_f32 v[102:103], v[98:99], v[100:101] op_sel_hi:[1,0] neg_lo:[0,1] neg_hi:[0,1]
; DEVI unsigned cvt_pk_bf16(float lo, float hi) { unsigned r; asm volatile("v_cvt_pk_bf16_f32 %0, %1, %2" : "=v"(r) : "v"(lo), "v"(hi)); return r; }
; DEVI void st_bf4(bf16_t* p, f32x4 v) { u32x2 w; w.x = cvt_pk_bf16(v[0], v[1]); w.y = cvt_pk_bf16(v[2], v[3]); *(u32x2*)p = w; }
; DEVI void row_stats(const f32x4 (&v)[4], float& mu, float& rstd) {
;     float s = 0.f;
; #pragma unroll
;     for (int i = 0; i < 4; ++i) s += (v[i][0] + v[i][1]) + (v[i][2] + v[i][3]);
;     mu = wave_sum(s) * (1.f / 1024.f);
;     float q = 0.f;
; #pragma unroll
;     for (int i = 0; i < 4; ++i)
; #pragma unroll
;         for (int j = 0; j < 4; ++j) { const float d = v[i][j] - mu; q += d * d; }
;     rstd = rsqrtf(wave_sum(q) * (1.f / 1024.f) + LN_EPS);
; }
;     float mu, rstd; row_stats(v, mu, rstd);
; #pragma unroll
;     for (int i = 0; i < 4; ++i) { const int c = LAY ? lane * 16 + 4 * i : lane * 4 + 256 * i;
;         const f32x4 s4 = *(const f32x4*)(sc + c), h4 = *(const f32x4*)(sh + c);
;         float o[4];
; #pragma unroll
;         for (int j = 0; j < 4; ++j) o[j] = (v[i][j] - mu) * rstd * (1.f + s4[j]) + h4[j];
;         u32x2 w; w.x = cvt_pk_bf16(o[0], o[1]); w.y = cvt_pk_bf16(o[2], o[3]);
;         *(u32x2*)(hrow + c) = w; }
; }
; DEVI void write_h_reg(const f32x4 (&v)[4], const f32x4 (&sh)[4], const f32x4 (&sc)[4], bf16_t* hrow, int lane) {
;     float mu, rstd; row_stats(v, mu, rstd);
; #pragma unroll
;     for (int i = 0; i < 4; ++i) { float o[4];
; #pragma unroll
;         for (int j = 0; j < 4; ++j) o[j] = (v[i][j] - mu) * rstd * (1.f + sc[i][j]) + sh[i][j];
;         u32x2 w; w.x = cvt_pk_bf16(o[0], o[1]); w.y = cvt_pk_bf16(o[2], o[3]);
;         *(u32x2*)(hrow + lane * 4 + 256 * i) = w; }
; }
; DEVI void phase_ln_mid(const Params& p, int l) {
;     ...
;         float mu, rstd; row_stats(v, mu, rstd);
; #pragma unroll
;         for (int i = 0; i < 4; ++i) { const int c = lane * 4 + 256 * i; v[i] = (v[i] - mu) * rstd * lg4[i] + lb4[i]; st_bf4(xab + (size_t)t * 1024 + c, v[i]); }
;         write_h_reg(v, sh4, sc4, hb + (size_t)t * 1024, lane);
	v_pk_add_f32 v[100:101], v[82:83], v[100:101] op_sel_hi:[1,0] neg_lo:[0,1] neg_hi:[0,1]
	v_pk_mul_f32 v[102:103], v[102:103], v[102:103]
	v_pk_mul_f32 v[100:101], v[100:101], v[100:101]
	v_add_f32_e32 v91, v103, v91
	v_add_f32_e32 v91, v102, v91
	v_add_f32_e32 v91, v101, v91
	v_add_f32_e32 v91, v100, v91
	v_mov_b32_e32 v102, v92
	v_mov_b32_e32 v103, v88
	v_add_f32_dpp v91, v91, v91 quad_perm:[1,0,3,2] row_mask:0xf bank_mask:0xf bound_ctrl:1
	v_mov_b32_e32 v88, v93
	v_fmac_f32_e32 v85, 0xba800000, v69
	v_add_f32_dpp v91, v91, v91 quad_perm:[2,3,0,1] row_mask:0xf bank_mask:0xf bound_ctrl:1
	v_fmac_f32_e32 v98, 0xba800000, v69
	v_fmac_f32_e32 v99, 0xba800000, v69
	v_add_f32_dpp v91, v91, v91 row_half_mirror row_mask:0xf bank_mask:0xf bound_ctrl:1
	v_fmac_f32_e32 v82, 0xba800000, v69
	v_fmac_f32_e32 v83, 0xba800000, v69
	v_add_f32_dpp v91, v91, v91 row_mirror row_mask:0xf bank_mask:0xf bound_ctrl:1
	s_nop 0
	v_readlane_b32 s20, v91, 16
	v_readlane_b32 s21, v91, 48
	v_readlane_b32 s4, v91, 0
	v_readlane_b32 s5, v91, 32
	v_mov_b32_e32 v100, s20
	v_mov_b32_e32 v101, s21
	v_pk_add_f32 v[100:101], s[4:5], v[100:101]
	s_nop 0
	v_add_f32_e32 v91, v100, v101
	v_fmamk_f32 v91, v91, 0x3a800000, v1
	v_mul_f32_e32 v100, 0x4b800000, v91
	v_cmp_gt_f32_e32 vcc, s23, v91
	s_nop 1
	v_cndmask_b32_e32 v91, v91, v100, vcc
	v_rsq_f32_e32 v91, v91
	s_nop 0
	v_mul_f32_e32 v100, 0x45800000, v91
	v_cndmask_b32_e32 v100, v91, v100, vcc
	v_pk_mul_f32 v[102:103], v[102:103], v[100:101] op_sel_hi:[1,0]
	v_pk_mul_f32 v[88:89], v[88:89], v[100:101] op_sel_hi:[1,0]
	v_pk_fma_f32 v[92:93], v[2:3], v[102:103], v[18:19]
	v_pk_fma_f32 v[88:89], v[4:5], v[88:89], v[20:21]
	v_lshl_add_u64 v[102:103], s[10:11], 0, v[70:71]
	v_cvt_pk_bf16_f32 v104, v92, v93
	v_cvt_pk_bf16_f32 v105, v88, v89
	global_store_dwordx2 v[102:103], v[104:105], off
	v_mov_b32_e32 v104, v94
	v_mov_b32_e32 v105, v86
	v_mov_b32_e32 v86, v95
	v_pk_mul_f32 v[104:105], v[104:105], v[100:101] op_sel_hi:[1,0]
	v_pk_mul_f32 v[86:87], v[86:87], v[100:101] op_sel_hi:[1,0]
	v_pk_fma_f32 v[94:95], v[6:7], v[104:105], v[22:23]
	v_pk_fma_f32 v[86:87], v[8:9], v[86:87], v[24:25]
	v_cvt_pk_bf16_f32 v104, v94, v95
	v_pk_mul_f32 v[96:97], v[96:97], v[100:101] op_sel_hi:[1,0]
	v_cvt_pk_bf16_f32 v105, v86, v87
	global_store_dwordx2 v[102:103], v[104:105], off offset:512
	v_mov_b32_e32 v104, v85
	v_mov_b32_e32 v105, v84
	v_pk_mul_f32 v[84:85], v[104:105], v[100:101] op_sel_hi:[1,0]
	v_pk_fma_f32 v[96:97], v[10:11], v[96:97], v[26:27]
	v_pk_fma_f32 v[84:85], v[12:13], v[84:85], v[28:29]
	v_cvt_pk_bf16_f32 v104, v96, v97
	v_mov_b32_e32 v106, v94
	v_cvt_pk_bf16_f32 v105, v84, v85
	global_store_dwordx2 v[102:103], v[104:105], off offset:1024
	v_mov_b32_e32 v104, v99
	v_mov_b32_e32 v105, v98
	v_pk_mul_f32 v[98:99], v[104:105], v[100:101] op_sel_hi:[1,0]
	v_mov_b32_e32 v104, v83
	v_mov_b32_e32 v105, v82
	v_pk_mul_f32 v[82:83], v[104:105], v[100:101] op_sel_hi:[1,0]
	v_pk_mov_b32 v[100:101], v[92:93], v[88:89] op_sel:[1,0]
	v_mov_b32_e32 v104, v92
	v_mov_b32_e32 v105, v89
	v_pk_add_f32 v[100:101], v[100:101], v[104:105]
	v_pk_mov_b32 v[104:105], v[94:95], v[86:87] op_sel:[1,0]
	v_mov_b32_e32 v107, v87
	v_pk_add_f32 v[104:105], v[104:105], v[106:107]
	v_pk_fma_f32 v[82:83], v[16:17], v[82:83], v[32:33]
	v_pk_fma_f32 v[98:99], v[14:15], v[98:99], v[30:31]
	v_add_f32_e32 v69, v100, v101
	v_pk_add_f32 v[104:105], v[104:105], v[104:105] op_sel_hi:[0,1]
	v_add_f32_e32 v101, 0, v69
	v_add_f32_e32 v107, v96, v97
	v_add_f32_e32 v109, v84, v85
	v_mov_b32_e32 v106, v98
	v_mov_b32_e32 v108, v99
	v_mov_b32_e32 v104, v82
	v_mov_b32_e32 v100, v83
	v_pk_add_f32 v[106:107], v[106:107], v[108:109]
	v_pk_add_f32 v[100:101], v[104:105], v[100:101]
	s_nop 0
	v_pk_add_f32 v[100:101], v[106:107], v[100:101]
	s_nop 0
	v_add_f32_e32 v69, v100, v101
	s_nop 1
	v_add_f32_dpp v69, v69, v69 quad_perm:[1,0,3,2] row_mask:0xf bank_mask:0xf bound_ctrl:1
	s_nop 1
	v_add_f32_dpp v69, v69, v69 quad_perm:[2,3,0,1] row_mask:0xf bank_mask:0xf bound_ctrl:1
	s_nop 1
	v_add_f32_dpp v69, v69, v69 row_half_mirror row_mask:0xf bank_mask:0xf bound_ctrl:1
	s_nop 1
	v_add_f32_dpp v69, v69, v69 row_mirror row_mask:0xf bank_mask:0xf bound_ctrl:1
	s_nop 0
	v_readlane_b32 s20, v69, 16
	v_readlane_b32 s21, v69, 48
	v_readlane_b32 s4, v69, 0
	v_readlane_b32 s5, v69, 32
	v_mov_b32_e32 v100, s20
	v_mov_b32_e32 v101, s21
	v_pk_add_f32 v[100:101], s[4:5], v[100:101]
	s_nop 0
	v_add_f32_e32 v69, v100, v101
	v_fmac_f32_e32 v93, 0xba800000, v69
	v_fmamk_f32 v91, v69, 0xba800000, v92
	v_mul_f32_e32 v92, v93, v93
	v_fmac_f32_e32 v92, v91, v91
	v_fmamk_f32 v88, v69, 0xba800000, v88
	v_fmac_f32_e32 v92, v88, v88
	v_fmac_f32_e32 v89, 0xba800000, v69
	v_fmac_f32_e32 v92, v89, v89
	v_fmamk_f32 v94, v69, 0xba800000, v94
	v_fmac_f32_e32 v92, v94, v94
	v_fmac_f32_e32 v95, 0xba800000, v69
	v_fmac_f32_e32 v92, v95, v95
	v_fmamk_f32 v86, v69, 0xba800000, v86
	v_fmac_f32_e32 v92, v86, v86
	v_fmac_f32_e32 v87, 0xba800000, v69
	v_mul_f32_e32 v100, 0x3a800000, v69
	v_fmac_f32_e32 v92, v87, v87
	v_fmamk_f32 v96, v69, 0xba800000, v96
	v_fmac_f32_e32 v92, v96, v96
	v_fmac_f32_e32 v97, 0xba800000, v69
	v_pk_add_f32 v[84:85], v[84:85], v[100:101] op_sel_hi:[1,0] neg_lo:[0,1] neg_hi:[0,1]
	v_fmac_f32_e32 v92, v97, v97
	v_pk_mul_f32 v[104:105], v[84:85], v[84:85]
	s_nop 0
	v_add_f32_e32 v69, v104, v92
	v_add_f32_e32 v69, v105, v69
	v_pk_add_f32 v[104:105], v[98:99], v[100:101] op_sel_hi:[1,0] neg_lo:[0,1] neg_hi:[0,1]
	v_pk_add_f32 v[100:101], v[82:83], v[100:101] op_sel_hi:[1,0] neg_lo:[0,1] neg_hi:[0,1]
	v_pk_mul_f32 v[106:107], v[104:105], v[104:105]
	v_cvt_pk_bf16_f32 v98, v98, v99
	v_cvt_pk_bf16_f32 v99, v82, v83
	global_store_dwordx2 v[102:103], v[98:99], off offset:1536
	v_add_f32_e32 v69, v106, v69
	v_add_f32_e32 v69, v107, v69
	v_pk_mul_f32 v[106:107], v[100:101], v[100:101]
	s_nop 0
	v_add_f32_e32 v69, v106, v69
	v_add_f32_e32 v69, v107, v69
	s_nop 1
	v_add_f32_dpp v69, v69, v69 quad_perm:[1,0,3,2] row_mask:0xf bank_mask:0xf bound_ctrl:1
	s_nop 1
	v_add_f32_dpp v69, v69, v69 quad_perm:[2,3,0,1] row_mask:0xf bank_mask:0xf bound_ctrl:1
	s_nop 1
	v_add_f32_dpp v69, v69, v69 row_half_mirror row_mask:0xf bank_mask:0xf bound_ctrl:1
	s_nop 1
	v_add_f32_dpp v69, v69, v69 row_mirror row_mask:0xf bank_mask:0xf bound_ctrl:1
	s_nop 0
	v_readlane_b32 s20, v69, 16
	v_readlane_b32 s21, v69, 48
	v_readlane_b32 s4, v69, 0
	v_readlane_b32 s5, v69, 32
	v_mov_b32_e32 v106, s20
	v_mov_b32_e32 v107, s21
	v_pk_add_f32 v[106:107], s[4:5], v[106:107]
	s_nop 0
	v_add_f32_e32 v69, v106, v107
	v_fmamk_f32 v69, v69, 0x3a800000, v1
	v_mul_f32_e32 v92, 0x4b800000, v69
	v_cmp_gt_f32_e32 vcc, s23, v69
	s_nop 1
	v_cndmask_b32_e32 v69, v69, v92, vcc
	v_rsq_f32_e32 v69, v69
	s_waitcnt vmcnt(0)
; DEVI unsigned cvt_pk_bf16(float lo, float hi) { unsigned r; asm volatile("v_cvt_pk_bf16_f32 %0, %1, %2" : "=v"(r) : "v"(lo), "v"(hi)); return r; }
; DEVI float bflo(unsigned w) { return __uint_as_float(w << 16); }
; DEVI float bfhi(unsigned w) { return __uint_as_float(w & 0xffff0000u); }
; DEVI void st_bf4(bf16_t* p, f32x4 v) { u32x2 w; w.x = cvt_pk_bf16(v[0], v[1]); w.y = cvt_pk_bf16(v[2], v[3]); *(u32x2*)p = w; }
; DEVI void write_h_reg(const f32x4 (&v)[4], const f32x4 (&sh)[4], const f32x4 (&sc)[4], bf16_t* hrow, int lane) {
;     float mu, rstd; row_stats(v, mu, rstd);
; #pragma unroll
;     for (int i = 0; i < 4; ++i) { float o[4];
; #pragma unroll
;         for (int j = 0; j < 4; ++j) o[j] = (v[i][j] - mu) * rstd * (1.f + sc[i][j]) + sh[i][j];
;         u32x2 w; w.x = cvt_pk_bf16(o[0], o[1]); w.y = cvt_pk_bf16(o[2], o[3]);
;         *(u32x2*)(hrow + lane * 4 + 256 * i) = w; }
; }
; DEVI void phase_ln_mid(const Params& p, int l) {
;     ...
;     for (int t = gw; t < T_; t += nw) {
;         const int b = t >> 12; f32x4 v[4]; const int tn = t + nw < T_ ? t + nw : t;
; #pragma unroll
;         for (int i = 0; i < 4; ++i) { v[i] = (f32x4){bflo(rw[i].x), bfhi(rw[i].x), bflo(rw[i].y), bfhi(rw[i].y)}; rn[i] = *(const u32x2*)(xab + (size_t)tn * 1024 + lane * 4 + 256 * i); }
;         if (b != bcur) { bcur = b; const float* ad = p.ada + ((size_t)l * 8 + b) * 6144;
; #pragma unroll
;             for (int i = 0; i < 4; ++i) { sh4[i] = *(const f32x4*)(ad + 3072 + lane * 4 + 256 * i); sc4[i] = *(const f32x4*)(ad + 4096 + lane * 4 + 256 * i); } }
;         float mu, rstd; row_stats(v, mu, rstd);
; #pragma unroll
;         for (int i = 0; i < 4; ++i) { const int c = lane * 4 + 256 * i; v[i] = (v[i] - mu) * rstd * lg4[i] + lb4[i]; st_bf4(xab + (size_t)t * 1024 + c, v[i]); }
;         write_h_reg(v, sh4, sc4, hb + (size_t)t * 1024, lane);
; #pragma unroll
;         for (int i = 0; i < 4; ++i) rw[i] = rn[i];
;     }
	v_add_f32_e32 v92, 1.0, v34
	v_mul_f32_e32 v82, 0x45800000, v69
	v_cndmask_b32_e32 v69, v69, v82, vcc
	v_mul_f32_e32 v91, v91, v69
	v_fma_f32 v91, v92, v91, v38
	v_mul_f32_e32 v92, v93, v69
	v_add_f32_e32 v93, 1.0, v35
	v_fma_f32 v92, v93, v92, v39
	v_mul_f32_e32 v88, v88, v69
	v_add_f32_e32 v93, 1.0, v36
	v_fma_f32 v93, v93, v88, v40
	v_mul_f32_e32 v88, v89, v69
	v_add_f32_e32 v89, 1.0, v37
	v_fma_f32 v89, v89, v88, v41
	v_lshl_add_u64 v[82:83], s[8:9], 0, v[70:71]
	v_cvt_pk_bf16_f32 v88, v91, v92
	v_cvt_pk_bf16_f32 v89, v93, v89
	global_store_dwordx2 v[82:83], v[88:89], off
	v_mul_f32_e32 v88, v94, v69
	v_add_f32_e32 v89, 1.0, v42
	v_fma_f32 v88, v89, v88, v50
	v_mul_f32_e32 v89, v95, v69
	v_add_f32_e32 v91, 1.0, v43
	v_fma_f32 v89, v91, v89, v51
	v_mul_f32_e32 v86, v86, v69
	v_add_f32_e32 v91, 1.0, v44
	v_fma_f32 v91, v91, v86, v52
	v_mul_f32_e32 v86, v87, v69
	v_add_f32_e32 v87, 1.0, v45
	v_fma_f32 v87, v87, v86, v53
	v_cvt_pk_bf16_f32 v86, v88, v89
	v_cvt_pk_bf16_f32 v87, v91, v87
	global_store_dwordx2 v[82:83], v[86:87], off offset:512
	v_mul_f32_e32 v86, v96, v69
	v_add_f32_e32 v87, 1.0, v46
	v_fma_f32 v86, v87, v86, v58
	v_mul_f32_e32 v87, v97, v69
	v_add_f32_e32 v88, 1.0, v47
	v_fma_f32 v87, v88, v87, v59
	v_mul_f32_e32 v84, v84, v69
	v_add_f32_e32 v88, 1.0, v48
	v_fma_f32 v88, v88, v84, v60
	v_mul_f32_e32 v84, v85, v69
	v_add_f32_e32 v85, 1.0, v49
	v_fma_f32 v85, v85, v84, v61
	v_cvt_pk_bf16_f32 v84, v86, v87
	v_cvt_pk_bf16_f32 v85, v88, v85
	global_store_dwordx2 v[82:83], v[84:85], off offset:1024
	v_mul_f32_e32 v84, v104, v69
	v_add_f32_e32 v85, 1.0, v54
	v_fma_f32 v84, v85, v84, v62
	v_mul_f32_e32 v85, v105, v69
	v_add_f32_e32 v86, 1.0, v55
	v_fma_f32 v85, v86, v85, v63
	v_mul_f32_e32 v86, v100, v69
	v_add_f32_e32 v87, 1.0, v56
	v_fma_f32 v86, v87, v86, v64
	v_mul_f32_e32 v69, v101, v69
	v_add_f32_e32 v87, 1.0, v57
	v_fma_f32 v69, v87, v69, v65
	v_cvt_pk_bf16_f32 v84, v84, v85
	v_cvt_pk_bf16_f32 v85, v86, v69
	global_store_dwordx2 v[82:83], v[84:85], off offset:1536
	v_lshl_add_u64 v[70:71], v[70:71], 0, s[18:19]
	v_mov_b64_e32 v[82:83], v[80:81]
	v_mov_b64_e32 v[84:85], v[78:79]
	v_mov_b64_e32 v[86:87], v[76:77]
	v_mov_b64_e32 v[88:89], v[74:75]
	s_andn2_b64 exec, exec, s[12:13]
	s_cbranch_execz .LBB0_2649
.LBB0_2647:
	v_mov_b32_e32 v69, v68
	v_add_u32_e32 v68, s86, v69
	v_cmp_gt_i32_e32 vcc, s22, v68
	s_nop 1
	v_cndmask_b32_e32 v74, v69, v68, vcc
	v_ashrrev_i32_e32 v75, 31, v74
	v_lshlrev_b64 v[74:75], 11, v[74:75]
	v_lshl_add_u64 v[92:93], v[72:73], 0, v[74:75]
	global_load_dwordx2 v[74:75], v[92:93], off
	global_load_dwordx2 v[76:77], v[92:93], off offset:512
	global_load_dwordx2 v[78:79], v[92:93], off offset:1024
	global_load_dwordx2 v[80:81], v[92:93], off offset:1536
	v_cmp_lt_i32_e32 vcc, s2, v68
	v_ashrrev_i32_e32 v69, 12, v69
	v_cmp_ne_u32_e64 s[4:5], v69, v90
	s_or_b64 s[12:13], vcc, s[12:13]
	s_and_saveexec_b64 s[20:21], s[4:5]
	s_cbranch_execz .LBB0_2646
	s_load_dwordx2 s[4:5], s[6:7], 0x108
	v_add_u32_e32 v34, 8, v69
	v_mul_hi_i32_i24_e32 v35, 0x6000, v34
	v_mul_i32_i24_e32 v34, 0x6000, v34
	s_waitcnt lgkmcnt(0)
	v_lshl_add_u64 v[34:35], s[4:5], 0, v[34:35]
	v_lshl_add_u64 v[34:35], v[34:35], 0, v[66:67]
	v_add_co_u32_e32 v94, vcc, 0x3000, v34
	v_lshl_add_u64 v[90:91], v[34:35], 0, s[14:15]
	s_nop 0
	v_addc_co_u32_e32 v95, vcc, 0, v35, vcc
	v_add_co_u32_e32 v96, vcc, 0x4000, v34
	v_lshl_add_u64 v[92:93], v[34:35], 0, s[16:17]
	s_nop 0
	v_addc_co_u32_e32 v97, vcc, 0, v35, vcc
	global_load_dwordx4 v[38:41], v[94:95], off
	global_load_dwordx4 v[34:37], v[96:97], off
	global_load_dwordx4 v[50:53], v[90:91], off offset:1024
	global_load_dwordx4 v[58:61], v[90:91], off offset:2048
	global_load_dwordx4 v[42:45], v[92:93], off offset:1024
	global_load_dwordx4 v[62:65], v[90:91], off offset:3072
	global_load_dwordx4 v[46:49], v[92:93], off offset:2048
	global_load_dwordx4 v[54:57], v[92:93], off offset:3072
	v_mov_b32_e32 v90, v69
	s_branch .LBB0_2646

; DEVI int vtid() { return tidx() & 255; }
; DEVI int vbid() { return bidx() * 2 + vhb(); }
; DEVI int vgrid() { return (int)gridDim.x * 2; }
; DEVI void phase_combine(const Params& p, char* smem, int l) {
;     const int lane = vtid() & 63, gw = vbid() * 4 + (vtid() >> 6), nw = vgrid() * 4;
;     const MoeTab mt = moe_tables(p, smem + 61440, l, vtid());
;     float* xo = p.out; bf16_t* xob = p.xb; bf16_t* hb = p.h; const bf16_t* xab = p.xa; const unsigned char* ysl = p.yslot; const int* tke = p.tok_e; const int* tkp = p.tok_pos;
;     asm volatile("" : "+s"(xo), "+s"(xob), "+s"(hb), "+s"(xab), "+s"(ysl), "+s"(tke), "+s"(tkp));
;     size_t slot_nx = (size_t)T_ * 8 + gw;
;     if (lane < 8 && gw < T_) slot_nx = (size_t)mt.rstart[tke[gw * 8 + lane]] + tkp[gw * 8 + lane];
.LBB0_3291:
	s_or_b64 exec, exec, s[4:5]
	s_lshr_b32 s2, s2, 6
	s_and_b32 s24, s2, 0x3fffffc
	s_waitcnt lgkmcnt(0)
	s_barrier
	s_load_dwordx2 s[26:27], s[0:1], 0xf0
	s_load_dwordx4 s[4:7], s[0:1], 0x160
	s_load_dwordx2 s[2:3], s[0:1], 0x170
	s_load_dwordx4 s[8:11], s[0:1], 0x1f0
	s_load_dwordx2 s[22:23], s[0:1], 0x228
	s_lshl_b32 s16, s84, 3
	s_add_i32 s17, s24, s16
	v_and_b32_e32 v32, 63, v5
	v_bfe_u32 v33, v4, 6, 2
	s_waitcnt lgkmcnt(0)
	s_cmpk_lt_u32 s17, 0x8000
	v_or_b32_e32 v105, s17, v33
	v_cmp_gt_u32_e64 s[2:3], 8, v32
	s_cselect_b64 s[4:5], -1, 0
	v_add_u32_e32 v48, 0x40000, v105
	s_and_b64 s[14:15], s[2:3], s[4:5]
	s_and_saveexec_b64 s[12:13], s[14:15]
	s_cbranch_execz .LBB0_3293
	v_lshl_or_b32 v0, v105, 3, v32
	v_mov_b32_e32 v1, 0
	v_lshlrev_b64 v[0:1], 2, v[0:1]
	v_lshl_add_u64 v[2:3], s[8:9], 0, v[0:1]
	global_load_dword v2, v[2:3], off
	v_lshl_add_u64 v[0:1], s[10:11], 0, v[0:1]
	global_load_dword v0, v[0:1], off
	s_waitcnt vmcnt(0) lgkmcnt(0)
	v_lshl_add_u32 v1, v2, 2, s19
	ds_read_b32 v1, v1 offset:61440
	s_waitcnt lgkmcnt(0)
	v_add_u32_e32 v48, v0, v1

; DEVI void phase_combine(const Params& p, char* smem, int l) {
;     ...
; #pragma unroll
;         for (int k = 0; k < 9; ++k)
; #pragma unroll
;             for (int i = 0; i < 4; ++i) { const f32x2 lo = __builtin_amdgcn_cvt_pk_f32_fp8((int)w[k][i], false), hi = __builtin_amdgcn_cvt_pk_f32_fp8((int)w[k][i], true);
;                 f[i][0] += lo[0]; f[i][1] += lo[1]; f[i][2] += hi[0]; f[i][3] += hi[1]; }
.LBB0_3295:
	s_or_b64 exec, exec, s[4:5]
	s_waitcnt vmcnt(0) lgkmcnt(0)
	v_cvt_pk_f32_fp8_e32 v[106:107], v88
	v_cvt_pk_f32_fp8_sdwa v[108:109], v88 src0_sel:WORD_1
	v_cvt_pk_f32_fp8_e32 v[110:111], v89
	v_cvt_pk_f32_fp8_sdwa v[88:89], v89 src0_sel:WORD_1
	v_cvt_pk_f32_fp8_e32 v[118:119], v80
	v_cvt_pk_f32_fp8_sdwa v[120:121], v80 src0_sel:WORD_1
	v_cvt_pk_f32_fp8_e32 v[122:123], v81
	v_cvt_pk_f32_fp8_sdwa v[80:81], v81 src0_sel:WORD_1
	v_cvt_pk_f32_fp8_e32 v[130:131], v84
	v_cvt_pk_f32_fp8_sdwa v[132:133], v84 src0_sel:WORD_1
	v_cvt_pk_f32_fp8_e32 v[134:135], v85
	v_cvt_pk_f32_fp8_sdwa v[84:85], v85 src0_sel:WORD_1
	v_cvt_pk_f32_fp8_e32 v[142:143], v72
	v_cvt_pk_f32_fp8_sdwa v[144:145], v72 src0_sel:WORD_1
	v_cvt_pk_f32_fp8_e32 v[146:147], v73
	v_cvt_pk_f32_fp8_sdwa v[72:73], v73 src0_sel:WORD_1
	v_cvt_pk_f32_fp8_e32 v[154:155], v76
	v_cvt_pk_f32_fp8_sdwa v[156:157], v76 src0_sel:WORD_1
	v_cvt_pk_f32_fp8_e32 v[158:159], v77
	v_cvt_pk_f32_fp8_sdwa v[76:77], v77 src0_sel:WORD_1
	v_pk_add_f32 v[110:111], v[110:111], 0 op_sel_hi:[1,0]
	v_pk_add_f32 v[88:89], v[88:89], 0 op_sel_hi:[1,0]
	v_cvt_pk_f32_fp8_sdwa v[114:115], v90 src0_sel:WORD_1
	v_cvt_pk_f32_fp8_e32 v[166:167], v64
	v_cvt_pk_f32_fp8_sdwa v[168:169], v64 src0_sel:WORD_1
	v_cvt_pk_f32_fp8_e32 v[170:171], v65
	v_cvt_pk_f32_fp8_sdwa v[64:65], v65 src0_sel:WORD_1
	v_pk_add_f32 v[80:81], v[88:89], v[80:81]
	v_pk_add_f32 v[88:89], v[110:111], v[122:123]
	v_cvt_pk_f32_fp8_sdwa v[126:127], v82 src0_sel:WORD_1
	v_cvt_pk_f32_fp8_e32 v[178:179], v68
	v_cvt_pk_f32_fp8_sdwa v[180:181], v68 src0_sel:WORD_1
	v_cvt_pk_f32_fp8_e32 v[182:183], v69
	v_cvt_pk_f32_fp8_sdwa v[68:69], v69 src0_sel:WORD_1
	v_pk_add_f32 v[88:89], v[88:89], v[134:135]
	v_pk_add_f32 v[80:81], v[80:81], v[84:85]
	v_cvt_pk_f32_fp8_e32 v[112:113], v90
	v_cvt_pk_f32_fp8_sdwa v[138:139], v86 src0_sel:WORD_1
	v_cvt_pk_f32_fp8_e32 v[190:191], v60
	v_cvt_pk_f32_fp8_sdwa v[192:193], v60 src0_sel:WORD_1
	v_cvt_pk_f32_fp8_e32 v[194:195], v61
	v_cvt_pk_f32_fp8_sdwa v[60:61], v61 src0_sel:WORD_1
	v_pk_add_f32 v[72:73], v[80:81], v[72:73]
	v_pk_add_f32 v[80:81], v[88:89], v[146:147]
	v_cvt_pk_f32_fp8_e32 v[124:125], v82
	v_cvt_pk_f32_fp8_sdwa v[150:151], v74 src0_sel:WORD_1
	v_pk_add_f32 v[80:81], v[80:81], v[158:159]
	v_pk_add_f32 v[72:73], v[72:73], v[76:77]
	v_cvt_pk_f32_fp8_e32 v[136:137], v86
	v_cvt_pk_f32_fp8_sdwa v[162:163], v78 src0_sel:WORD_1
	v_pk_add_f32 v[64:65], v[72:73], v[64:65]
	v_pk_add_f32 v[72:73], v[80:81], v[170:171]
	v_pk_add_f32 v[76:77], v[114:115], 0 op_sel_hi:[1,0]
	v_cvt_pk_f32_fp8_e32 v[148:149], v74
	v_cvt_pk_f32_fp8_sdwa v[174:175], v66 src0_sel:WORD_1
	v_pk_add_f32 v[106:107], v[106:107], 0 op_sel_hi:[1,0]
	v_pk_add_f32 v[72:73], v[72:73], v[182:183]
	v_pk_add_f32 v[64:65], v[64:65], v[68:69]
	v_pk_add_f32 v[76:77], v[76:77], v[126:127]
	v_cvt_pk_f32_fp8_e32 v[116:117], v91
	v_cvt_pk_f32_fp8_sdwa v[90:91], v91 src0_sel:WORD_1
	v_cvt_pk_f32_fp8_e32 v[160:161], v78
	v_cvt_pk_f32_fp8_sdwa v[186:187], v70 src0_sel:WORD_1
	v_cvt_pk_f32_fp8_e32 v[202:203], v56
	v_cvt_pk_f32_fp8_sdwa v[204:205], v56 src0_sel:WORD_1
	v_pk_add_f32 v[106:107], v[106:107], v[118:119]
	v_cvt_pk_f32_fp8_e32 v[118:119], v57
	v_cvt_pk_f32_fp8_sdwa v[56:57], v57 src0_sel:WORD_1
	v_pk_add_f32 v[60:61], v[64:65], v[60:61]
	v_pk_add_f32 v[64:65], v[72:73], v[194:195]
	v_pk_add_f32 v[72:73], v[112:113], 0 op_sel_hi:[1,0]
	v_pk_add_f32 v[76:77], v[76:77], v[138:139]
	v_cvt_pk_f32_fp8_e32 v[128:129], v83
	v_cvt_pk_f32_fp8_sdwa v[82:83], v83 src0_sel:WORD_1
	v_cvt_pk_f32_fp8_e32 v[172:173], v66
	v_cvt_pk_f32_fp8_sdwa v[198:199], v62 src0_sel:WORD_1
	v_pk_add_f32 v[72:73], v[72:73], v[124:125]
	v_pk_add_f32 v[76:77], v[76:77], v[150:151]
	v_cvt_pk_f32_fp8_e32 v[140:141], v87
	v_cvt_pk_f32_fp8_sdwa v[86:87], v87 src0_sel:WORD_1
	v_cvt_pk_f32_fp8_e32 v[184:185], v70
	v_pk_add_f32 v[108:109], v[108:109], 0 op_sel_hi:[1,0]
	v_cvt_pk_f32_fp8_sdwa v[68:69], v58 src0_sel:WORD_1
	v_pk_add_f32 v[72:73], v[72:73], v[136:137]
	v_pk_add_f32 v[76:77], v[76:77], v[162:163]
	v_cvt_pk_f32_fp8_e32 v[152:153], v75
	v_cvt_pk_f32_fp8_sdwa v[74:75], v75 src0_sel:WORD_1
	v_cvt_pk_f32_fp8_e32 v[196:197], v62
	v_pk_add_f32 v[108:109], v[108:109], v[120:121]
	v_pk_add_f32 v[72:73], v[72:73], v[148:149]
	v_pk_add_f32 v[76:77], v[76:77], v[174:175]
	v_cvt_pk_f32_fp8_e32 v[164:165], v79
	v_cvt_pk_f32_fp8_sdwa v[78:79], v79 src0_sel:WORD_1
	v_pk_add_f32 v[108:109], v[108:109], v[132:133]
	v_pk_add_f32 v[56:57], v[60:61], v[56:57]
	v_cvt_pk_f32_fp8_e32 v[60:61], v58
	v_pk_add_f32 v[72:73], v[72:73], v[160:161]
	v_pk_add_f32 v[76:77], v[76:77], v[186:187]
	v_pk_add_f32 v[80:81], v[90:91], 0 op_sel_hi:[1,0]
	v_cvt_pk_f32_fp8_e32 v[176:177], v67
	v_cvt_pk_f32_fp8_sdwa v[66:67], v67 src0_sel:WORD_1
	v_pk_add_f32 v[108:109], v[108:109], v[144:145]
	v_pk_add_f32 v[72:73], v[72:73], v[172:173]
	v_pk_add_f32 v[76:77], v[76:77], v[198:199]
	v_pk_add_f32 v[80:81], v[80:81], v[82:83]
	v_cvt_pk_f32_fp8_e32 v[188:189], v71
	v_cvt_pk_f32_fp8_sdwa v[70:71], v71 src0_sel:WORD_1
	v_pk_add_f32 v[108:109], v[108:109], v[156:157]
	v_pk_add_f32 v[72:73], v[72:73], v[184:185]
	v_pk_add_f32 v[68:69], v[76:77], v[68:69]
	v_pk_add_f32 v[76:77], v[116:117], 0 op_sel_hi:[1,0]
	v_pk_add_f32 v[80:81], v[80:81], v[86:87]
	v_cvt_pk_f32_fp8_e32 v[200:201], v63
	v_cvt_pk_f32_fp8_sdwa v[62:63], v63 src0_sel:WORD_1
	v_pk_add_f32 v[106:107], v[106:107], v[130:131]
	v_pk_add_f32 v[108:109], v[108:109], v[168:169]
	v_pk_add_f32 v[72:73], v[72:73], v[196:197]
	v_pk_add_f32 v[76:77], v[76:77], v[128:129]
	v_pk_add_f32 v[74:75], v[80:81], v[74:75]
	v_pk_add_f32 v[106:107], v[106:107], v[142:143]
; DEVI float bflo(unsigned w) { return __uint_as_float(w << 16); }
; DEVI float bfhi(unsigned w) { return __uint_as_float(w & 0xffff0000u); }
; DEVI void phase_combine(const Params& p, char* smem, int l) {
;     ...
; #pragma unroll
;         for (int k = 0; k < 9; ++k)
; #pragma unroll
;             for (int i = 0; i < 4; ++i) { const f32x2 lo = __builtin_amdgcn_cvt_pk_f32_fp8((int)w[k][i], false), hi = __builtin_amdgcn_cvt_pk_f32_fp8((int)w[k][i], true);
;                 f[i][0] += lo[0]; f[i][1] += lo[1]; f[i][2] += hi[0]; f[i][3] += hi[1]; }
;         f32x4 v[4];
; #pragma unroll
;         for (int i = 0; i < 4; ++i) { const unsigned x0 = i < 2 ? xr0[2 * i] : xr1[2 * i - 4], x1 = i < 2 ? xr0[2 * i + 1] : xr1[2 * i - 3];
;             v[i] = (f32x4){bflo(x0), bfhi(x0), bflo(x1), bfhi(x1)} * ALPHA + gate4[i] * (f[i] * (1.f / YS_SCALE)); }
;         float mu, rstd; row_stats(v, mu, rstd);
; #pragma unroll
;         for (int i = 0; i < 4; ++i) v[i] = (v[i] - mu) * rstd * lg4[i] + lb4[i];
	v_pk_add_f32 v[108:109], v[108:109], v[180:181]
	v_pk_add_f32 v[60:61], v[72:73], v[60:61]
	v_cvt_pk_f32_fp8_e32 v[72:73], v59
	v_cvt_pk_f32_fp8_sdwa v[58:59], v59 src0_sel:WORD_1
	v_pk_add_f32 v[76:77], v[76:77], v[140:141]
	v_pk_add_f32 v[74:75], v[74:75], v[78:79]
	v_pk_add_f32 v[106:107], v[106:107], v[154:155]
	v_pk_add_f32 v[108:109], v[108:109], v[192:193]
	v_pk_add_f32 v[76:77], v[76:77], v[152:153]
	v_pk_add_f32 v[66:67], v[74:75], v[66:67]
	v_pk_add_f32 v[106:107], v[106:107], v[166:167]
	v_pk_add_f32 v[108:109], v[108:109], v[204:205]
	v_pk_add_f32 v[76:77], v[76:77], v[164:165]
	v_pk_add_f32 v[66:67], v[66:67], v[70:71]
	v_pk_add_f32 v[106:107], v[106:107], v[178:179]
	v_pk_add_f32 v[64:65], v[64:65], v[118:119]
	v_pk_add_f32 v[74:75], v[76:77], v[176:177]
	v_pk_add_f32 v[62:63], v[66:67], v[62:63]
	v_pk_mul_f32 v[70:71], v[108:109], s[18:19] op_sel_hi:[1,0]
	v_pk_add_f32 v[106:107], v[106:107], v[190:191]
	v_pk_add_f32 v[74:75], v[74:75], v[188:189]
	v_pk_add_f32 v[58:59], v[62:63], v[58:59]
	v_lshlrev_b32_e32 v62, 16, v52
	v_and_b32_e32 v63, 0xffff0000, v52
	v_lshlrev_b32_e32 v52, 16, v53
	v_and_b32_e32 v53, 0xffff0000, v53
	v_pk_mul_f32 v[70:71], v[34:35], v[70:71]
	v_pk_mul_f32 v[56:57], v[56:57], s[18:19] op_sel_hi:[1,0]
	v_pk_mul_f32 v[64:65], v[64:65], s[18:19] op_sel_hi:[1,0]
	v_pk_add_f32 v[106:107], v[106:107], v[202:203]
	v_pk_add_f32 v[66:67], v[74:75], v[200:201]
	v_pk_fma_f32 v[52:53], v[52:53], s[20:21], v[70:71] op_sel_hi:[1,0,1]
	v_lshlrev_b32_e32 v70, 16, v54
	v_and_b32_e32 v71, 0xffff0000, v54
	v_lshlrev_b32_e32 v54, 16, v55
	v_and_b32_e32 v55, 0xffff0000, v55
	v_pk_mul_f32 v[64:65], v[36:37], v[64:65]
	v_pk_mul_f32 v[56:57], v[38:39], v[56:57]
	v_pk_mul_f32 v[60:61], v[60:61], s[18:19] op_sel_hi:[1,0]
	v_pk_add_f32 v[66:67], v[66:67], v[72:73]
	v_pk_mul_f32 v[72:73], v[106:107], s[18:19] op_sel_hi:[1,0]
	v_pk_fma_f32 v[54:55], v[54:55], s[20:21], v[56:57] op_sel_hi:[1,0,1]
	v_pk_fma_f32 v[56:57], v[70:71], s[20:21], v[64:65] op_sel_hi:[1,0,1]
	v_lshlrev_b32_e32 v64, 16, v48
	v_and_b32_e32 v65, 0xffff0000, v48
	v_pk_mul_f32 v[68:69], v[68:69], s[18:19] op_sel_hi:[1,0]
	v_pk_mul_f32 v[60:61], v[40:41], v[60:61]
	v_pk_mul_f32 v[72:73], v[32:33], v[72:73]
	v_lshlrev_b32_e32 v48, 16, v49
	v_and_b32_e32 v49, 0xffff0000, v49
	v_pk_mul_f32 v[68:69], v[42:43], v[68:69]
	v_pk_fma_f32 v[60:61], v[64:65], s[20:21], v[60:61] op_sel_hi:[1,0,1]
	v_pk_mul_f32 v[58:59], v[58:59], s[18:19] op_sel_hi:[1,0]
	v_pk_mul_f32 v[64:65], v[66:67], s[18:19] op_sel_hi:[1,0]
	v_pk_fma_f32 v[62:63], v[62:63], s[20:21], v[72:73] op_sel_hi:[1,0,1]
	v_pk_fma_f32 v[68:69], v[48:49], s[20:21], v[68:69] op_sel_hi:[1,0,1]
	v_lshlrev_b32_e32 v48, 16, v50
	v_and_b32_e32 v49, 0xffff0000, v50
	v_lshlrev_b32_e32 v50, 16, v51
	v_and_b32_e32 v51, 0xffff0000, v51
	v_pk_mul_f32 v[64:65], v[44:45], v[64:65]
	v_pk_mul_f32 v[58:59], v[46:47], v[58:59]
	v_pk_fma_f32 v[64:65], v[48:49], s[20:21], v[64:65] op_sel_hi:[1,0,1]
	v_pk_fma_f32 v[66:67], v[50:51], s[20:21], v[58:59] op_sel_hi:[1,0,1]
	v_pk_mov_b32 v[48:49], v[62:63], v[52:53] op_sel:[1,0]
	v_mov_b32_e32 v50, v62
	v_mov_b32_e32 v51, v53
	v_pk_add_f32 v[48:49], v[48:49], v[50:51]
	v_pk_mov_b32 v[50:51], v[56:57], v[54:55] op_sel:[1,0]
	v_mov_b32_e32 v58, v56
	v_mov_b32_e32 v59, v55
	v_pk_add_f32 v[50:51], v[50:51], v[58:59]
	v_add_f32_e32 v48, v48, v49
	v_pk_add_f32 v[50:51], v[50:51], v[50:51] op_sel:[0,1] op_sel_hi:[1,0]
	v_add_f32_e32 v48, 0, v48
	v_add_f32_e32 v58, v60, v61
	v_add_f32_e32 v70, v68, v69
	v_mov_b32_e32 v49, v64
	v_mov_b32_e32 v51, v65
	v_mov_b32_e32 v59, v66
	v_mov_b32_e32 v71, v67
	v_pk_add_f32 v[48:49], v[48:49], v[50:51]
	v_pk_add_f32 v[50:51], v[58:59], v[70:71]
	v_add_u32_e32 v96, s21, v96
	v_pk_add_f32 v[48:49], v[48:49], v[50:51]
	v_lshl_add_u64 v[100:101], v[100:101], 0, s[24:25]
	v_add_f32_e32 v48, v48, v49
	v_mov_b32_e32 v105, v104
	s_nop 0
	v_add_f32_dpp v48, v48, v48 quad_perm:[1,0,3,2] row_mask:0xf bank_mask:0xf bound_ctrl:1
	s_nop 1
	v_add_f32_dpp v48, v48, v48 quad_perm:[2,3,0,1] row_mask:0xf bank_mask:0xf bound_ctrl:1
	s_nop 1
	v_add_f32_dpp v48, v48, v48 row_half_mirror row_mask:0xf bank_mask:0xf bound_ctrl:1
	s_nop 1
	v_add_f32_dpp v48, v48, v48 row_mirror row_mask:0xf bank_mask:0xf bound_ctrl:1
	s_nop 0
	v_readlane_b32 s6, v48, 16
	v_readlane_b32 s7, v48, 48
	v_readlane_b32 s4, v48, 0
	v_readlane_b32 s5, v48, 32
	v_mov_b32_e32 v48, s6
	v_mov_b32_e32 v49, s7
	v_pk_add_f32 v[48:49], s[4:5], v[48:49]
	s_nop 0
	v_add_f32_e32 v71, v48, v49
	v_fmamk_f32 v63, v71, 0xba800000, v63
	v_mul_f32_e32 v49, v63, v63
	v_fmac_f32_e32 v62, 0xba800000, v71
	v_fmac_f32_e32 v49, v62, v62
	v_fmamk_f32 v52, v71, 0xba800000, v52
	v_fmac_f32_e32 v49, v52, v52
	v_fmac_f32_e32 v53, 0xba800000, v71
	v_fmac_f32_e32 v49, v53, v53
	v_fmamk_f32 v56, v71, 0xba800000, v56
	v_fmac_f32_e32 v49, v56, v56
	v_fmac_f32_e32 v57, 0xba800000, v71
	v_fmac_f32_e32 v49, v57, v57
	v_fmamk_f32 v54, v71, 0xba800000, v54
	v_fmac_f32_e32 v49, v54, v54
	v_fmac_f32_e32 v55, 0xba800000, v71
	v_fmac_f32_e32 v49, v55, v55
	v_fmamk_f32 v60, v71, 0xba800000, v60
	v_fmac_f32_e32 v49, v60, v60
	v_fmac_f32_e32 v61, 0xba800000, v71
	v_mul_f32_e32 v48, 0x3a800000, v71
; DEVI float bflo(unsigned w) { return __uint_as_float(w << 16); }
; DEVI float bfhi(unsigned w) { return __uint_as_float(w & 0xffff0000u); }
; DEVI void phase_combine(const Params& p, char* smem, int l) {
;     ...
;     for (int t = gw; t < T_; t += nw) {
;         const int b = t >> 12;
;         const size_t slot = slot_nx;
;         { const int tn = t + nw; slot_nx = (size_t)T_ * 8 + tn;
;           if (lane < 8 && tn < T_) slot_nx = (size_t)mt.rstart[tke[tn * 8 + lane]] + tkp[tn * 8 + lane]; }
;         u32x4 w[9];
; #pragma unroll
;         for (int k = 0; k < 9; ++k) { const size_t sl = (size_t)(unsigned)__builtin_amdgcn_readlane((int)(unsigned)slot, k);
;             w[k] = *(const u32x4*)(ysl + sl * 1024 + lane * 16); }
;         const u32x4 xr0 = *(const u32x4*)(xab + (size_t)t * 1024 + lane * 16), xr1 = *(const u32x4*)(xab + (size_t)t * 1024 + lane * 16 + 8);
;         if (b != bcur) { bcur = b; const float* ad = p.ada + ((size_t)l * 8 + b) * 6144; const float* ad2 = p.ada + ((size_t)(l + 1 < NL_ ? l + 1 : l) * 8 + b) * 6144;
; #pragma unroll
;             for (int i = 0; i < 4; ++i) { const int c = lane * 16 + 4 * i; gate4[i] = *(const f32x4*)(ad + 5120 + c); sh4[i] = *(const f32x4*)(ad2 + c); sc4[i] = *(const f32x4*)(ad2 + 1024 + c); } }
;         f32x4 f[4];
; #pragma unroll
;         for (int i = 0; i < 4; ++i) f[i] = (f32x4){0.f, 0.f, 0.f, 0.f};
; #pragma unroll
;         for (int k = 0; k < 9; ++k)
; #pragma unroll
;             for (int i = 0; i < 4; ++i) { const f32x2 lo = __builtin_amdgcn_cvt_pk_f32_fp8((int)w[k][i], false), hi = __builtin_amdgcn_cvt_pk_f32_fp8((int)w[k][i], true);
;                 f[i][0] += lo[0]; f[i][1] += lo[1]; f[i][2] += hi[0]; f[i][3] += hi[1]; }
;         f32x4 v[4];
; #pragma unroll
;         for (int i = 0; i < 4; ++i) { const unsigned x0 = i < 2 ? xr0[2 * i] : xr1[2 * i - 4], x1 = i < 2 ? xr0[2 * i + 1] : xr1[2 * i - 3];
;             v[i] = (f32x4){bflo(x0), bfhi(x0), bflo(x1), bfhi(x1)} * ALPHA + gate4[i] * (f[i] * (1.f / YS_SCALE)); }
;         float mu, rstd; row_stats(v, mu, rstd);
; #pragma unroll
;         for (int i = 0; i < 4; ++i) v[i] = (v[i] - mu) * rstd * lg4[i] + lb4[i];
;         if (l == NL_ - 1) {
; #pragma unroll
;             for (int i = 0; i < 4; ++i) *(f32x4*)(xo + (size_t)t * 1024 + lane * 16 + 4 * i) = v[i];
	v_fmac_f32_e32 v49, v61, v61
	v_pk_add_f32 v[50:51], v[68:69], v[48:49] op_sel_hi:[1,0] neg_lo:[0,1] neg_hi:[0,1]
	v_fmamk_f32 v69, v71, 0xba800000, v69
	v_pk_mul_f32 v[50:51], v[50:51], v[50:51]
	v_fmac_f32_e32 v68, 0xba800000, v71
	v_add_f32_e32 v49, v50, v49
	v_add_f32_e32 v49, v51, v49
	v_pk_add_f32 v[50:51], v[64:65], v[48:49] op_sel_hi:[1,0] neg_lo:[0,1] neg_hi:[0,1]
	v_fmamk_f32 v65, v71, 0xba800000, v65
	v_pk_mul_f32 v[50:51], v[50:51], v[50:51]
	v_fmac_f32_e32 v64, 0xba800000, v71
	v_add_f32_e32 v49, v50, v49
	v_add_f32_e32 v50, v51, v49
	v_pk_add_f32 v[48:49], v[66:67], v[48:49] op_sel_hi:[1,0] neg_lo:[0,1] neg_hi:[0,1]
	v_fmamk_f32 v67, v71, 0xba800000, v67
	v_pk_mul_f32 v[48:49], v[48:49], v[48:49]
	v_fmac_f32_e32 v66, 0xba800000, v71
	v_add_f32_e32 v48, v48, v50
	v_add_f32_e32 v48, v49, v48
	s_nop 1
	v_add_f32_dpp v48, v48, v48 quad_perm:[1,0,3,2] row_mask:0xf bank_mask:0xf bound_ctrl:1
	s_nop 1
	v_add_f32_dpp v48, v48, v48 quad_perm:[2,3,0,1] row_mask:0xf bank_mask:0xf bound_ctrl:1
	s_nop 1
	v_add_f32_dpp v48, v48, v48 row_half_mirror row_mask:0xf bank_mask:0xf bound_ctrl:1
	s_nop 1
	v_add_f32_dpp v48, v48, v48 row_mirror row_mask:0xf bank_mask:0xf bound_ctrl:1
	s_nop 0
	v_readlane_b32 s6, v48, 16
	v_readlane_b32 s7, v48, 48
	v_readlane_b32 s4, v48, 0
	v_readlane_b32 s5, v48, 32
	v_mov_b32_e32 v48, s6
	v_mov_b32_e32 v49, s7
	v_pk_add_f32 v[48:49], s[4:5], v[48:49]
	s_nop 0
	v_add_f32_e32 v48, v48, v49
	v_fmamk_f32 v48, v48, 0x3a800000, v102
	v_mul_f32_e32 v49, 0x4b800000, v48
	v_cmp_gt_f32_e32 vcc, s30, v48
	s_nop 1
	v_cndmask_b32_e32 v48, v48, v49, vcc
	v_rsq_f32_e32 v48, v48
	s_nop 0
	v_mul_f32_e32 v49, 0x45800000, v48
	v_cndmask_b32_e32 v70, v48, v49, vcc
	v_pk_mul_f32 v[48:49], v[62:63], v[70:71] op_sel_hi:[1,0]
	v_pk_mul_f32 v[50:51], v[52:53], v[70:71] op_sel_hi:[1,0]
	v_pk_fma_f32 v[48:49], v[0:1], v[48:49], v[16:17]
	v_pk_fma_f32 v[50:51], v[2:3], v[50:51], v[18:19]
	v_pk_mul_f32 v[52:53], v[56:57], v[70:71] op_sel_hi:[1,0]
	v_pk_mul_f32 v[54:55], v[54:55], v[70:71] op_sel_hi:[1,0]
	v_pk_mul_f32 v[56:57], v[60:61], v[70:71] op_sel_hi:[1,0]
	v_pk_mul_f32 v[58:59], v[68:69], v[70:71] op_sel_hi:[1,0]
	v_pk_mul_f32 v[60:61], v[64:65], v[70:71] op_sel_hi:[1,0]
	v_pk_mul_f32 v[62:63], v[66:67], v[70:71] op_sel_hi:[1,0]
	v_pk_fma_f32 v[54:55], v[14:15], v[54:55], v[30:31]
	v_pk_fma_f32 v[52:53], v[12:13], v[52:53], v[28:29]
	v_pk_fma_f32 v[58:59], v[10:11], v[58:59], v[26:27]
	v_pk_fma_f32 v[56:57], v[8:9], v[56:57], v[24:25]
	v_pk_fma_f32 v[62:63], v[6:7], v[62:63], v[22:23]
	v_pk_fma_f32 v[60:61], v[4:5], v[60:61], v[20:21]
	global_store_dwordx4 v[98:99], v[48:51], off
	global_store_dwordx4 v[98:99], v[52:55], off offset:16
	global_store_dwordx4 v[98:99], v[56:59], off offset:32
	global_store_dwordx4 v[98:99], v[60:63], off offset:48
	v_lshl_add_u64 v[98:99], v[98:99], 0, s[22:23]
	v_mov_b32_e32 v48, v97
	s_andn2_b64 exec, exec, s[14:15]
	s_cbranch_execz .LBB0_3300
.LBB0_3296:
	v_add_u32_e32 v104, s86, v105
	v_cmp_gt_i32_e64 s[4:5], s29, v104
	v_add_u32_e32 v97, 0x40000, v104
	v_cmp_lt_i32_e32 vcc, s28, v104
	s_and_b64 s[6:7], s[2:3], s[4:5]
	s_and_b64 s[4:5], exec, vcc
	s_or_b64 s[14:15], s[4:5], s[14:15]
	v_readlane_b32 s12, v48, 0
	s_lshl_b64 s[4:5], s[12:13], 10
	v_readlane_b32 s12, v48, 1
	v_lshl_add_u64 v[50:51], v[94:95], 0, s[4:5]
	s_lshl_b64 s[4:5], s[12:13], 10
	v_readlane_b32 s12, v48, 2
	v_lshl_add_u64 v[52:53], v[94:95], 0, s[4:5]
	s_lshl_b64 s[4:5], s[12:13], 10
	v_readlane_b32 s12, v48, 3
	global_load_dwordx4 v[88:91], v[50:51], off
	global_load_dwordx4 v[80:83], v[52:53], off
	v_lshl_add_u64 v[50:51], v[94:95], 0, s[4:5]
	s_lshl_b64 s[4:5], s[12:13], 10
	v_readlane_b32 s12, v48, 4
	v_lshl_add_u64 v[52:53], v[94:95], 0, s[4:5]
	s_lshl_b64 s[4:5], s[12:13], 10
	v_readlane_b32 s12, v48, 5
	global_load_dwordx4 v[84:87], v[50:51], off
	global_load_dwordx4 v[72:75], v[52:53], off
	v_lshl_add_u64 v[50:51], v[94:95], 0, s[4:5]
	s_lshl_b64 s[4:5], s[12:13], 10
	v_readlane_b32 s12, v48, 6
	v_lshl_add_u64 v[52:53], v[94:95], 0, s[4:5]
	s_lshl_b64 s[4:5], s[12:13], 10
	v_readlane_b32 s12, v48, 7
	global_load_dwordx4 v[76:79], v[50:51], off
	global_load_dwordx4 v[64:67], v[52:53], off
	v_lshl_add_u64 v[50:51], v[94:95], 0, s[4:5]
	s_lshl_b64 s[4:5], s[12:13], 10
	v_readlane_b32 s12, v48, 8
	v_lshl_add_u64 v[52:53], v[94:95], 0, s[4:5]
	s_lshl_b64 s[4:5], s[12:13], 10
	v_lshl_add_u64 v[106:107], v[94:95], 0, s[4:5]
	global_load_dwordx4 v[68:71], v[50:51], off
	global_load_dwordx4 v[60:63], v[52:53], off
	global_load_dwordx4 v[56:59], v[106:107], off
	s_nop 0
	global_load_dwordx4 v[52:55], v[100:101], off
	global_load_dwordx4 v[48:51], v[100:101], off offset:16
	s_and_saveexec_b64 s[4:5], s[6:7]
	s_cbranch_execz .Lmy_cmb_skip_b
	v_ashrrev_i32_e32 v97, 31, v96
	v_lshlrev_b64 v[250:251], 2, v[96:97]
	v_lshl_add_u64 v[252:253], s[8:9], 0, v[250:251]
	global_load_dword v254, v[252:253], off
	v_lshl_add_u64 v[250:251], s[10:11], 0, v[250:251]
	global_load_dword v255, v[250:251], off
	s_waitcnt vmcnt(0) lgkmcnt(0)
	v_lshl_add_u32 v254, v254, 2, s19
	ds_read_b32 v254, v254 offset:61440
	s_waitcnt lgkmcnt(0)
	v_add_u32_e32 v97, v255, v254
